# wave reductions: DPP move + add fused into v_add_f32_dpp (one VALU slot less per butterfly step, 204 sites)
# speedup vs baseline: 1.0209x; 1.0016x over previous
.LBB0_86:
	global_load_dwordx4 v[18:21], v13, s[10:11]
	global_load_dwordx4 v[128:131], v13, s[10:11] offset:1024
	global_load_dwordx4 v[132:135], v13, s[10:11] offset:2048
	global_load_dwordx4 v[136:139], v13, s[10:11] offset:3072
	s_lshl_b64 s[12:13], s[12:13], 11
	v_lshl_add_u64 v[34:35], v[2:3], 0, s[12:13]
	s_ashr_i32 s2, s0, 31
	s_lshr_b32 s2, s2, 20
	s_add_i32 s2, s0, s2
	s_ashr_i32 s2, s2, 12
	s_and_b64 s[8:9], exec, s[8:9]
	s_cselect_b32 s2, s2, 4
	s_mul_hi_i32 s9, s2, 0x6000
	s_mulk_i32 s2, 0x6000
	s_add_u32 s8, s14, s2
	s_addc_u32 s9, s15, s9
	s_waitcnt vmcnt(3)
	v_cvt_pk_bf16_f32 v22, v18, v19
	v_cvt_pk_bf16_f32 v23, v20, v21
	global_store_dwordx2 v[34:35], v[22:23], off
	s_waitcnt vmcnt(3)
	v_mov_b64_e32 v[22:23], v[128:129]
	v_mov_b64_e32 v[24:25], v[130:131]
	v_pk_mul_f32 v[46:47], v[20:21], v[20:21]
	v_pk_mul_f32 v[48:49], v[18:19], v[18:19]
	s_nop 0
	v_cvt_pk_bf16_f32 v26, v22, v23
	v_cvt_pk_bf16_f32 v27, v24, v25
	global_store_dwordx2 v[34:35], v[26:27], off offset:512
	s_waitcnt vmcnt(3)
	v_mov_b64_e32 v[26:27], v[132:133]
	v_mov_b64_e32 v[28:29], v[134:135]
	v_pk_mov_b32 v[50:51], v[48:49], v[46:47] op_sel:[1,0]
	v_mov_b32_e32 v49, v47
	v_pk_add_f32 v[46:47], v[50:51], v[48:49]
	v_pk_mul_f32 v[48:49], v[24:25], v[24:25]
	v_pk_mul_f32 v[50:51], v[22:23], v[22:23]
	v_pk_add_f32 v[46:47], v[46:47], v[46:47] op_sel:[0,1] op_sel_hi:[1,0]
	v_pk_mov_b32 v[52:53], v[50:51], v[48:49] op_sel:[1,0]
	v_mov_b32_e32 v51, v49
	v_pk_add_f32 v[48:49], v[52:53], v[50:51]
	s_nop 0
	v_cvt_pk_bf16_f32 v30, v26, v27
	v_cvt_pk_bf16_f32 v31, v28, v29
	global_store_dwordx2 v[34:35], v[30:31], off offset:1024
	s_waitcnt vmcnt(3)
	v_mov_b64_e32 v[30:31], v[136:137]
	v_mov_b64_e32 v[32:33], v[138:139]
	s_add_u32 s10, s8, 0x1000
	s_addc_u32 s11, s9, 0
	v_mul_f32_e32 v50, v27, v27
	v_mul_f32_e32 v52, v29, v29
	v_pk_add_f32 v[48:49], v[48:49], v[48:49] op_sel:[0,1] op_sel_hi:[1,0]
	v_pk_fma_f32 v[50:51], v[26:27], v[26:27], v[50:51] op_sel_hi:[1,1,0]
	v_pk_fma_f32 v[52:53], v[28:29], v[28:29], v[52:53] op_sel_hi:[1,1,0]
	s_add_u32 s0, s0, s28
	s_addc_u32 s1, s1, s29
	s_add_u32 s4, s4, s6
	s_addc_u32 s5, s5, s7
	s_cmpk_lt_i32 s0, 0x4400
	s_nop 0
	v_cvt_pk_bf16_f32 v36, v30, v31
	v_cvt_pk_bf16_f32 v37, v32, v33
	global_store_dwordx2 v[34:35], v[36:37], off offset:1536
	global_load_dwordx4 v[34:37], v[4:5], off
	s_nop 0
	global_load_dwordx4 v[38:41], v13, s[10:11]
	global_load_dwordx4 v[42:45], v13, s[8:9]
	global_load_dwordx4 v[140:143], v[4:5], off offset:1024
	global_load_dwordx4 v[144:147], v15, s[10:11]
	global_load_dwordx4 v[148:151], v13, s[8:9] offset:1024
	global_load_dwordx4 v[152:155], v[4:5], off offset:2048
	global_load_dwordx4 v[156:159], v16, s[10:11]
	global_load_dwordx4 v[160:163], v13, s[8:9] offset:2048
	global_load_dwordx4 v[176:179], v[4:5], off offset:3072
	global_load_dwordx4 v[180:183], v17, s[10:11]
	global_load_dwordx4 v[184:187], v13, s[8:9] offset:3072
	v_mul_f32_e32 v47, v30, v30
	v_mul_f32_e32 v49, v31, v31
	v_mul_f32_e32 v51, v32, v32
	v_mul_f32_e32 v53, v33, v33
	v_pk_add_f32 v[46:47], v[46:47], v[48:49]
	v_pk_add_f32 v[48:49], v[50:51], v[52:53]
	s_nop 0
	v_pk_add_f32 v[46:47], v[46:47], v[48:49]
	v_lshl_add_u64 v[48:49], v[6:7], 0, s[12:13]
	v_add_f32_e32 v46, v46, v47
	s_nop 1
	s_waitcnt lgkmcnt(0)
	v_add_f32_dpp v46, v46, v46 quad_perm:[1,0,3,2] row_mask:0xf bank_mask:0xf
	s_nop 1
	s_waitcnt lgkmcnt(0)
	v_add_f32_dpp v46, v46, v46 quad_perm:[2,3,0,1] row_mask:0xf bank_mask:0xf
	s_nop 1
	s_waitcnt lgkmcnt(0)
	v_add_f32_dpp v46, v46, v46 row_half_mirror row_mask:0xf bank_mask:0xf
	s_nop 1
	s_waitcnt lgkmcnt(0)
	v_add_f32_dpp v46, v46, v46 row_mirror row_mask:0xf bank_mask:0xf
	v_mov_b32_e32 v47, v46
	s_nop 1
	v_permlane16_swap_b32_e32 v47, v46
	s_waitcnt lgkmcnt(0)
	v_add_f32_e32 v46, v46, v47
	ds_bpermute_b32 v47, v12, v46
	s_waitcnt lgkmcnt(0)
	v_add_f32_e32 v46, v46, v47
	v_fmamk_f32 v46, v46, 0x3a800000, v14
	v_rsq_f32_e32 v46, v46
	s_nop 0
	v_pk_mul_f32 v[20:21], v[20:21], v[46:47] op_sel_hi:[1,0]
	v_pk_mul_f32 v[18:19], v[18:19], v[46:47] op_sel_hi:[1,0]
	v_pk_mul_f32 v[24:25], v[24:25], v[46:47] op_sel_hi:[1,0]
	v_pk_mul_f32 v[22:23], v[22:23], v[46:47] op_sel_hi:[1,0]
	v_pk_mul_f32 v[28:29], v[28:29], v[46:47] op_sel_hi:[1,0]
	v_pk_mul_f32 v[26:27], v[26:27], v[46:47] op_sel_hi:[1,0]
	v_pk_mul_f32 v[32:33], v[32:33], v[46:47] op_sel_hi:[1,0]
	v_pk_mul_f32 v[30:31], v[30:31], v[46:47] op_sel_hi:[1,0]
	s_waitcnt vmcnt(11)
	v_pk_mul_f32 v[18:19], v[34:35], v[18:19]
	v_pk_mul_f32 v[20:21], v[36:37], v[20:21]
	s_waitcnt vmcnt(10)
	v_pk_add_f32 v[34:35], v[40:41], 1.0 op_sel_hi:[1,0]
	v_pk_add_f32 v[36:37], v[38:39], 1.0 op_sel_hi:[1,0]
	s_waitcnt vmcnt(9)
	v_pk_fma_f32 v[20:21], v[34:35], v[20:21], v[44:45]
	v_pk_fma_f32 v[18:19], v[36:37], v[18:19], v[42:43]
	s_nop 0
	v_cvt_pk_bf16_f32 v18, v18, v19
	v_cvt_pk_bf16_f32 v19, v20, v21
	global_store_dwordx2 v[48:49], v[18:19], off
	s_waitcnt vmcnt(7)
	v_mov_b64_e32 v[18:19], v[140:141]
	v_mov_b64_e32 v[20:21], v[142:143]
	v_mov_b64_e32 v[34:35], v[144:145]
	v_mov_b64_e32 v[36:37], v[146:147]
	v_mov_b64_e32 v[38:39], v[148:149]
	v_mov_b64_e32 v[40:41], v[150:151]
	s_nop 0
	s_nop 0
	s_nop 0
	s_nop 0
	v_pk_mul_f32 v[18:19], v[18:19], v[22:23]
	v_pk_mul_f32 v[20:21], v[20:21], v[24:25]
	s_nop 0
	v_pk_add_f32 v[22:23], v[36:37], 1.0 op_sel_hi:[1,0]
	v_pk_add_f32 v[24:25], v[34:35], 1.0 op_sel_hi:[1,0]
	s_nop 0
	v_pk_fma_f32 v[20:21], v[22:23], v[20:21], v[40:41]
	v_pk_fma_f32 v[18:19], v[24:25], v[18:19], v[38:39]
	s_nop 0
	v_cvt_pk_bf16_f32 v18, v18, v19
	v_cvt_pk_bf16_f32 v19, v20, v21
	global_store_dwordx2 v[48:49], v[18:19], off offset:512
	s_waitcnt vmcnt(5)
	v_mov_b64_e32 v[18:19], v[152:153]
	v_mov_b64_e32 v[20:21], v[154:155]
	v_mov_b64_e32 v[22:23], v[156:157]
	v_mov_b64_e32 v[24:25], v[158:159]
	v_mov_b64_e32 v[34:35], v[160:161]
	v_mov_b64_e32 v[36:37], v[162:163]
	s_nop 0
	s_nop 0
	s_nop 0
	s_nop 0
	v_pk_mul_f32 v[18:19], v[18:19], v[26:27]
	v_pk_mul_f32 v[20:21], v[20:21], v[28:29]
	s_nop 0
	v_pk_add_f32 v[24:25], v[24:25], 1.0 op_sel_hi:[1,0]
	v_pk_add_f32 v[22:23], v[22:23], 1.0 op_sel_hi:[1,0]
	s_nop 0
	v_pk_fma_f32 v[20:21], v[20:21], v[24:25], v[36:37]
	v_pk_fma_f32 v[18:19], v[18:19], v[22:23], v[34:35]
	s_nop 0
	v_cvt_pk_bf16_f32 v18, v18, v19
	v_cvt_pk_bf16_f32 v19, v20, v21
	global_store_dwordx2 v[48:49], v[18:19], off offset:1024
	s_waitcnt vmcnt(3)
	v_mov_b64_e32 v[18:19], v[176:177]
	v_mov_b64_e32 v[20:21], v[178:179]
	v_mov_b64_e32 v[22:23], v[180:181]
	v_mov_b64_e32 v[24:25], v[182:183]
	v_mov_b64_e32 v[26:27], v[184:185]
	v_mov_b64_e32 v[28:29], v[186:187]
	s_nop 0
	s_nop 0
	s_nop 0
	s_nop 0
	v_pk_mul_f32 v[18:19], v[30:31], v[18:19]
	v_pk_mul_f32 v[20:21], v[32:33], v[20:21]
	s_nop 0
	v_pk_add_f32 v[24:25], v[24:25], 1.0 op_sel_hi:[1,0]
	v_pk_add_f32 v[22:23], v[22:23], 1.0 op_sel_hi:[1,0]
	s_nop 0
	v_pk_fma_f32 v[20:21], v[20:21], v[24:25], v[28:29]
	v_pk_fma_f32 v[18:19], v[18:19], v[22:23], v[26:27]
	s_nop 0
	v_cvt_pk_bf16_f32 v18, v18, v19
	v_cvt_pk_bf16_f32 v19, v20, v21
	global_store_dwordx2 v[48:49], v[18:19], off offset:1536
	s_cbranch_scc0 .LBB0_89

.Lmy_pp_a:
	v_and_b32_e32 v34, 1, v3
	v_lshlrev_b32_e32 v34, 4, v34
	v_lshl_add_u32 v34, v2, 7, v34
	v_add_u32_e32 v34, s3, v34
	v_lshlrev_b32_e32 v110, 5, v203
	v_add_u32_e32 v110, s3, v110
	ds_read_b128 v[114:117], v4 offset:256
	ds_read_b128 v[118:121], v4 offset:272
	v_add_u32_e32 v108, 0x2000, v5
	ds_read_b128 v[122:125], v108 offset:0
	ds_read_b128 v[126:129], v108 offset:1024
	ds_read_b128 v[130:133], v108 offset:2048
	ds_read_b128 v[170:173], v108 offset:3072
	s_waitcnt lgkmcnt(0)
	v_mfma_f32_16x16x4_f32 v[6:9], v114, v122, 0
	v_mfma_f32_16x16x4_f32 v[10:13], v114, v123, 0
	v_mfma_f32_16x16x4_f32 v[14:17], v114, v124, 0
	v_mfma_f32_16x16x4_f32 v[94:97], v114, v125, 0
	v_mfma_f32_16x16x4_f32 v[6:9], v115, v126, v[6:9]
	v_mfma_f32_16x16x4_f32 v[10:13], v115, v127, v[10:13]
	v_mfma_f32_16x16x4_f32 v[14:17], v115, v128, v[14:17]
	v_mfma_f32_16x16x4_f32 v[94:97], v115, v129, v[94:97]
	v_mfma_f32_16x16x4_f32 v[6:9], v116, v130, v[6:9]
	v_mfma_f32_16x16x4_f32 v[10:13], v116, v131, v[10:13]
	v_mfma_f32_16x16x4_f32 v[14:17], v116, v132, v[14:17]
	v_mfma_f32_16x16x4_f32 v[94:97], v116, v133, v[94:97]
	v_mfma_f32_16x16x4_f32 v[6:9], v117, v170, v[6:9]
	v_mfma_f32_16x16x4_f32 v[10:13], v117, v171, v[10:13]
	v_mfma_f32_16x16x4_f32 v[14:17], v117, v172, v[14:17]
	v_mfma_f32_16x16x4_f32 v[94:97], v117, v173, v[94:97]
	s_nop 7
	ds_read_b128 v[122:125], v108 offset:4096
	ds_read_b128 v[126:129], v108 offset:5120
	ds_read_b128 v[130:133], v108 offset:6144
	ds_read_b128 v[170:173], v108 offset:7168
	s_waitcnt lgkmcnt(0)
	v_mfma_f32_16x16x4_f32 v[6:9], v118, v122, v[6:9]
	v_mfma_f32_16x16x4_f32 v[10:13], v118, v123, v[10:13]
	v_mfma_f32_16x16x4_f32 v[14:17], v118, v124, v[14:17]
	v_mfma_f32_16x16x4_f32 v[94:97], v118, v125, v[94:97]
	v_mfma_f32_16x16x4_f32 v[6:9], v119, v126, v[6:9]
	v_mfma_f32_16x16x4_f32 v[10:13], v119, v127, v[10:13]
	v_mfma_f32_16x16x4_f32 v[14:17], v119, v128, v[14:17]
	v_mfma_f32_16x16x4_f32 v[94:97], v119, v129, v[94:97]
	v_mfma_f32_16x16x4_f32 v[6:9], v120, v130, v[6:9]
	v_mfma_f32_16x16x4_f32 v[10:13], v120, v131, v[10:13]
	v_mfma_f32_16x16x4_f32 v[14:17], v120, v132, v[14:17]
	v_mfma_f32_16x16x4_f32 v[94:97], v120, v133, v[94:97]
	v_mfma_f32_16x16x4_f32 v[6:9], v121, v170, v[6:9]
	v_mfma_f32_16x16x4_f32 v[10:13], v121, v171, v[10:13]
	v_mfma_f32_16x16x4_f32 v[14:17], v121, v172, v[14:17]
	v_mfma_f32_16x16x4_f32 v[94:97], v121, v173, v[94:97]
	s_nop 7
	s_nop 15
	s_nop 15
	s_cmp_lt_u32 s2, 4
	s_cselect_b32 exec_lo, -1, 0
	s_cselect_b32 exec_hi, 0, -1
	ds_write_b128 v34, v[6:9] offset:0
	ds_write_b128 v34, v[10:13] offset:32
	ds_write_b128 v34, v[14:17] offset:64
	ds_write_b128 v34, v[94:97] offset:96
	s_mov_b64 exec, -1
	s_waitcnt lgkmcnt(0)
	ds_read_b128 v[174:177], v110
	ds_read_b128 v[178:181], v110 offset:16
	s_waitcnt lgkmcnt(0)
	ds_read_b128 v[114:117], v4 offset:0
	ds_read_b128 v[118:121], v4 offset:16
	v_add_u32_e32 v108, 0xa000, v5
	ds_read_b128 v[122:125], v108 offset:0
	ds_read_b128 v[126:129], v108 offset:1024
	ds_read_b128 v[130:133], v108 offset:2048
	ds_read_b128 v[170:173], v108 offset:3072
	s_waitcnt lgkmcnt(0)
	v_mfma_f32_16x16x4_f32 v[6:9], v114, v122, 0
	v_mfma_f32_16x16x4_f32 v[10:13], v114, v123, 0
	v_mfma_f32_16x16x4_f32 v[14:17], v114, v124, 0
	v_mfma_f32_16x16x4_f32 v[94:97], v114, v125, 0
	v_mfma_f32_16x16x4_f32 v[6:9], v115, v126, v[6:9]
	v_mfma_f32_16x16x4_f32 v[10:13], v115, v127, v[10:13]
	v_mfma_f32_16x16x4_f32 v[14:17], v115, v128, v[14:17]
	v_mfma_f32_16x16x4_f32 v[94:97], v115, v129, v[94:97]
	v_mfma_f32_16x16x4_f32 v[6:9], v116, v130, v[6:9]
	v_mfma_f32_16x16x4_f32 v[10:13], v116, v131, v[10:13]
	v_mfma_f32_16x16x4_f32 v[14:17], v116, v132, v[14:17]
	v_mfma_f32_16x16x4_f32 v[94:97], v116, v133, v[94:97]
	v_mfma_f32_16x16x4_f32 v[6:9], v117, v170, v[6:9]
	v_mfma_f32_16x16x4_f32 v[10:13], v117, v171, v[10:13]
	v_mfma_f32_16x16x4_f32 v[14:17], v117, v172, v[14:17]
	v_mfma_f32_16x16x4_f32 v[94:97], v117, v173, v[94:97]
	s_nop 7
	ds_read_b128 v[122:125], v108 offset:4096
	ds_read_b128 v[126:129], v108 offset:5120
	ds_read_b128 v[130:133], v108 offset:6144
	ds_read_b128 v[170:173], v108 offset:7168
	s_waitcnt lgkmcnt(0)
	v_mfma_f32_16x16x4_f32 v[6:9], v118, v122, v[6:9]
	v_mfma_f32_16x16x4_f32 v[10:13], v118, v123, v[10:13]
	v_mfma_f32_16x16x4_f32 v[14:17], v118, v124, v[14:17]
	v_mfma_f32_16x16x4_f32 v[94:97], v118, v125, v[94:97]
	v_mfma_f32_16x16x4_f32 v[6:9], v119, v126, v[6:9]
	v_mfma_f32_16x16x4_f32 v[10:13], v119, v127, v[10:13]
	v_mfma_f32_16x16x4_f32 v[14:17], v119, v128, v[14:17]
	v_mfma_f32_16x16x4_f32 v[94:97], v119, v129, v[94:97]
	v_mfma_f32_16x16x4_f32 v[6:9], v120, v130, v[6:9]
	v_mfma_f32_16x16x4_f32 v[10:13], v120, v131, v[10:13]
	v_mfma_f32_16x16x4_f32 v[14:17], v120, v132, v[14:17]
	v_mfma_f32_16x16x4_f32 v[94:97], v120, v133, v[94:97]
	v_mfma_f32_16x16x4_f32 v[6:9], v121, v170, v[6:9]
	v_mfma_f32_16x16x4_f32 v[10:13], v121, v171, v[10:13]
	v_mfma_f32_16x16x4_f32 v[14:17], v121, v172, v[14:17]
	v_mfma_f32_16x16x4_f32 v[94:97], v121, v173, v[94:97]
	s_nop 7
	s_nop 15
	s_nop 15
	s_cmp_lt_u32 s2, 4
	s_cselect_b32 exec_lo, -1, 0
	s_cselect_b32 exec_hi, 0, -1
	ds_write_b128 v34, v[6:9] offset:0
	ds_write_b128 v34, v[10:13] offset:32
	ds_write_b128 v34, v[14:17] offset:64
	ds_write_b128 v34, v[94:97] offset:96
	s_mov_b64 exec, -1
	s_waitcnt lgkmcnt(0)
	ds_read_b128 v[182:185], v110
	ds_read_b128 v[186:189], v110 offset:16
	s_waitcnt lgkmcnt(0)
	ds_read_b128 v[114:117], v4 offset:128
	ds_read_b128 v[118:121], v4 offset:144
	v_add_u32_e32 v108, 0x12000, v5
	ds_read_b128 v[122:125], v108 offset:0
	ds_read_b128 v[126:129], v108 offset:1024
	ds_read_b128 v[130:133], v108 offset:2048
	ds_read_b128 v[170:173], v108 offset:3072
	s_waitcnt lgkmcnt(0)
	v_mfma_f32_16x16x4_f32 v[6:9], v114, v122, 0
	v_mfma_f32_16x16x4_f32 v[10:13], v114, v123, 0
	v_mfma_f32_16x16x4_f32 v[14:17], v114, v124, 0
	v_mfma_f32_16x16x4_f32 v[94:97], v114, v125, 0
	v_mfma_f32_16x16x4_f32 v[6:9], v115, v126, v[6:9]
	v_mfma_f32_16x16x4_f32 v[10:13], v115, v127, v[10:13]
	v_mfma_f32_16x16x4_f32 v[14:17], v115, v128, v[14:17]
	v_mfma_f32_16x16x4_f32 v[94:97], v115, v129, v[94:97]
	v_mfma_f32_16x16x4_f32 v[6:9], v116, v130, v[6:9]
	v_mfma_f32_16x16x4_f32 v[10:13], v116, v131, v[10:13]
	v_mfma_f32_16x16x4_f32 v[14:17], v116, v132, v[14:17]
	v_mfma_f32_16x16x4_f32 v[94:97], v116, v133, v[94:97]
	v_mfma_f32_16x16x4_f32 v[6:9], v117, v170, v[6:9]
	v_mfma_f32_16x16x4_f32 v[10:13], v117, v171, v[10:13]
	v_mfma_f32_16x16x4_f32 v[14:17], v117, v172, v[14:17]
	v_mfma_f32_16x16x4_f32 v[94:97], v117, v173, v[94:97]
	s_nop 7
	ds_read_b128 v[122:125], v108 offset:4096
	ds_read_b128 v[126:129], v108 offset:5120
	ds_read_b128 v[130:133], v108 offset:6144
	ds_read_b128 v[170:173], v108 offset:7168
	s_waitcnt lgkmcnt(0)
	v_mfma_f32_16x16x4_f32 v[6:9], v118, v122, v[6:9]
	v_mfma_f32_16x16x4_f32 v[10:13], v118, v123, v[10:13]
	v_mfma_f32_16x16x4_f32 v[14:17], v118, v124, v[14:17]
	v_mfma_f32_16x16x4_f32 v[94:97], v118, v125, v[94:97]
	v_mfma_f32_16x16x4_f32 v[6:9], v119, v126, v[6:9]
	v_mfma_f32_16x16x4_f32 v[10:13], v119, v127, v[10:13]
	v_mfma_f32_16x16x4_f32 v[14:17], v119, v128, v[14:17]
	v_mfma_f32_16x16x4_f32 v[94:97], v119, v129, v[94:97]
	v_mfma_f32_16x16x4_f32 v[6:9], v120, v130, v[6:9]
	v_mfma_f32_16x16x4_f32 v[10:13], v120, v131, v[10:13]
	v_mfma_f32_16x16x4_f32 v[14:17], v120, v132, v[14:17]
	v_mfma_f32_16x16x4_f32 v[94:97], v120, v133, v[94:97]
	v_mfma_f32_16x16x4_f32 v[6:9], v121, v170, v[6:9]
	v_mfma_f32_16x16x4_f32 v[10:13], v121, v171, v[10:13]
	v_mfma_f32_16x16x4_f32 v[14:17], v121, v172, v[14:17]
	v_mfma_f32_16x16x4_f32 v[94:97], v121, v173, v[94:97]
	s_nop 7
	s_nop 15
	s_nop 15
	s_cmp_lt_u32 s2, 4
	s_cselect_b32 exec_lo, -1, 0
	s_cselect_b32 exec_hi, 0, -1
	ds_write_b128 v34, v[6:9] offset:0
	ds_write_b128 v34, v[10:13] offset:32
	ds_write_b128 v34, v[14:17] offset:64
	ds_write_b128 v34, v[94:97] offset:96
	s_mov_b64 exec, -1
	s_waitcnt lgkmcnt(0)
	ds_read_b128 v[122:125], v110
	ds_read_b128 v[126:129], v110 offset:16
	s_waitcnt lgkmcnt(0)
	v_add_f32_e32 v102, v138, v174
	v_add_f32_e32 v103, v138, v175
	v_add_f32_e32 v16, v138, v176
	v_add_f32_e32 v17, v138, v177
	v_add_f32_e32 v10, v138, v178
	v_add_f32_e32 v11, v138, v179
	v_add_f32_e32 v96, v138, v180
	v_add_f32_e32 v97, v138, v181
	v_add_f32_e32 v107, v134, v182
	v_add_f32_e32 v106, v134, v183
	v_add_f32_e32 v13, v134, v184
	v_add_f32_e32 v12, v134, v185
	v_add_f32_e32 v8, v134, v186
	v_add_f32_e32 v9, v134, v187
	v_add_f32_e32 v94, v134, v188
	v_add_f32_e32 v95, v134, v189
	v_add_f32_e32 v105, v136, v122
	v_add_f32_e32 v104, v136, v123
	v_add_f32_e32 v15, v136, v124
	v_add_f32_e32 v14, v136, v125
	v_add_f32_e32 v7, v136, v126
	v_add_f32_e32 v6, v136, v127
	v_add_f32_e32 v91, v136, v128
	v_add_f32_e32 v90, v136, v129
	s_mov_b32 s2, 0
	v_lshlrev_b32_e32 v2, 16, v157
	v_cndmask_b32_e64 v123, 0, v2, s[40:41]
	v_lshlrev_b32_e32 v2, 16, v154
	v_cndmask_b32_e32 v126, 0, v2, vcc
	v_lshlrev_b32_e32 v2, 16, v152
	v_cndmask_b32_e32 v127, 0, v2, vcc
	global_load_dword v2, v[32:33], off offset:1024
	global_load_dword v3, v[40:41], off
	global_load_dword v4, v[36:37], off
	global_load_dword v5, v[38:39], off
	global_load_dword v110, v[32:33], off offset:3712
	global_load_dword v108, v[32:33], off offset:2048
	global_load_dword v112, v[32:33], off
	v_lshlrev_b32_e32 v34, 16, v160
	v_cndmask_b32_e64 v128, 0, v34, s[42:43]
	v_lshlrev_b32_e32 v81, 16, v81
	v_lshlrev_b32_e32 v34, 16, v83
	v_cndmask_b32_e32 v129, 0, v34, vcc
	v_lshlrev_b32_e32 v34, 16, v144
	v_cndmask_b32_e32 v144, 0, v81, vcc
	global_load_dword v81, v[42:43], off
	v_lshlrev_b32_e32 v116, 16, v153
	v_cndmask_b32_e64 v130, 0, v34, s[44:45]
	v_lshlrev_b32_e32 v34, 16, v109
	v_lshlrev_b32_e32 v89, 16, v89
	v_lshlrev_b32_e32 v114, 16, v156
	v_cndmask_b32_e64 v83, 0, v34, s[46:47]
	v_lshlrev_b32_e32 v34, 16, v93
	v_lshlrev_b32_e32 v93, 16, v99
	v_cndmask_b32_e32 v133, 0, v116, vcc
	v_cndmask_b32_e64 v116, 0, v89, s[48:49]
	v_and_b32_e32 v89, 64, v203
	v_lshlrev_b32_e32 v117, 16, v155
	v_lshlrev_b32_e32 v118, 16, v151
	v_lshlrev_b32_e32 v119, 16, v161
	v_lshlrev_b32_e32 v85, 16, v85
	v_lshlrev_b32_e32 v79, 16, v79
	v_lshlrev_b32_e32 v109, 16, v111
	v_cndmask_b32_e64 v111, 0, v34, s[48:49]
	v_lshlrev_b32_e32 v99, 16, v148
	v_lshlrev_b32_e32 v34, 16, v149
	v_lshlrev_b32_e32 v122, 16, v150
	v_cndmask_b32_e64 v131, 0, v114, s[40:41]
	v_cndmask_b32_e64 v114, 0, v93, s[48:49]
	v_add_u32_e32 v89, 64, v89
	v_xor_b32_e32 v93, 1, v203
	v_cndmask_b32_e32 v34, 0, v34, vcc
	v_lshlrev_b32_e32 v124, 16, v145
	v_cndmask_b32_e32 v134, 0, v117, vcc
	v_cndmask_b32_e32 v136, 0, v118, vcc
	v_cndmask_b32_e32 v138, 0, v119, vcc
	v_cndmask_b32_e32 v85, 0, v85, vcc
	v_cndmask_b32_e64 v145, 0, v79, s[44:45]
	v_cndmask_b32_e64 v148, 0, v109, s[46:47]
	v_cndmask_b32_e32 v109, 0, v99, vcc
	v_cndmask_b32_e32 v79, 0, v122, vcc
	v_cmp_lt_i32_e32 vcc, v93, v89
	v_lshlrev_b32_e32 v121, 16, v113
	v_lshlrev_b32_e32 v113, 16, v146
	v_cndmask_b32_e32 v93, v203, v93, vcc
	v_lshlrev_b32_e32 v122, 2, v93
	v_xor_b32_e32 v93, 2, v203
	v_cmp_lt_i32_e32 vcc, v93, v89
	v_cndmask_b32_e64 v146, 0, v121, s[44:45]
	v_lshlrev_b32_e32 v120, 16, v159
	v_cndmask_b32_e32 v93, v203, v93, vcc
	v_lshlrev_b32_e32 v121, 2, v93
	v_xor_b32_e32 v93, 4, v203
	v_cmp_lt_i32_e32 vcc, v93, v89
	v_cndmask_b32_e64 v140, 0, v120, s[42:43]
	v_sub_f32_e32 v99, v127, v126
	v_cndmask_b32_e32 v93, v203, v93, vcc
	v_lshlrev_b32_e32 v120, 2, v93
	v_xor_b32_e32 v93, 8, v203
	v_cmp_lt_i32_e32 vcc, v93, v89
	v_lshlrev_b32_e32 v101, 16, v101
	v_lshlrev_b32_e32 v125, 16, v147
	v_cndmask_b32_e32 v93, v203, v93, vcc
	v_lshlrev_b32_e32 v119, 2, v93
	v_xor_b32_e32 v93, 16, v203
	v_cmp_lt_i32_e32 vcc, v93, v89
	v_cndmask_b32_e64 v147, 0, v101, s[46:47]
	v_lshlrev_b32_e32 v115, 16, v158
	v_cndmask_b32_e32 v93, v203, v93, vcc
	v_lshlrev_b32_e32 v118, 2, v93
	v_xor_b32_e32 v93, 32, v203
	v_cmp_lt_i32_e32 vcc, v93, v89
	v_cndmask_b32_e64 v132, 0, v115, s[40:41]
	v_cndmask_b32_e64 v115, 0, v125, s[50:51]
	v_cndmask_b32_e32 v89, v203, v93, vcc
	v_sub_f32_e32 v93, v123, v126
	s_waitcnt vmcnt(7)
	v_fma_f32 v93, v93, v2, v126
	s_waitcnt vmcnt(5)
	v_fmac_f32_e32 v93, v99, v4
	v_mul_f32_e32 v99, v93, v3
	v_mul_f32_e32 v101, v99, v99
	s_nop 1
	v_mov_b32_dpp v101, v101 quad_perm:[1,0,3,2] row_mask:0xf bank_mask:0xf
	v_lshlrev_b32_e32 v123, 2, v89
	v_sub_f32_e32 v89, v131, v133
	v_cndmask_b32_e64 v117, 0, v124, s[50:51]
	s_waitcnt vmcnt(1)
	v_fma_f32 v89, v89, v112, v133
	s_waitcnt lgkmcnt(0)
	v_fmac_f32_e32 v101, v99, v99
	s_nop 1
	v_sub_f32_e32 v124, v136, v133
	v_fmac_f32_e32 v89, v124, v110
	v_sub_f32_e32 v124, v132, v134
	v_fma_f32 v131, v124, v108, v134
	s_waitcnt lgkmcnt(0)
	v_add_f32_dpp v101, v101, v101 quad_perm:[2,3,0,1] row_mask:0xf bank_mask:0xf
	s_nop 1
	v_sub_f32_e32 v124, v138, v134
	v_fmac_f32_e32 v131, v124, v5
	v_mul_f32_e32 v102, 0xbfb8aa3b, v102
	v_exp_f32_e32 v102, v102
	s_waitcnt lgkmcnt(0)
	v_add_f32_dpp v101, v101, v101 row_half_mirror row_mask:0xf bank_mask:0xf
	s_nop 1
	v_mul_f32_e32 v107, 0xbfb8aa3b, v107
	v_add_f32_e32 v102, 1.0, v102
	v_rcp_f32_e32 v102, v102
	v_exp_f32_e32 v107, v107
	s_waitcnt lgkmcnt(0)
	v_add_f32_dpp v101, v101, v101 row_mirror row_mask:0xf bank_mask:0xf
	v_mov_b32_e32 v124, v101
	s_nop 1
	v_permlane16_swap_b32_e32 v124, v101
	v_mul_f32_e32 v105, 0xbfb8aa3b, v105
	v_exp_f32_e32 v105, v105
	v_cvt_pk_bf16_f32 v89, v89, s0
	v_add_f32_e32 v107, 1.0, v107
	s_waitcnt lgkmcnt(0)
	v_add_f32_e32 v101, v101, v124
	v_mov_b32_e32 v124, v101
	s_nop 1
	v_permlane32_swap_b32_e32 v124, v101
	v_rcp_f32_e32 v107, v107
	v_add_f32_e32 v105, 1.0, v105
	v_rcp_f32_e32 v105, v105
	v_mul_f32_e32 v103, 0xbfb8aa3b, v103
	s_waitcnt lgkmcnt(0)
	v_add_f32_e32 v101, v101, v124
	v_add_f32_e32 v101, 0x2b8cbccc, v101
	v_rsq_f32_e32 v101, v101
	v_mul_f32_e32 v107, 0xbf1b459e, v107
	v_mul_f32_e32 v107, 0x3fb8aa3b, v107
	v_mul_f32_e32 v105, 0xbf1b459e, v105
	v_mul_f32_e32 v99, v99, v101
	v_add_f32_e32 v101, -1.0, v102
	s_waitcnt vmcnt(0)
	v_fma_f32 v101, v101, v81, 1.0
	v_mul_f32_e32 v93, v93, v101
	v_ashrrev_i32_e32 v101, 31, v100
	v_lshlrev_b64 v[100:101], 9, v[100:101]
	v_or_b32_e32 v100, v100, v31
	v_lshl_add_u64 v[124:125], s[74:75], 0, v[100:101]
	global_store_short v[124:125], v89, off
	v_lshl_add_u64 v[124:125], s[76:77], 0, v[100:101]
	v_cvt_pk_bf16_f32 v89, v93, s0
	global_store_short v[124:125], v89, off
	v_lshl_add_u64 v[124:125], s[78:79], 0, v[100:101]
	v_cvt_pk_bf16_f32 v89, v131, s0
	global_store_short v[124:125], v89, off
	v_lshl_add_u64 v[124:125], s[80:81], 0, v[100:101]
	v_cvt_pk_bf16_f32 v89, v99, s0
	v_sub_f32_e32 v93, v126, v127
	global_store_short v[124:125], v89, off
	v_mul_f32_e32 v89, v102, v99
	v_fma_f32 v93, v93, v2, v127
	v_sub_f32_e32 v99, v128, v127
	v_fmac_f32_e32 v93, v99, v4
	v_mul_f32_e32 v99, v93, v3
	v_mul_f32_e32 v102, v99, v99
	v_exp_f32_e32 v107, v107
	v_mul_f32_e32 v105, 0x3fb8aa3b, v105
	s_nop 1
	v_mov_b32_dpp v102, v102 quad_perm:[1,0,3,2] row_mask:0xf bank_mask:0xf
	v_exp_f32_e32 v105, v105
	v_lshl_add_u64 v[124:125], s[82:83], 0, v[100:101]
	v_cvt_pk_bf16_f32 v89, v89, s0
	global_store_short v[124:125], v89, off
	v_lshl_add_u64 v[124:125], s[84:85], 0, v[100:101]
	v_cvt_pk_bf16_f32 v89, v107, s0
	global_store_short v[124:125], v89, off
	v_lshl_add_u64 v[100:101], s[86:87], 0, v[100:101]
	v_cvt_pk_bf16_f32 v89, v105, s0
	s_waitcnt lgkmcnt(0)
	v_fmac_f32_e32 v102, v99, v99
	global_store_short v[100:101], v89, off
	s_nop 1
	v_mul_f32_e32 v106, 0xbfb8aa3b, v106
	v_sub_f32_e32 v89, v133, v136
	v_exp_f32_e32 v103, v103
	v_exp_f32_e32 v106, v106
	s_waitcnt lgkmcnt(0)
	v_add_f32_dpp v101, v102, v102 quad_perm:[2,3,0,1] row_mask:0xf bank_mask:0xf
	s_nop 1
	v_lshlrev_b32_e32 v87, 16, v87
	v_fma_f32 v89, v89, v112, v136
	v_sub_f32_e32 v100, v140, v136
	v_cndmask_b32_e64 v87, 0, v87, s[42:43]
	s_waitcnt lgkmcnt(0)
	v_add_f32_dpp v101, v101, v101 row_half_mirror row_mask:0xf bank_mask:0xf
	s_nop 1
	v_fmac_f32_e32 v89, v100, v110
	v_sub_f32_e32 v100, v134, v138
	v_fma_f32 v105, v100, v108, v138
	v_sub_f32_e32 v100, v87, v138
	s_waitcnt lgkmcnt(0)
	v_add_f32_dpp v101, v101, v101 row_mirror row_mask:0xf bank_mask:0xf
	v_mov_b32_e32 v102, v101
	s_nop 1
	v_permlane16_swap_b32_e32 v102, v101
	v_fmac_f32_e32 v105, v100, v5
	v_add_f32_e32 v100, 1.0, v103
	v_add_f32_e32 v103, 1.0, v106
	v_rcp_f32_e32 v103, v103
	s_waitcnt lgkmcnt(0)
	v_add_f32_e32 v101, v101, v102
	v_mov_b32_e32 v102, v101
	s_nop 1
	v_permlane32_swap_b32_e32 v102, v101
	v_rcp_f32_e32 v106, v100
	v_mul_f32_e32 v100, 0xbf1b459e, v103
	v_mul_f32_e32 v103, 0xbfb8aa3b, v104
	v_exp_f32_e32 v103, v103
	s_waitcnt lgkmcnt(0)
	v_add_f32_e32 v101, v101, v102
	v_add_f32_e32 v101, 0x2b8cbccc, v101
	v_rsq_f32_e32 v101, v101
	v_mul_f32_e32 v100, 0x3fb8aa3b, v100
	v_exp_f32_e32 v104, v100
	v_add_f32_e32 v100, 1.0, v103
	v_rcp_f32_e32 v100, v100
	v_mul_f32_e32 v103, v99, v101
	v_add_f32_e32 v99, -1.0, v106
	v_fma_f32 v99, v99, v81, 1.0
	v_mul_f32_e32 v93, v93, v99
	v_ashrrev_i32_e32 v99, 31, v98
	v_mul_f32_e32 v100, 0xbf1b459e, v100
	v_lshlrev_b64 v[98:99], 9, v[98:99]
	v_mul_f32_e32 v100, 0x3fb8aa3b, v100
	v_or_b32_e32 v98, v98, v31
	v_exp_f32_e32 v102, v100
	v_lshl_add_u64 v[100:101], s[74:75], 0, v[98:99]
	v_cvt_pk_bf16_f32 v89, v89, s0
	global_store_short v[100:101], v89, off
	v_lshl_add_u64 v[100:101], s[76:77], 0, v[98:99]
	v_cvt_pk_bf16_f32 v89, v93, s0
	global_store_short v[100:101], v89, off
	v_lshl_add_u64 v[100:101], s[78:79], 0, v[98:99]
	v_cvt_pk_bf16_f32 v89, v105, s0
	global_store_short v[100:101], v89, off
	v_lshl_add_u64 v[100:101], s[80:81], 0, v[98:99]
	v_cvt_pk_bf16_f32 v89, v103, s0
	global_store_short v[100:101], v89, off
	v_mul_f32_e32 v89, v106, v103
	v_lshl_add_u64 v[100:101], s[82:83], 0, v[98:99]
	v_cvt_pk_bf16_f32 v89, v89, s0
	global_store_short v[100:101], v89, off
	v_lshl_add_u64 v[100:101], s[84:85], 0, v[98:99]
	v_cvt_pk_bf16_f32 v89, v104, s0
	v_sub_f32_e32 v93, v127, v128
	global_store_short v[100:101], v89, off
	v_fma_f32 v93, v93, v2, v128
	v_sub_f32_e32 v100, v129, v128
	v_fmac_f32_e32 v93, v100, v4
	v_mul_f32_e32 v100, v93, v3
	v_mul_f32_e32 v101, v100, v100
	s_nop 1
	v_mov_b32_dpp v101, v101 quad_perm:[1,0,3,2] row_mask:0xf bank_mask:0xf
	v_lshl_add_u64 v[98:99], s[86:87], 0, v[98:99]
	v_cvt_pk_bf16_f32 v89, v102, s0
	global_store_short v[98:99], v89, off
	v_sub_f32_e32 v89, v136, v140
	s_waitcnt lgkmcnt(0)
	v_fmac_f32_e32 v101, v100, v100
	s_nop 1
	v_fma_f32 v89, v89, v112, v140
	v_sub_f32_e32 v98, v144, v140
	v_fmac_f32_e32 v89, v98, v110
	v_sub_f32_e32 v98, v138, v87
	s_waitcnt lgkmcnt(0)
	v_add_f32_dpp v99, v101, v101 quad_perm:[2,3,0,1] row_mask:0xf bank_mask:0xf
	s_nop 1
	v_fma_f32 v102, v98, v108, v87
	v_sub_f32_e32 v98, v85, v87
	v_fmac_f32_e32 v102, v98, v5
	v_mul_f32_e32 v16, 0xbfb8aa3b, v16
	s_waitcnt lgkmcnt(0)
	v_add_f32_dpp v99, v99, v99 row_half_mirror row_mask:0xf bank_mask:0xf
	s_nop 1
	v_exp_f32_e32 v16, v16
	v_mul_f32_e32 v13, 0xbfb8aa3b, v13
	v_exp_f32_e32 v13, v13
	v_mul_f32_e32 v15, 0xbfb8aa3b, v15
	s_waitcnt lgkmcnt(0)
	v_add_f32_dpp v98, v99, v99 row_mirror row_mask:0xf bank_mask:0xf
	v_mov_b32_e32 v99, v98
	s_nop 1
	v_permlane16_swap_b32_e32 v99, v98
	v_add_f32_e32 v16, 1.0, v16
	v_rcp_f32_e32 v16, v16
	v_exp_f32_e32 v15, v15
	v_add_f32_e32 v13, 1.0, v13
	s_waitcnt lgkmcnt(0)
	v_add_f32_e32 v98, v98, v99
	v_mov_b32_e32 v99, v98
	s_nop 1
	v_permlane32_swap_b32_e32 v99, v98
	v_rcp_f32_e32 v13, v13
	v_add_f32_e32 v15, 1.0, v15
	v_rcp_f32_e32 v15, v15
	v_cvt_pk_bf16_f32 v89, v89, s0
	s_waitcnt lgkmcnt(0)
	v_add_f32_e32 v98, v98, v99
	v_add_f32_e32 v98, 0x2b8cbccc, v98
	v_rsq_f32_e32 v98, v98
	v_mul_f32_e32 v13, 0xbf1b459e, v13
	v_mul_f32_e32 v13, 0x3fb8aa3b, v13
	v_mul_f32_e32 v15, 0xbf1b459e, v15
	v_mul_f32_e32 v100, v100, v98
	v_add_f32_e32 v98, -1.0, v16
	v_fma_f32 v98, v98, v81, 1.0
	v_mul_f32_e32 v101, v93, v98
	v_ashrrev_i32_e32 v93, 31, v92
	v_lshlrev_b64 v[92:93], 9, v[92:93]
	v_or_b32_e32 v92, v92, v31
	v_lshl_add_u64 v[98:99], s[74:75], 0, v[92:93]
	v_exp_f32_e32 v13, v13
	v_mul_f32_e32 v15, 0x3fb8aa3b, v15
	global_store_short v[98:99], v89, off
	v_lshl_add_u64 v[98:99], s[76:77], 0, v[92:93]
	v_cvt_pk_bf16_f32 v89, v101, s0
	v_exp_f32_e32 v15, v15
	global_store_short v[98:99], v89, off
	v_lshl_add_u64 v[98:99], s[78:79], 0, v[92:93]
	v_cvt_pk_bf16_f32 v89, v102, s0
	global_store_short v[98:99], v89, off
	v_lshl_add_u64 v[98:99], s[80:81], 0, v[92:93]
	v_cvt_pk_bf16_f32 v89, v100, s0
	v_mul_f32_e32 v16, v16, v100
	global_store_short v[98:99], v89, off
	v_lshl_add_u64 v[98:99], s[82:83], 0, v[92:93]
	v_cvt_pk_bf16_f32 v16, v16, s0
	global_store_short v[98:99], v16, off
	v_lshl_add_u64 v[98:99], s[84:85], 0, v[92:93]
	v_cvt_pk_bf16_f32 v13, v13, s0
	global_store_short v[98:99], v13, off
	v_cvt_pk_bf16_f32 v13, v15, s0
	v_sub_f32_e32 v15, v128, v129
	v_fma_f32 v15, v15, v2, v129
	v_sub_f32_e32 v16, v130, v129
	v_fmac_f32_e32 v15, v16, v4
	v_mul_f32_e32 v16, v15, v3
	v_mul_f32_e32 v89, v16, v16
	s_nop 1
	v_mov_b32_dpp v89, v89 quad_perm:[1,0,3,2] row_mask:0xf bank_mask:0xf
	v_lshl_add_u64 v[92:93], s[86:87], 0, v[92:93]
	global_store_short v[92:93], v13, off
	v_sub_f32_e32 v13, v140, v144
	v_fma_f32 v92, v13, v112, v144
	s_waitcnt lgkmcnt(0)
	v_fmac_f32_e32 v89, v16, v16
	s_nop 1
	v_sub_f32_e32 v13, v145, v144
	v_fmac_f32_e32 v92, v13, v110
	v_sub_f32_e32 v13, v87, v85
	v_mul_f32_e32 v17, 0xbfb8aa3b, v17
	s_waitcnt lgkmcnt(0)
	v_add_f32_dpp v87, v89, v89 quad_perm:[2,3,0,1] row_mask:0xf bank_mask:0xf
	s_nop 1
	v_exp_f32_e32 v17, v17
	v_mul_f32_e32 v12, 0xbfb8aa3b, v12
	v_exp_f32_e32 v12, v12
	v_fma_f32 v98, v13, v108, v85
	s_waitcnt lgkmcnt(0)
	v_add_f32_dpp v87, v87, v87 row_half_mirror row_mask:0xf bank_mask:0xf
	s_nop 1
	v_sub_f32_e32 v13, v146, v85
	v_fmac_f32_e32 v98, v13, v5
	v_add_f32_e32 v13, 1.0, v17
	v_add_f32_e32 v12, 1.0, v12
	s_waitcnt lgkmcnt(0)
	v_add_f32_dpp v17, v87, v87 row_mirror row_mask:0xf bank_mask:0xf
	v_mov_b32_e32 v87, v17
	s_nop 1
	v_permlane16_swap_b32_e32 v87, v17
	v_rcp_f32_e32 v12, v12
	v_rcp_f32_e32 v89, v13
	v_mul_f32_e32 v13, 0xbfb8aa3b, v14
	v_exp_f32_e32 v13, v13
	s_waitcnt lgkmcnt(0)
	v_add_f32_e32 v14, v17, v87
	v_mul_f32_e32 v12, 0xbf1b459e, v12
	v_mov_b32_e32 v17, v14
	s_nop 1
	v_permlane32_swap_b32_e32 v17, v14
	v_mul_f32_e32 v12, 0x3fb8aa3b, v12
	v_exp_f32_e32 v93, v12
	v_add_f32_e32 v12, 1.0, v13
	v_rcp_f32_e32 v12, v12
	s_waitcnt lgkmcnt(0)
	v_add_f32_e32 v13, v14, v17
	v_add_f32_e32 v13, 0x2b8cbccc, v13
	v_rsq_f32_e32 v13, v13
	v_mul_f32_e32 v12, 0xbf1b459e, v12
	v_mul_f32_e32 v12, 0x3fb8aa3b, v12
	v_exp_f32_e32 v17, v12
	v_add_f32_e32 v12, -1.0, v89
	v_fma_f32 v12, v12, v81, 1.0
	v_ashrrev_i32_e32 v87, 31, v86
	v_mul_f32_e32 v16, v16, v13
	v_mul_f32_e32 v99, v15, v12
	v_lshlrev_b64 v[12:13], 9, v[86:87]
	v_or_b32_e32 v12, v12, v31
	v_lshl_add_u64 v[14:15], s[74:75], 0, v[12:13]
	v_cvt_pk_bf16_f32 v86, v92, s0
	global_store_short v[14:15], v86, off
	v_lshl_add_u64 v[14:15], s[76:77], 0, v[12:13]
	v_cvt_pk_bf16_f32 v86, v99, s0
	global_store_short v[14:15], v86, off
	v_lshl_add_u64 v[14:15], s[78:79], 0, v[12:13]
	v_cvt_pk_bf16_f32 v86, v98, s0
	global_store_short v[14:15], v86, off
	v_lshl_add_u64 v[14:15], s[80:81], 0, v[12:13]
	v_cvt_pk_bf16_f32 v86, v16, s0
	v_mul_f32_e32 v16, v89, v16
	global_store_short v[14:15], v86, off
	v_lshl_add_u64 v[14:15], s[82:83], 0, v[12:13]
	v_cvt_pk_bf16_f32 v16, v16, s0
	global_store_short v[14:15], v16, off
	v_lshl_add_u64 v[14:15], s[84:85], 0, v[12:13]
	v_cvt_pk_bf16_f32 v16, v93, s0
	global_store_short v[14:15], v16, off
	v_sub_f32_e32 v15, v129, v130
	v_fma_f32 v15, v15, v2, v130
	v_sub_f32_e32 v16, v83, v130
	v_fmac_f32_e32 v15, v16, v4
	v_mul_f32_e32 v16, v15, v3
	v_cvt_pk_bf16_f32 v14, v17, s0
	v_mul_f32_e32 v17, v16, v16
	s_nop 1
	v_mov_b32_dpp v17, v17 quad_perm:[1,0,3,2] row_mask:0xf bank_mask:0xf
	v_lshl_add_u64 v[12:13], s[86:87], 0, v[12:13]
	global_store_short v[12:13], v14, off
	v_sub_f32_e32 v12, v144, v145
	v_fma_f32 v86, v12, v112, v145
	s_waitcnt lgkmcnt(0)
	v_fmac_f32_e32 v17, v16, v16
	s_nop 1
	v_sub_f32_e32 v12, v147, v145
	v_fmac_f32_e32 v86, v12, v110
	v_sub_f32_e32 v12, v85, v146
	v_fma_f32 v85, v12, v108, v146
	s_waitcnt lgkmcnt(0)
	v_add_f32_dpp v13, v17, v17 quad_perm:[2,3,0,1] row_mask:0xf bank_mask:0xf
	s_nop 1
	v_sub_f32_e32 v12, v148, v146
	v_fmac_f32_e32 v85, v12, v5
	v_mul_f32_e32 v10, 0xbfb8aa3b, v10
	v_exp_f32_e32 v10, v10
	s_waitcnt lgkmcnt(0)
	v_add_f32_dpp v13, v13, v13 row_half_mirror row_mask:0xf bank_mask:0xf
	s_nop 1
	v_mul_f32_e32 v8, 0xbfb8aa3b, v8
	v_exp_f32_e32 v8, v8
	v_add_f32_e32 v10, 1.0, v10
	v_rcp_f32_e32 v10, v10
	s_waitcnt lgkmcnt(0)
	v_add_f32_dpp v12, v13, v13 row_mirror row_mask:0xf bank_mask:0xf
	v_mov_b32_e32 v13, v12
	s_nop 1
	v_permlane16_swap_b32_e32 v13, v12
	v_add_f32_e32 v8, 1.0, v8
	v_rcp_f32_e32 v8, v8
	v_ashrrev_i32_e32 v89, 31, v88
	v_mul_f32_e32 v7, 0xbfb8aa3b, v7
	s_waitcnt lgkmcnt(0)
	v_add_f32_e32 v12, v12, v13
	v_mov_b32_e32 v13, v12
	s_nop 1
	v_permlane32_swap_b32_e32 v13, v12
	v_mul_f32_e32 v8, 0xbf1b459e, v8
	v_mul_f32_e32 v8, 0x3fb8aa3b, v8
	v_cvt_pk_bf16_f32 v86, v86, s0
	v_exp_f32_e32 v7, v7
	s_waitcnt lgkmcnt(0)
	v_add_f32_e32 v12, v12, v13
	v_add_f32_e32 v12, 0x2b8cbccc, v12
	v_rsq_f32_e32 v12, v12
	v_exp_f32_e32 v8, v8
	v_add_f32_e32 v7, 1.0, v7
	v_rcp_f32_e32 v7, v7
	v_mul_f32_e32 v16, v16, v12
	v_add_f32_e32 v12, -1.0, v10
	v_fma_f32 v12, v12, v81, 1.0
	v_mul_f32_e32 v17, v15, v12
	v_lshlrev_b64 v[12:13], 9, v[88:89]
	v_or_b32_e32 v12, v12, v31
	v_lshl_add_u64 v[14:15], s[74:75], 0, v[12:13]
	global_store_short v[14:15], v86, off
	v_lshl_add_u64 v[14:15], s[76:77], 0, v[12:13]
	v_cvt_pk_bf16_f32 v17, v17, s0
	global_store_short v[14:15], v17, off
	v_lshl_add_u64 v[14:15], s[78:79], 0, v[12:13]
	v_cvt_pk_bf16_f32 v17, v85, s0
	global_store_short v[14:15], v17, off
	v_lshl_add_u64 v[14:15], s[80:81], 0, v[12:13]
	v_cvt_pk_bf16_f32 v17, v16, s0
	v_mul_f32_e32 v10, v10, v16
	global_store_short v[14:15], v17, off
	v_lshl_add_u64 v[14:15], s[82:83], 0, v[12:13]
	v_cvt_pk_bf16_f32 v10, v10, s0
	global_store_short v[14:15], v10, off
	v_lshl_add_u64 v[14:15], s[84:85], 0, v[12:13]
	v_cvt_pk_bf16_f32 v8, v8, s0
	global_store_short v[14:15], v8, off
	v_sub_f32_e32 v8, v130, v83
	v_fma_f32 v8, v8, v2, v83
	v_sub_f32_e32 v10, v111, v83
	v_fmac_f32_e32 v8, v10, v4
	v_mul_f32_e32 v10, v8, v3
	v_mul_f32_e32 v7, 0xbf1b459e, v7
	v_mul_f32_e32 v14, v10, v10
	v_mul_f32_e32 v7, 0x3fb8aa3b, v7
	s_nop 1
	v_mov_b32_dpp v14, v14 quad_perm:[1,0,3,2] row_mask:0xf bank_mask:0xf
	v_exp_f32_e32 v7, v7
	v_lshl_add_u64 v[12:13], s[86:87], 0, v[12:13]
	v_mul_f32_e32 v11, 0xbfb8aa3b, v11
	v_exp_f32_e32 v11, v11
	v_cvt_pk_bf16_f32 v7, v7, s0
	s_waitcnt lgkmcnt(0)
	v_fmac_f32_e32 v14, v10, v10
	global_store_short v[12:13], v7, off
	s_nop 1
	v_sub_f32_e32 v7, v145, v147
	v_mul_f32_e32 v9, 0xbfb8aa3b, v9
	v_fma_f32 v12, v7, v112, v147
	v_sub_f32_e32 v7, v116, v147
	s_waitcnt lgkmcnt(0)
	v_add_f32_dpp v13, v14, v14 quad_perm:[2,3,0,1] row_mask:0xf bank_mask:0xf
	s_nop 1
	v_exp_f32_e32 v9, v9
	v_fmac_f32_e32 v12, v7, v110
	v_sub_f32_e32 v7, v146, v148
	v_fma_f32 v15, v7, v108, v148
	s_waitcnt lgkmcnt(0)
	v_add_f32_dpp v13, v13, v13 row_half_mirror row_mask:0xf bank_mask:0xf
	s_nop 1
	v_sub_f32_e32 v7, v114, v148
	v_fmac_f32_e32 v15, v7, v5
	v_add_f32_e32 v7, 1.0, v11
	v_add_f32_e32 v9, 1.0, v9
	s_waitcnt lgkmcnt(0)
	v_add_f32_dpp v11, v13, v13 row_mirror row_mask:0xf bank_mask:0xf
	v_mov_b32_e32 v13, v11
	s_nop 1
	v_permlane16_swap_b32_e32 v13, v11
	v_rcp_f32_e32 v9, v9
	v_mul_f32_e32 v6, 0xbfb8aa3b, v6
	v_exp_f32_e32 v6, v6
	v_rcp_f32_e32 v14, v7
	v_mul_f32_e32 v7, 0xbf1b459e, v9
	s_waitcnt lgkmcnt(0)
	v_add_f32_e32 v9, v11, v13
	v_mov_b32_e32 v11, v9
	s_nop 1
	v_permlane32_swap_b32_e32 v11, v9
	v_add_f32_e32 v6, 1.0, v6
	v_rcp_f32_e32 v6, v6
	v_mul_f32_e32 v7, 0x3fb8aa3b, v7
	v_exp_f32_e32 v13, v7
	s_waitcnt lgkmcnt(0)
	v_add_f32_e32 v7, v9, v11
	v_add_f32_e32 v7, 0x2b8cbccc, v7
	v_rsq_f32_e32 v7, v7
	v_mul_f32_e32 v6, 0xbf1b459e, v6
	v_mul_f32_e32 v6, 0x3fb8aa3b, v6
	v_exp_f32_e32 v11, v6
	v_add_f32_e32 v6, -1.0, v14
	v_fma_f32 v6, v6, v81, 1.0
	v_ashrrev_i32_e32 v85, 31, v84
	v_mul_f32_e32 v10, v10, v7
	v_mul_f32_e32 v16, v8, v6
	v_lshlrev_b64 v[6:7], 9, v[84:85]
	v_or_b32_e32 v6, v6, v31
	v_lshl_add_u64 v[8:9], s[74:75], 0, v[6:7]
	v_cvt_pk_bf16_f32 v12, v12, s0
	global_store_short v[8:9], v12, off
	v_lshl_add_u64 v[8:9], s[76:77], 0, v[6:7]
	v_cvt_pk_bf16_f32 v12, v16, s0
	global_store_short v[8:9], v12, off
	v_lshl_add_u64 v[8:9], s[78:79], 0, v[6:7]
	v_cvt_pk_bf16_f32 v12, v15, s0
	global_store_short v[8:9], v12, off
	v_lshl_add_u64 v[8:9], s[80:81], 0, v[6:7]
	v_cvt_pk_bf16_f32 v12, v10, s0
	v_mul_f32_e32 v10, v14, v10
	global_store_short v[8:9], v12, off
	v_lshl_add_u64 v[8:9], s[82:83], 0, v[6:7]
	v_cvt_pk_bf16_f32 v10, v10, s0
	global_store_short v[8:9], v10, off
	v_lshl_add_u64 v[8:9], s[84:85], 0, v[6:7]
	v_cvt_pk_bf16_f32 v10, v13, s0
	global_store_short v[8:9], v10, off
	v_sub_f32_e32 v9, v83, v111
	v_fma_f32 v9, v9, v2, v111
	v_sub_f32_e32 v10, v34, v111
	v_fmac_f32_e32 v9, v10, v4
	v_mul_f32_e32 v10, v9, v3
	v_cvt_pk_bf16_f32 v8, v11, s0
	v_mul_f32_e32 v11, v10, v10
	s_nop 1
	v_mov_b32_dpp v11, v11 quad_perm:[1,0,3,2] row_mask:0xf bank_mask:0xf
	v_lshl_add_u64 v[6:7], s[86:87], 0, v[6:7]
	global_store_short v[6:7], v8, off
	v_mul_f32_e32 v14, 0xbfb8aa3b, v94
	v_sub_f32_e32 v6, v147, v116
	s_waitcnt lgkmcnt(0)
	v_fmac_f32_e32 v11, v10, v10
	s_nop 1
	v_exp_f32_e32 v14, v14
	v_fma_f32 v12, v6, v112, v116
	v_sub_f32_e32 v6, v109, v116
	v_fmac_f32_e32 v12, v6, v110
	s_waitcnt lgkmcnt(0)
	v_add_f32_dpp v7, v11, v11 quad_perm:[2,3,0,1] row_mask:0xf bank_mask:0xf
	s_nop 1
	v_mul_f32_e32 v11, 0xbfb8aa3b, v96
	v_exp_f32_e32 v11, v11
	v_sub_f32_e32 v6, v148, v114
	v_fma_f32 v13, v6, v108, v114
	s_waitcnt lgkmcnt(0)
	v_add_f32_dpp v7, v7, v7 row_half_mirror row_mask:0xf bank_mask:0xf
	s_nop 1
	v_sub_f32_e32 v6, v79, v114
	v_fmac_f32_e32 v13, v6, v5
	v_add_f32_e32 v6, 1.0, v11
	v_add_f32_e32 v11, 1.0, v14
	v_rcp_f32_e32 v11, v11
	s_waitcnt lgkmcnt(0)
	v_add_f32_dpp v7, v7, v7 row_mirror row_mask:0xf bank_mask:0xf
	v_mov_b32_e32 v8, v7
	s_nop 1
	v_permlane16_swap_b32_e32 v8, v7
	v_rcp_f32_e32 v14, v6
	v_mul_f32_e32 v6, 0xbf1b459e, v11
	v_mul_f32_e32 v11, 0xbfb8aa3b, v91
	v_exp_f32_e32 v11, v11
	s_waitcnt lgkmcnt(0)
	v_add_f32_e32 v7, v7, v8
	v_mov_b32_e32 v8, v7
	s_nop 1
	v_permlane32_swap_b32_e32 v8, v7
	v_mul_f32_e32 v6, 0x3fb8aa3b, v6
	v_exp_f32_e32 v15, v6
	v_add_f32_e32 v6, 1.0, v11
	v_rcp_f32_e32 v6, v6
	s_waitcnt lgkmcnt(0)
	v_add_f32_e32 v7, v7, v8
	v_add_f32_e32 v7, 0x2b8cbccc, v7
	v_rsq_f32_e32 v7, v7
	v_mul_f32_e32 v6, 0xbf1b459e, v6
	v_mul_f32_e32 v6, 0x3fb8aa3b, v6
	v_exp_f32_e32 v11, v6
	v_add_f32_e32 v6, -1.0, v14
	v_fma_f32 v6, v6, v81, 1.0
	v_ashrrev_i32_e32 v83, 31, v82
	v_mul_f32_e32 v10, v10, v7
	v_mul_f32_e32 v16, v9, v6
	v_lshlrev_b64 v[6:7], 9, v[82:83]
	v_or_b32_e32 v6, v6, v31
	v_lshl_add_u64 v[8:9], s[74:75], 0, v[6:7]
	v_cvt_pk_bf16_f32 v12, v12, s0
	global_store_short v[8:9], v12, off
	v_lshl_add_u64 v[8:9], s[76:77], 0, v[6:7]
	v_cvt_pk_bf16_f32 v12, v16, s0
	global_store_short v[8:9], v12, off
	v_lshl_add_u64 v[8:9], s[78:79], 0, v[6:7]
	v_cvt_pk_bf16_f32 v12, v13, s0
	global_store_short v[8:9], v12, off
	v_lshl_add_u64 v[8:9], s[80:81], 0, v[6:7]
	v_cvt_pk_bf16_f32 v12, v10, s0
	v_mul_f32_e32 v10, v14, v10
	global_store_short v[8:9], v12, off
	v_lshl_add_u64 v[8:9], s[82:83], 0, v[6:7]
	v_cvt_pk_bf16_f32 v10, v10, s0
	global_store_short v[8:9], v10, off
	v_lshl_add_u64 v[8:9], s[84:85], 0, v[6:7]
	v_cvt_pk_bf16_f32 v10, v15, s0
	global_store_short v[8:9], v10, off
	v_lshl_add_u64 v[6:7], s[86:87], 0, v[6:7]
	v_cvt_pk_bf16_f32 v8, v11, s0
	v_cndmask_b32_e64 v113, 0, v113, s[50:51]
	global_store_short v[6:7], v8, off
	v_sub_f32_e32 v6, v111, v34
	v_sub_f32_e32 v7, v113, v34
	v_fmac_f32_e32 v34, v6, v2
	v_fmac_f32_e32 v34, v7, v4
	v_mul_f32_e32 v2, v34, v3
	v_mul_f32_e32 v3, v2, v2
	s_nop 1
	v_mov_b32_dpp v3, v3 quad_perm:[1,0,3,2] row_mask:0xf bank_mask:0xf
	global_load_dword v122, v[44:45], off
	v_sub_f32_e32 v4, v116, v109
	v_sub_f32_e32 v6, v117, v109
	v_fmac_f32_e32 v109, v4, v112
	s_waitcnt lgkmcnt(0)
	v_fmac_f32_e32 v3, v2, v2
	s_nop 1
	v_fmac_f32_e32 v109, v6, v110
	v_sub_f32_e32 v6, v114, v79
	v_sub_f32_e32 v7, v115, v79
	v_fmac_f32_e32 v79, v6, v108
	s_waitcnt lgkmcnt(0)
	v_add_f32_dpp v3, v3, v3 quad_perm:[2,3,0,1] row_mask:0xf bank_mask:0xf
	s_nop 1
	v_mul_f32_e32 v6, 0xbfb8aa3b, v97
	v_mul_f32_e32 v8, 0xbfb8aa3b, v95
	v_exp_f32_e32 v6, v6
	v_exp_f32_e32 v8, v8
	s_waitcnt lgkmcnt(0)
	v_add_f32_dpp v3, v3, v3 row_half_mirror row_mask:0xf bank_mask:0xf
	s_nop 1
	v_fmac_f32_e32 v79, v7, v5
	v_add_f32_e32 v5, 1.0, v6
	v_add_f32_e32 v6, 1.0, v8
	v_rcp_f32_e32 v6, v6
	s_waitcnt lgkmcnt(0)
	v_add_f32_dpp v3, v3, v3 row_mirror row_mask:0xf bank_mask:0xf
	v_mov_b32_e32 v4, v3
	s_nop 1
	v_permlane16_swap_b32_e32 v4, v3
	v_rcp_f32_e32 v7, v5
	v_mul_f32_e32 v5, 0xbf1b459e, v6
	v_mul_f32_e32 v6, 0xbfb8aa3b, v90
	v_exp_f32_e32 v6, v6
	s_waitcnt lgkmcnt(0)
	v_add_f32_e32 v3, v3, v4
	v_mov_b32_e32 v4, v3
	s_nop 1
	v_permlane32_swap_b32_e32 v4, v3
	v_mul_f32_e32 v5, 0x3fb8aa3b, v5
	v_exp_f32_e32 v8, v5
	v_add_f32_e32 v5, 1.0, v6
	v_rcp_f32_e32 v5, v5
	s_waitcnt lgkmcnt(0)
	v_add_f32_e32 v3, v3, v4
	v_add_f32_e32 v3, 0x2b8cbccc, v3
	v_rsq_f32_e32 v3, v3
	v_mul_f32_e32 v4, 0xbf1b459e, v5
	v_mul_f32_e32 v4, 0x3fb8aa3b, v4
	v_exp_f32_e32 v6, v4
	v_mul_f32_e32 v9, v2, v3
	v_add_f32_e32 v2, -1.0, v7
	v_fma_f32 v2, v2, v81, 1.0
	v_ashrrev_i32_e32 v81, 31, v80
	v_mul_f32_e32 v10, v34, v2
	v_lshlrev_b64 v[2:3], 9, v[80:81]
	v_or_b32_e32 v2, v2, v31
	v_lshl_add_u64 v[4:5], s[74:75], 0, v[2:3]
	v_cvt_pk_bf16_f32 v11, v109, s0
	global_store_short v[4:5], v11, off
	v_lshl_add_u64 v[4:5], s[76:77], 0, v[2:3]
	v_cvt_pk_bf16_f32 v10, v10, s0
	global_store_short v[4:5], v10, off
	v_lshl_add_u64 v[4:5], s[78:79], 0, v[2:3]
	v_cvt_pk_bf16_f32 v10, v79, s0
	global_store_short v[4:5], v10, off
	v_lshl_add_u64 v[4:5], s[80:81], 0, v[2:3]
	v_cvt_pk_bf16_f32 v10, v9, s0
	v_mul_f32_e32 v7, v7, v9
	global_store_short v[4:5], v10, off
	v_lshl_add_u64 v[4:5], s[82:83], 0, v[2:3]
	v_cvt_pk_bf16_f32 v7, v7, s0
	global_store_short v[4:5], v7, off
	v_lshl_add_u64 v[4:5], s[84:85], 0, v[2:3]
	v_cvt_pk_bf16_f32 v7, v8, s0
	global_store_short v[4:5], v7, off
	v_lshl_add_u64 v[2:3], s[86:87], 0, v[2:3]
	v_cvt_pk_bf16_f32 v4, v6, s0
	global_store_short v[2:3], v4, off
	ds_read2st64_b32 v[116:117], v141 offset1:2
	ds_read_b128 v[2:5], v142 offset:384
	ds_read2st64_b32 v[118:119], v141 offset0:4 offset1:6
	ds_read_b128 v[6:9], v142 offset:400
	ds_read_b128 v[10:13], v142 offset:416
	ds_read_b128 v[14:17], v142 offset:432
	ds_read_b128 v[80:83], v142 offset:896
	s_waitcnt lgkmcnt(5)
	v_mul_f32_e32 v3, v117, v3
	v_fmac_f32_e32 v3, v116, v2
	s_waitcnt lgkmcnt(4)
	v_mul_f32_e32 v2, v119, v5
	v_fmac_f32_e32 v2, v118, v4
	ds_read_b128 v[84:87], v142 offset:1408
	v_add_f32_e32 v2, v3, v2
	ds_read_b128 v[88:91], v142 offset:1920
	ds_read_b128 v[92:95], v142 offset:2432
	ds_read_b128 v[96:99], v142 offset:2944
	s_waitcnt vmcnt(7)
	v_add_f32_e32 v34, v122, v2
	ds_read_b128 v[2:5], v142 offset:912
	s_waitcnt lgkmcnt(5)
	v_mul_f32_e32 v79, v117, v81
	v_fmac_f32_e32 v79, v116, v80
	v_mul_f32_e32 v80, v119, v83
	v_fmac_f32_e32 v80, v118, v82
	v_add_f32_e32 v79, v79, v80
	ds_read_b128 v[80:83], v142 offset:1424
	s_waitcnt lgkmcnt(5)
	v_mul_f32_e32 v85, v117, v85
	v_fmac_f32_e32 v85, v116, v84
	v_mul_f32_e32 v84, v119, v87
	v_fmac_f32_e32 v84, v118, v86
	v_add_f32_e32 v84, v85, v84
	v_add_f32_e32 v120, v122, v84
	ds_read_b128 v[84:87], v142 offset:1936
	s_waitcnt lgkmcnt(5)
	v_mul_f32_e32 v89, v117, v89
	v_fmac_f32_e32 v89, v116, v88
	v_mul_f32_e32 v88, v119, v91
	v_fmac_f32_e32 v88, v118, v90
	v_add_f32_e32 v88, v89, v88
	v_add_f32_e32 v121, v122, v88
	ds_read_b128 v[88:91], v142 offset:2448
	s_waitcnt lgkmcnt(5)
	v_mul_f32_e32 v93, v117, v93
	v_fmac_f32_e32 v93, v116, v92
	v_mul_f32_e32 v92, v119, v95
	v_fmac_f32_e32 v92, v118, v94
	v_add_f32_e32 v92, v93, v92
	ds_read_b128 v[100:103], v142 offset:3456
	v_add_f32_e32 v123, v122, v92
	ds_read_b128 v[92:95], v142 offset:2960
	s_waitcnt lgkmcnt(6)
	v_mul_f32_e32 v97, v117, v97
	v_fmac_f32_e32 v97, v116, v96
	v_mul_f32_e32 v96, v119, v99
	v_fmac_f32_e32 v96, v118, v98
	v_add_f32_e32 v96, v97, v96
	v_add_f32_e32 v124, v122, v96
	ds_read_b128 v[96:99], v142 offset:3472
	s_waitcnt lgkmcnt(2)
	v_mul_f32_e32 v101, v117, v101
	v_fmac_f32_e32 v101, v116, v100
	v_mul_f32_e32 v100, v119, v103
	v_fmac_f32_e32 v100, v118, v102
	v_add_f32_e32 v104, v101, v100
	ds_read_b128 v[100:103], v143 offset:384
	v_add_f32_e32 v125, v122, v104
	ds_read_b128 v[104:107], v143 offset:400
	ds_read_b128 v[108:111], v143 offset:416
	ds_read_b128 v[112:115], v143 offset:432
	v_add_f32_e32 v79, v122, v79
	s_mov_b32 s2, 0xbfb8aa3b
	s_waitcnt lgkmcnt(3)
	v_mul_f32_e32 v117, v117, v101
	v_fmac_f32_e32 v117, v116, v100
	v_mul_f32_e32 v116, v119, v103
	ds_read2st64_b32 v[100:101], v141 offset0:8 offset1:10
	v_fmac_f32_e32 v116, v118, v102
	ds_read2st64_b32 v[102:103], v141 offset0:12 offset1:14
	v_add_f32_e32 v116, v117, v116
	v_add_f32_e32 v116, v122, v116
	s_waitcnt lgkmcnt(1)
	v_mul_f32_e32 v7, v101, v7
	v_mul_f32_e32 v3, v101, v3
	v_fmac_f32_e32 v7, v100, v6
	s_waitcnt lgkmcnt(0)
	v_mul_f32_e32 v6, v103, v9
	v_fmac_f32_e32 v3, v100, v2
	v_mul_f32_e32 v2, v103, v5
	v_fmac_f32_e32 v6, v102, v8
	v_fmac_f32_e32 v2, v102, v4
	v_add_f32_e32 v6, v7, v6
	v_add_f32_e32 v2, v3, v2
	v_add_f32_e32 v6, v34, v6
	v_add_f32_e32 v34, v79, v2
	v_mul_f32_e32 v2, v101, v81
	v_mul_f32_e32 v3, v103, v83
	v_fmac_f32_e32 v2, v100, v80
	v_fmac_f32_e32 v3, v102, v82
	v_add_f32_e32 v2, v2, v3
	v_add_f32_e32 v79, v120, v2
	v_mul_f32_e32 v2, v101, v85
	v_mul_f32_e32 v3, v103, v87
	v_fmac_f32_e32 v2, v100, v84
	v_fmac_f32_e32 v3, v102, v86
	v_add_f32_e32 v2, v2, v3
	v_add_f32_e32 v117, v121, v2
	v_mul_f32_e32 v2, v101, v89
	v_mul_f32_e32 v3, v103, v91
	v_fmac_f32_e32 v2, v100, v88
	v_fmac_f32_e32 v3, v102, v90
	v_add_f32_e32 v2, v2, v3
	v_add_f32_e32 v118, v123, v2
	v_mul_f32_e32 v2, v101, v93
	v_mul_f32_e32 v3, v103, v95
	v_fmac_f32_e32 v2, v100, v92
	v_fmac_f32_e32 v3, v102, v94
	v_add_f32_e32 v2, v2, v3
	v_add_f32_e32 v119, v124, v2
	v_mul_f32_e32 v2, v101, v97
	v_mul_f32_e32 v3, v103, v99
	v_fmac_f32_e32 v2, v100, v96
	v_fmac_f32_e32 v3, v102, v98
	v_add_f32_e32 v2, v2, v3
	ds_read2st64_b32 v[96:97], v141 offset0:16 offset1:18
	ds_read2st64_b32 v[98:99], v141 offset0:20 offset1:22
	v_add_f32_e32 v120, v125, v2
	v_mul_f32_e32 v2, v101, v105
	v_mul_f32_e32 v3, v103, v107
	v_fmac_f32_e32 v2, v100, v104
	v_fmac_f32_e32 v3, v102, v106
	v_add_f32_e32 v2, v2, v3
	v_add_f32_e32 v100, v116, v2
	ds_read_b128 v[2:5], v142 offset:928
	s_waitcnt lgkmcnt(2)
	v_mul_f32_e32 v7, v97, v11
	s_waitcnt lgkmcnt(1)
	v_mul_f32_e32 v8, v99, v13
	v_fmac_f32_e32 v7, v96, v10
	v_fmac_f32_e32 v8, v98, v12
	v_add_f32_e32 v7, v7, v8
	v_add_f32_e32 v101, v6, v7
	ds_read_b128 v[6:9], v142 offset:1440
	ds_read_b128 v[10:13], v142 offset:944
	s_waitcnt lgkmcnt(2)
	v_mul_f32_e32 v3, v97, v3
	v_fmac_f32_e32 v3, v96, v2
	v_mul_f32_e32 v2, v99, v5
	v_fmac_f32_e32 v2, v98, v4
	v_add_f32_e32 v2, v3, v2
	v_add_f32_e32 v34, v34, v2
	ds_read_b128 v[2:5], v142 offset:1456
	s_waitcnt lgkmcnt(2)
	v_mul_f32_e32 v7, v97, v7
	ds_read_b128 v[80:83], v142 offset:1952
	ds_read_b128 v[84:87], v142 offset:1968
	v_fmac_f32_e32 v7, v96, v6
	v_mul_f32_e32 v6, v99, v9
	v_fmac_f32_e32 v6, v98, v8
	v_add_f32_e32 v6, v7, v6
	v_add_f32_e32 v79, v79, v6
	ds_read_b128 v[6:9], v142 offset:2464
	s_waitcnt lgkmcnt(2)
	v_mul_f32_e32 v81, v97, v81
	v_fmac_f32_e32 v81, v96, v80
	v_mul_f32_e32 v80, v99, v83
	v_fmac_f32_e32 v80, v98, v82
	v_add_f32_e32 v80, v81, v80
	v_add_f32_e32 v102, v117, v80
	ds_read_b128 v[80:83], v142 offset:2480
	s_waitcnt lgkmcnt(1)
	v_mul_f32_e32 v7, v97, v7
	ds_read_b128 v[88:91], v142 offset:2976
	ds_read_b128 v[92:95], v142 offset:2992
	v_fmac_f32_e32 v7, v96, v6
	v_mul_f32_e32 v6, v99, v9
	v_fmac_f32_e32 v6, v98, v8
	v_add_f32_e32 v6, v7, v6
	v_add_f32_e32 v103, v118, v6
	ds_read_b128 v[6:9], v142 offset:3488
	s_waitcnt lgkmcnt(2)
	v_mul_f32_e32 v89, v97, v89
	v_fmac_f32_e32 v89, v96, v88
	v_mul_f32_e32 v88, v99, v91
	v_fmac_f32_e32 v88, v98, v90
	v_add_f32_e32 v88, v89, v88
	v_add_f32_e32 v104, v119, v88
	ds_read_b128 v[88:91], v142 offset:3504
	s_waitcnt lgkmcnt(1)
	v_mul_f32_e32 v7, v97, v7
	v_fmac_f32_e32 v7, v96, v6
	v_mul_f32_e32 v6, v99, v9
	v_fmac_f32_e32 v6, v98, v8
	v_add_f32_e32 v6, v7, v6
	v_add_f32_e32 v105, v120, v6
	v_mul_f32_e32 v6, v97, v109
	v_mul_f32_e32 v7, v99, v111
	v_fmac_f32_e32 v6, v96, v108
	ds_read2st64_b32 v[96:97], v141 offset0:24 offset1:26
	v_fmac_f32_e32 v7, v98, v110
	ds_read2st64_b32 v[98:99], v141 offset0:28 offset1:30
	v_add_f32_e32 v6, v6, v7
	v_add_f32_e32 v100, v100, v6
	s_waitcnt lgkmcnt(1)
	v_mul_f32_e32 v6, v97, v15
	v_fmac_f32_e32 v6, v96, v14
	s_waitcnt lgkmcnt(0)
	v_mul_f32_e32 v7, v99, v17
	v_fmac_f32_e32 v7, v98, v16
	v_mul_f32_e32 v3, v97, v3
	v_add_f32_e32 v6, v6, v7
	v_fmac_f32_e32 v3, v96, v2
	v_mul_f32_e32 v2, v99, v5
	v_add_f32_e32 v9, v101, v6
	v_mul_f32_e32 v6, v97, v11
	v_mul_f32_e32 v7, v99, v13
	v_fmac_f32_e32 v2, v98, v4
	v_fmac_f32_e32 v6, v96, v10
	v_fmac_f32_e32 v7, v98, v12
	v_add_f32_e32 v2, v3, v2
	v_add_f32_e32 v6, v6, v7
	v_add_f32_e32 v7, v79, v2
	v_mul_f32_e32 v2, v97, v85
	v_mul_f32_e32 v3, v99, v87
	v_fmac_f32_e32 v2, v96, v84
	v_fmac_f32_e32 v3, v98, v86
	v_add_f32_e32 v2, v2, v3
	v_add_f32_e32 v8, v34, v6
	v_add_f32_e32 v6, v102, v2
	v_mul_f32_e32 v2, v97, v81
	v_mul_f32_e32 v3, v99, v83
	v_fmac_f32_e32 v2, v96, v80
	v_fmac_f32_e32 v3, v98, v82
	v_add_f32_e32 v2, v2, v3
	v_add_f32_e32 v5, v103, v2
	v_mul_f32_e32 v2, v97, v93
	v_mul_f32_e32 v3, v99, v95
	v_fmac_f32_e32 v2, v96, v92
	v_fmac_f32_e32 v3, v98, v94
	v_add_f32_e32 v2, v2, v3
	v_mul_f32_e64 v11, |v9|, s2
	v_add_f32_e32 v3, v104, v2
	v_mul_f32_e32 v2, v97, v89
	v_mul_f32_e32 v4, v99, v91
	v_exp_f32_e32 v11, v11
	v_fmac_f32_e32 v2, v96, v88
	v_fmac_f32_e32 v4, v98, v90
	v_add_f32_e32 v2, v2, v4
	v_mul_f32_e32 v4, v97, v113
	v_mul_f32_e32 v10, v99, v115
	v_fmac_f32_e32 v4, v96, v112
	v_fmac_f32_e32 v10, v98, v114
	v_add_f32_e32 v4, v4, v10
	v_add_f32_e32 v10, 1.0, v11
	v_log_f32_e32 v10, v10
	v_max_f32_e64 v9, -v9, 0
	s_ashr_i32 s89, s88, 31
	v_lshl_add_u64 v[12:13], v[46:47], 0, s[88:89]
	v_fmac_f32_e32 v9, 0x3f317218, v10
	v_mul_f32_e64 v10, |v8|, s2
	v_exp_f32_e32 v14, v10
	v_lshlrev_b64 v[10:11], 9, v[12:13]
	v_add_f32_e32 v4, v100, v4
	v_mul_f32_e32 v9, 0xbd800000, v9
	v_lshl_add_u64 v[100:101], v[48:49], 0, v[10:11]
	global_store_dword v[100:101], v9, off
	v_add_f32_e32 v9, 1.0, v14
	v_log_f32_e32 v9, v9
	v_mul_f32_e64 v10, |v7|, s2
	v_exp_f32_e32 v10, v10
	v_max_f32_e64 v8, -v8, 0
	v_fmac_f32_e32 v8, 0x3f317218, v9
	v_mul_f32_e32 v8, 0xbd800000, v8
	global_store_dword v[100:101], v8, off offset:512
	v_add_f32_e32 v8, 1.0, v10
	v_log_f32_e32 v8, v8
	v_mul_f32_e64 v9, |v6|, s2
	v_exp_f32_e32 v9, v9
	v_max_f32_e64 v7, -v7, 0
	v_fmac_f32_e32 v7, 0x3f317218, v8
	v_mul_f32_e32 v7, 0xbd800000, v7
	global_store_dword v[100:101], v7, off offset:1024
	v_add_f32_e32 v7, 1.0, v9
	v_log_f32_e32 v7, v7
	v_mul_f32_e64 v8, |v5|, s2
	v_exp_f32_e32 v8, v8
	v_max_f32_e64 v6, -v6, 0
	v_fmac_f32_e32 v6, 0x3f317218, v7
	v_mul_f32_e32 v6, 0xbd800000, v6
	global_store_dword v[100:101], v6, off offset:1536
	v_add_f32_e32 v6, 1.0, v8
	v_log_f32_e32 v6, v6
	v_mul_f32_e64 v7, |v3|, s2
	v_exp_f32_e32 v7, v7
	v_max_f32_e64 v5, -v5, 0
	v_fmac_f32_e32 v5, 0x3f317218, v6
	v_add_f32_e32 v2, v105, v2
	v_mul_f32_e32 v5, 0xbd800000, v5
	global_store_dword v[100:101], v5, off offset:2048
	v_add_f32_e32 v5, 1.0, v7
	v_mul_f32_e64 v6, |v2|, s2
	v_log_f32_e32 v5, v5
	v_exp_f32_e32 v6, v6
	v_max_f32_e64 v3, -v3, 0
	s_add_i32 s4, s88, -2
	v_fmac_f32_e32 v3, 0x3f317218, v5
	v_add_f32_e32 v5, 1.0, v6
	v_mul_f32_e64 v6, |v4|, s2
	v_exp_f32_e32 v6, v6
	v_log_f32_e32 v5, v5
	v_mul_f32_e32 v3, 0xbd800000, v3
	v_mad_i64_i32 v[102:103], s[2:3], s88, v202, v[76:77]
	s_cmp_ge_i32 s4, s1
	global_store_dword v[100:101], v3, off offset:2560
	v_add_f32_e32 v3, 1.0, v6
	s_cselect_b64 s[2:3], -1, 0
	s_cmp_lt_i32 s4, s0
	v_max_f32_e64 v2, -v2, 0
	v_log_f32_e32 v3, v3
	s_cselect_b64 s[4:5], -1, 0
	v_fmac_f32_e32 v2, 0x3f317218, v5
	s_and_b64 vcc, s[2:3], s[4:5]
	v_mul_f32_e32 v2, 0xbd800000, v2
	s_and_b64 s[2:3], vcc, exec
	global_store_dword v[100:101], v2, off offset:3072
	v_max_f32_e64 v2, -v4, 0
	s_cselect_b32 s3, -1, 0
	s_cselect_b32 s2, 0xffffcc00, 0
	s_add_i32 s4, s88, -1
	v_fmac_f32_e32 v2, 0x3f317218, v3
	s_cmp_ge_i32 s4, s1
	v_mul_f32_e32 v34, 0xbd800000, v2
	v_lshl_add_u64 v[2:3], v[102:103], 0, s[2:3]
	s_cselect_b64 s[2:3], -1, 0
	s_cmp_lt_i32 s4, s0
	s_cselect_b64 s[4:5], -1, 0
	s_and_b64 s[2:3], s[2:3], s[4:5]
	s_and_b64 s[4:5], s[2:3], exec
	s_cselect_b32 s5, -1, 0
	s_cselect_b32 s4, 0xffffe600, 0
	s_cmp_ge_i32 s88, s1
	v_lshl_add_u64 v[4:5], v[102:103], 0, s[4:5]
	s_cselect_b64 s[4:5], -1, 0
	s_cmp_lt_i32 s88, s0
	s_cselect_b64 s[6:7], -1, 0
	s_and_b64 s[4:5], s[4:5], s[6:7]
	s_or_b32 s10, s88, 1
	s_cmp_ge_i32 s10, s1
	s_cselect_b64 s[6:7], -1, 0
	s_cmp_lt_i32 s10, s0
	s_cselect_b64 s[8:9], -1, 0
	s_and_b64 s[40:41], s[6:7], s[8:9]
	s_and_b64 s[6:7], s[40:41], exec
	s_cselect_b32 s6, 0x1a00, 0
	s_mov_b32 s72, 0
	s_or_b32 s14, s88, 2
	s_mov_b32 s73, 1
	s_mov_b32 s7, s72
	s_cmp_ge_i32 s14, s1
	v_lshl_add_u64 v[6:7], v[102:103], 0, s[6:7]
	s_cselect_b64 s[6:7], -1, 0
	s_cmp_lt_i32 s14, s0
	s_cselect_b64 s[8:9], -1, 0
	s_and_b64 s[42:43], s[6:7], s[8:9]
	s_and_b64 s[6:7], s[42:43], exec
	s_cselect_b32 s6, 0x3400, 0
	s_mov_b32 s7, s72
	v_lshl_add_u64 v[8:9], v[102:103], 0, s[6:7]
	s_or_b32 s6, s88, 3
	s_cmp_ge_i32 s6, s1
	s_cselect_b64 s[8:9], -1, 0
	s_cmp_lt_i32 s6, s0
	s_cselect_b64 s[18:19], -1, 0
	s_and_b64 s[44:45], s[8:9], s[18:19]
	s_and_b64 s[8:9], s[44:45], exec
	s_cselect_b32 s8, 0x4e00, 0
	s_mov_b32 s9, s72
	v_lshl_add_u64 v[10:11], v[102:103], 0, s[8:9]
	s_or_b32 s8, s88, 4
	s_cmp_ge_i32 s8, s1
	s_cselect_b64 s[18:19], -1, 0
	s_cmp_lt_i32 s8, s0
	s_cselect_b64 s[22:23], -1, 0
	s_and_b64 s[46:47], s[18:19], s[22:23]
	s_and_b64 s[18:19], s[46:47], exec
	s_cselect_b32 s18, 0x6800, 0
	s_or_b32 s34, s88, 5
	s_mov_b32 s19, s72
	s_cmp_ge_i32 s34, s1
	v_lshl_add_u64 v[12:13], v[102:103], 0, s[18:19]
	s_cselect_b64 s[18:19], -1, 0
	s_cmp_lt_i32 s34, s0
	s_cselect_b64 s[22:23], -1, 0
	s_and_b64 s[48:49], s[18:19], s[22:23]
	s_and_b64 s[18:19], s[48:49], exec
	s_cselect_b32 s18, 0x8200, 0
	s_or_b32 s36, s88, 6
	s_mov_b32 s19, s72
	s_cmp_ge_i32 s36, s1
	v_lshl_add_u64 v[14:15], v[102:103], 0, s[18:19]
	s_cselect_b64 s[18:19], -1, 0
	s_cmp_lt_i32 s36, s0
	s_cselect_b64 s[22:23], -1, 0
	s_and_b64 s[50:51], s[18:19], s[22:23]
	s_and_b64 s[18:19], s[50:51], exec
	s_cselect_b32 s18, 0x9c00, 0
	s_or_b32 s28, s88, 7
	s_mov_b32 s19, s72
	s_cmp_ge_i32 s28, s1
	v_lshl_add_u64 v[16:17], v[102:103], 0, s[18:19]
	s_cselect_b64 s[18:19], -1, 0
	s_cmp_lt_i32 s28, s0
	s_cselect_b64 s[22:23], -1, 0
	s_and_b64 s[52:53], s[18:19], s[22:23]
	s_and_b64 s[18:19], s[52:53], exec
	s_cselect_b32 s18, 0xb600, 0
	s_or_b32 s30, s88, 8
	s_mov_b32 s19, s72
	s_cmp_ge_i32 s30, s1
	v_lshl_add_u64 v[80:81], v[102:103], 0, s[18:19]
	s_cselect_b64 s[18:19], -1, 0
	s_cmp_lt_i32 s30, s0
	s_cselect_b64 s[22:23], -1, 0
	s_and_b64 s[54:55], s[18:19], s[22:23]
	s_and_b64 s[18:19], s[54:55], exec
	s_cselect_b32 s18, 0xd000, 0
	s_or_b32 s24, s88, 9
	s_mov_b32 s19, s72
	s_cmp_ge_i32 s24, s1
	v_lshl_add_u64 v[82:83], v[102:103], 0, s[18:19]
	s_cselect_b64 s[18:19], -1, 0
	s_cmp_lt_i32 s24, s0
	s_cselect_b64 s[22:23], -1, 0
	s_and_b64 s[56:57], s[18:19], s[22:23]
	s_and_b64 s[18:19], s[56:57], exec
	s_cselect_b32 s18, 0xea00, 0
	s_or_b32 s26, s88, 10
	s_mov_b32 s19, s72
	s_cmp_ge_i32 s26, s1
	v_lshl_add_u64 v[84:85], v[102:103], 0, s[18:19]
	s_cselect_b64 s[18:19], -1, 0
	s_cmp_lt_i32 s26, s0
	s_cselect_b64 s[22:23], -1, 0
	s_and_b64 s[58:59], s[18:19], s[22:23]
	s_and_b64 s[18:19], s[58:59], exec
	s_cselect_b32 s18, 0x10400, 0
	s_mov_b32 s19, s72
	v_lshl_add_u64 v[86:87], v[102:103], 0, s[18:19]
	s_or_b32 s18, s88, 11
	s_cmp_ge_i32 s18, s1
	s_cselect_b64 s[22:23], -1, 0
	s_cmp_lt_i32 s18, s0
	s_cselect_b64 s[60:61], -1, 0
	s_and_b64 s[60:61], s[22:23], s[60:61]
	s_and_b64 s[22:23], s[60:61], exec
	s_cselect_b32 s22, 0x11e00, 0
	s_mov_b32 s23, s72
	v_lshl_add_u64 v[88:89], v[102:103], 0, s[22:23]
	s_or_b32 s22, s88, 12
	s_cmp_ge_i32 s22, s1
	s_cselect_b64 s[62:63], -1, 0
	s_cmp_lt_i32 s22, s0
	s_cselect_b64 s[64:65], -1, 0
	s_and_b64 s[62:63], s[62:63], s[64:65]
	s_and_b64 s[64:65], s[62:63], exec
	s_cselect_b32 s64, 0x13800, 0
	s_or_b32 s92, s88, 13
	s_mov_b32 s65, s72
	s_cmp_ge_i32 s92, s1
	v_lshl_add_u64 v[90:91], v[102:103], 0, s[64:65]
	s_cselect_b64 s[64:65], -1, 0
	s_cmp_lt_i32 s92, s0
	s_cselect_b64 s[66:67], -1, 0
	s_and_b64 s[64:65], s[64:65], s[66:67]
	s_and_b64 s[66:67], s[64:65], exec
	s_cselect_b32 s66, 0x15200, 0
	s_or_b32 s94, s88, 14
	s_mov_b32 s67, s72
	s_cmp_ge_i32 s94, s1
	v_lshl_add_u64 v[92:93], v[102:103], 0, s[66:67]
	s_cselect_b64 s[66:67], -1, 0
	s_cmp_lt_i32 s94, s0
	s_cselect_b64 s[68:69], -1, 0
	s_and_b64 s[66:67], s[66:67], s[68:69]
	s_and_b64 s[68:69], s[66:67], exec
	s_cselect_b32 s68, 0x16c00, 0
	s_or_b32 s90, s88, 15
	s_mov_b32 s69, s72
	s_cmp_ge_i32 s90, s1
	v_lshl_add_u64 v[94:95], v[102:103], 0, s[68:69]
	s_cselect_b64 s[68:69], -1, 0
	s_cmp_lt_i32 s90, s0
	s_cselect_b64 s[70:71], -1, 0
	s_and_b64 s[70:71], s[68:69], s[70:71]
	s_and_b64 s[68:69], s[70:71], exec
	s_cselect_b32 s68, 0x18600, 0
	s_add_i32 s7, s88, 16
	s_mov_b32 s69, s72
	s_cmp_ge_i32 s7, s1
	v_lshl_add_u64 v[96:97], v[102:103], 0, s[68:69]
	s_cselect_b64 s[68:69], -1, 0
	s_cmp_lt_i32 s7, s0
	s_cselect_b64 s[0:1], -1, 0
	s_and_b64 s[68:69], s[68:69], s[0:1]
	s_and_b64 s[0:1], s[68:69], exec
	global_load_ushort v79, v[2:3], off
	global_load_ushort v104, v[4:5], off
	global_load_ushort v105, v[102:103], off
	global_load_ushort v106, v[6:7], off
	global_load_ushort v107, v[8:9], off
	global_load_ushort v108, v[10:11], off
	global_load_ushort v109, v[12:13], off
	s_cselect_b32 s0, 0x1a000, 0
	s_mov_b32 s1, s72
	global_load_ushort v118, v[14:15], off
	global_load_ushort v119, v[16:17], off
	global_load_ushort v120, v[80:81], off
	global_load_ushort v121, v[82:83], off
	global_load_ushort v122, v[84:85], off
	global_load_ushort v123, v[86:87], off
	global_load_ushort v124, v[88:89], off
	global_load_ushort v125, v[90:91], off
	global_load_ushort v126, v[92:93], off
	global_load_ushort v127, v[94:95], off
	global_load_ushort v128, v[96:97], off
	v_lshl_add_u64 v[98:99], v[102:103], 0, s[0:1]
	global_store_dword v[100:101], v34, off offset:3584
	global_load_ushort v129, v[98:99], off
	global_load_dword v117, v[52:53], off
	global_load_dword v116, v[50:51], off
	global_load_dword v133, v[54:55], off
	global_load_dword v134, v[56:57], off
	global_load_dword v136, v[58:59], off
	global_load_ushort v132, v[102:103], off offset:1024
	s_lshl_b64 s[0:1], s[88:89], 11
	s_ashr_i32 s11, s10, 31
	s_ashr_i32 s15, s14, 31
	s_ashr_i32 s7, s6, 31
	s_ashr_i32 s9, s8, 31
	s_ashr_i32 s35, s34, 31
	s_ashr_i32 s37, s36, 31
	s_ashr_i32 s29, s28, 31
	s_ashr_i32 s31, s30, 31
	s_ashr_i32 s25, s24, 31
	s_ashr_i32 s27, s26, 31
	s_ashr_i32 s19, s18, 31
	s_ashr_i32 s23, s22, 31
	s_ashr_i32 s93, s92, 31
	s_ashr_i32 s95, s94, 31
	s_ashr_i32 s91, s90, 31
	s_mov_b32 s97, 0xbfb8aa3b
	s_waitcnt vmcnt(25)
	v_lshlrev_b32_e32 v34, 16, v79
	v_cndmask_b32_e32 v79, 0, v34, vcc
	s_waitcnt vmcnt(24)
	v_lshlrev_b32_e32 v34, 16, v104
	v_cndmask_b32_e64 v115, 0, v34, s[2:3]
	s_waitcnt vmcnt(23)
	v_lshlrev_b32_e32 v34, 16, v105
	v_cndmask_b32_e64 v114, 0, v34, s[4:5]
	s_waitcnt vmcnt(22)
	v_lshlrev_b32_e32 v34, 16, v106
	v_cndmask_b32_e64 v113, 0, v34, s[40:41]
	s_waitcnt vmcnt(21)
	v_lshlrev_b32_e32 v34, 16, v107
	s_waitcnt vmcnt(5)
	v_mul_f32_e32 v101, v117, v115
	s_waitcnt vmcnt(4)
	v_fmac_f32_e32 v101, v116, v79
	v_cndmask_b32_e64 v112, 0, v34, s[42:43]
	v_lshlrev_b32_e32 v34, 16, v108
	s_waitcnt vmcnt(3)
	v_fmac_f32_e32 v101, v133, v114
	v_cndmask_b32_e64 v111, 0, v34, s[44:45]
	v_lshlrev_b32_e32 v34, 16, v109
	s_waitcnt vmcnt(2)
	v_fmac_f32_e32 v101, v134, v113
	v_cndmask_b32_e64 v110, 0, v34, s[46:47]
	v_lshlrev_b32_e32 v34, 16, v118
	s_waitcnt vmcnt(1)
	v_add_f32_e32 v118, v136, v101
	v_mul_f32_e32 v101, 0xbfb8aa3b, v118
	v_cndmask_b32_e64 v109, 0, v34, s[48:49]
	v_lshlrev_b32_e32 v34, 16, v119
	v_exp_f32_e32 v119, v101
	v_cndmask_b32_e64 v108, 0, v34, s[50:51]
	v_lshlrev_b32_e32 v34, 16, v120
	v_mul_f32_e32 v120, v117, v114
	v_fmac_f32_e32 v120, v116, v115
	v_fmac_f32_e32 v120, v133, v113
	v_add_f32_e32 v119, 1.0, v119
	v_fmac_f32_e32 v120, v134, v112
	v_rcp_f32_e32 v119, v119
	v_add_f32_e32 v115, v136, v120
	v_mul_f32_e32 v120, 0xbfb8aa3b, v115
	v_exp_f32_e32 v120, v120
	v_lshlrev_b32_e32 v100, 16, v129
	v_mul_f32_e32 v118, v118, v119
	v_cndmask_b32_e64 v145, 0, v100, s[68:69]
	v_lshl_add_u64 v[100:101], v[60:61], 0, s[0:1]
	v_cvt_pk_bf16_f32 v118, v118, s0
	v_cndmask_b32_e64 v107, 0, v34, s[52:53]
	v_lshlrev_b32_e32 v34, 16, v121
	global_store_short v[100:101], v118, off
	v_add_f32_e32 v118, 1.0, v120
	v_cndmask_b32_e64 v105, 0, v34, s[54:55]
	v_lshlrev_b32_e32 v34, 16, v122
	v_rcp_f32_e32 v118, v118
	v_cndmask_b32_e64 v104, 0, v34, s[56:57]
	v_lshlrev_b32_e32 v34, 16, v123
	v_cndmask_b32_e64 v103, 0, v34, s[58:59]
	v_lshlrev_b32_e32 v34, 16, v124
	v_cndmask_b32_e64 v102, 0, v34, s[60:61]
	v_lshlrev_b32_e32 v34, 16, v125
	v_cndmask_b32_e64 v106, 0, v34, s[62:63]
	v_lshlrev_b32_e32 v34, 16, v126
	s_lshl_b64 s[0:1], s[10:11], 11
	v_mul_f32_e32 v115, v115, v118
	v_cndmask_b32_e64 v138, 0, v34, s[64:65]
	v_lshlrev_b32_e32 v34, 16, v127
	v_lshl_add_u64 v[126:127], v[60:61], 0, s[0:1]
	v_cvt_pk_bf16_f32 v115, v115, s0
	global_store_short v[126:127], v115, off
	v_mul_f32_e32 v115, v117, v113
	v_fmac_f32_e32 v115, v116, v114
	v_fmac_f32_e32 v115, v133, v112
	v_fmac_f32_e32 v115, v134, v111
	v_add_f32_e32 v114, v136, v115
	v_mul_f32_e32 v115, 0xbfb8aa3b, v114
	v_exp_f32_e32 v115, v115
	v_mul_f32_e32 v118, v117, v112
	v_fmac_f32_e32 v118, v116, v113
	v_fmac_f32_e32 v118, v133, v111
	v_add_f32_e32 v115, 1.0, v115
	v_fmac_f32_e32 v118, v134, v110
	v_rcp_f32_e32 v115, v115
	v_add_f32_e32 v113, v136, v118
	v_mul_f32_e32 v118, 0xbfb8aa3b, v113
	v_exp_f32_e32 v118, v118
	s_lshl_b64 s[0:1], s[14:15], 11
	v_mul_f32_e32 v114, v114, v115
	v_lshl_add_u64 v[130:131], v[60:61], 0, s[0:1]
	v_cvt_pk_bf16_f32 v114, v114, s0
	global_store_short v[130:131], v114, off
	v_add_f32_e32 v114, 1.0, v118
	v_rcp_f32_e32 v114, v114
	s_lshl_b64 s[0:1], s[6:7], 11
	v_lshl_add_u64 v[122:123], v[60:61], 0, s[0:1]
	v_cndmask_b32_e64 v140, 0, v34, s[66:67]
	v_mul_f32_e32 v113, v113, v114
	v_cvt_pk_bf16_f32 v113, v113, s0
	global_store_short v[122:123], v113, off
	v_mul_f32_e32 v113, v117, v111
	v_fmac_f32_e32 v113, v116, v112
	v_fmac_f32_e32 v113, v133, v110
	v_fmac_f32_e32 v113, v134, v109
	v_add_f32_e32 v112, v136, v113
	v_mul_f32_e32 v113, 0xbfb8aa3b, v112
	v_exp_f32_e32 v113, v113
	v_mul_f32_e32 v114, v117, v110
	v_fmac_f32_e32 v114, v116, v111
	v_fmac_f32_e32 v114, v133, v109
	v_add_f32_e32 v113, 1.0, v113
	v_fmac_f32_e32 v114, v134, v108
	v_rcp_f32_e32 v113, v113
	v_add_f32_e32 v111, v136, v114
	v_mul_f32_e32 v114, 0xbfb8aa3b, v111
	v_exp_f32_e32 v114, v114
	s_lshl_b64 s[0:1], s[8:9], 11
	v_mul_f32_e32 v112, v112, v113
	v_lshlrev_b32_e32 v34, 16, v128
	v_lshl_add_u64 v[128:129], v[60:61], 0, s[0:1]
	v_cvt_pk_bf16_f32 v112, v112, s0
	global_store_short v[128:129], v112, off
	v_add_f32_e32 v112, 1.0, v114
	v_rcp_f32_e32 v112, v112
	s_lshl_b64 s[0:1], s[34:35], 11
	v_lshl_add_u64 v[118:119], v[60:61], 0, s[0:1]
	v_mul_f32_e32 v146, v117, v106
	v_mul_f32_e32 v111, v111, v112
	v_cvt_pk_bf16_f32 v111, v111, s0
	global_store_short v[118:119], v111, off
	v_mul_f32_e32 v111, v117, v109
	v_fmac_f32_e32 v111, v116, v110
	v_fmac_f32_e32 v111, v133, v108
	v_fmac_f32_e32 v111, v134, v107
	v_add_f32_e32 v110, v136, v111
	v_mul_f32_e32 v111, 0xbfb8aa3b, v110
	v_exp_f32_e32 v111, v111
	v_mul_f32_e32 v112, v117, v108
	v_fmac_f32_e32 v112, v116, v109
	v_fmac_f32_e32 v112, v133, v107
	v_add_f32_e32 v111, 1.0, v111
	v_fmac_f32_e32 v112, v134, v105
	v_rcp_f32_e32 v111, v111
	v_add_f32_e32 v109, v136, v112
	v_mul_f32_e32 v112, 0xbfb8aa3b, v109
	v_exp_f32_e32 v112, v112
	s_lshl_b64 s[0:1], s[36:37], 11
	v_mul_f32_e32 v110, v110, v111
	v_lshl_add_u64 v[124:125], v[60:61], 0, s[0:1]
	v_cvt_pk_bf16_f32 v110, v110, s0
	global_store_short v[124:125], v110, off
	v_add_f32_e32 v110, 1.0, v112
	v_rcp_f32_e32 v110, v110
	s_lshl_b64 s[0:1], s[28:29], 11
	v_lshl_add_u64 v[112:113], v[60:61], 0, s[0:1]
	v_fmac_f32_e32 v146, v116, v102
	v_mul_f32_e32 v109, v109, v110
	v_cvt_pk_bf16_f32 v109, v109, s0
	global_store_short v[112:113], v109, off
	v_mul_f32_e32 v109, v117, v107
	v_fmac_f32_e32 v109, v116, v108
	v_fmac_f32_e32 v109, v133, v105
	v_fmac_f32_e32 v109, v134, v104
	v_add_f32_e32 v108, v136, v109
	v_mul_f32_e32 v109, 0xbfb8aa3b, v108
	v_exp_f32_e32 v109, v109
	v_mul_f32_e32 v110, v117, v105
	v_fmac_f32_e32 v110, v116, v107
	v_fmac_f32_e32 v110, v133, v104
	v_add_f32_e32 v109, 1.0, v109
	v_fmac_f32_e32 v110, v134, v103
	v_rcp_f32_e32 v109, v109
	v_add_f32_e32 v107, v136, v110
	v_mul_f32_e32 v110, 0xbfb8aa3b, v107
	v_exp_f32_e32 v110, v110
	s_lshl_b64 s[0:1], s[30:31], 11
	v_mul_f32_e32 v108, v108, v109
	v_lshl_add_u64 v[120:121], v[60:61], 0, s[0:1]
	v_cvt_pk_bf16_f32 v108, v108, s0
	global_store_short v[120:121], v108, off
	v_add_f32_e32 v108, 1.0, v110
	v_rcp_f32_e32 v110, v108
	s_lshl_b64 s[0:1], s[24:25], 11
	v_lshl_add_u64 v[108:109], v[60:61], 0, s[0:1]
	v_fmac_f32_e32 v146, v133, v138
	v_mul_f32_e32 v107, v107, v110
	v_cvt_pk_bf16_f32 v107, v107, s0
	global_store_short v[108:109], v107, off
	v_mul_f32_e32 v107, v117, v104
	v_fmac_f32_e32 v107, v116, v105
	v_fmac_f32_e32 v107, v133, v103
	v_fmac_f32_e32 v107, v134, v102
	v_add_f32_e32 v105, v136, v107
	v_mul_f32_e32 v110, v117, v103
	v_mul_f32_e32 v107, 0xbfb8aa3b, v105
	v_fmac_f32_e32 v110, v116, v104
	v_exp_f32_e32 v107, v107
	v_fmac_f32_e32 v110, v133, v102
	v_fmac_f32_e32 v110, v134, v106
	v_add_f32_e32 v110, v136, v110
	v_mul_f32_e32 v104, 0xbfb8aa3b, v110
	v_add_f32_e32 v107, 1.0, v107
	v_exp_f32_e32 v104, v104
	v_rcp_f32_e32 v107, v107
	s_lshl_b64 s[0:1], s[26:27], 11
	v_lshl_add_u64 v[114:115], v[60:61], 0, s[0:1]
	v_add_f32_e32 v104, 1.0, v104
	v_mul_f32_e32 v105, v105, v107
	v_rcp_f32_e32 v107, v104
	v_cvt_pk_bf16_f32 v105, v105, s0
	s_lshl_b64 s[0:1], s[18:19], 11
	global_store_short v[114:115], v105, off
	v_mul_f32_e32 v107, v110, v107
	v_lshl_add_u64 v[104:105], v[60:61], 0, s[0:1]
	v_cvt_pk_bf16_f32 v107, v107, s0
	global_store_short v[104:105], v107, off
	v_mul_f32_e32 v107, v117, v102
	v_fmac_f32_e32 v107, v116, v103
	v_fmac_f32_e32 v107, v133, v106
	v_fmac_f32_e32 v107, v134, v138
	v_add_f32_e32 v103, v136, v107
	v_mul_f32_e32 v107, 0xbfb8aa3b, v103
	v_exp_f32_e32 v107, v107
	v_fmac_f32_e32 v146, v134, v140
	v_add_f32_e32 v146, v136, v146
	v_mul_f32_e32 v102, 0xbfb8aa3b, v146
	v_add_f32_e32 v107, 1.0, v107
	v_exp_f32_e32 v102, v102
	v_rcp_f32_e32 v107, v107
	s_lshl_b64 s[0:1], s[22:23], 11
	v_lshl_add_u64 v[110:111], v[60:61], 0, s[0:1]
	v_add_f32_e32 v102, 1.0, v102
	v_mul_f32_e32 v103, v103, v107
	v_rcp_f32_e32 v107, v102
	v_cvt_pk_bf16_f32 v103, v103, s0
	s_lshl_b64 s[0:1], s[92:93], 11
	global_store_short v[110:111], v103, off
	v_mul_f32_e32 v107, v146, v107
	v_lshl_add_u64 v[102:103], v[60:61], 0, s[0:1]
	v_cvt_pk_bf16_f32 v107, v107, s0
	global_store_short v[102:103], v107, off
	v_mul_f32_e32 v107, v117, v138
	v_fmac_f32_e32 v107, v116, v106
	v_mul_f32_e32 v117, v117, v140
	v_cndmask_b32_e64 v144, 0, v34, s[70:71]
	v_fmac_f32_e32 v107, v133, v140
	v_fmac_f32_e32 v117, v116, v138
	v_fmac_f32_e32 v107, v134, v144
	v_fmac_f32_e32 v117, v133, v144
	v_add_f32_e32 v146, v136, v107
	v_fmac_f32_e32 v117, v134, v145
	v_mul_f32_e32 v106, 0xbfb8aa3b, v146
	v_add_f32_e32 v133, v136, v117
	v_exp_f32_e32 v147, v106
	v_mul_f32_e32 v116, 0xbfb8aa3b, v133
	v_exp_f32_e32 v116, v116
	s_lshl_b64 s[0:1], s[94:95], 11
	v_add_f32_e32 v147, 1.0, v147
	v_rcp_f32_e32 v147, v147
	v_add_f32_e32 v116, 1.0, v116
	v_rcp_f32_e32 v134, v116
	v_lshl_add_u64 v[106:107], v[60:61], 0, s[0:1]
	v_mul_f32_e32 v117, v146, v147
	v_cvt_pk_bf16_f32 v117, v117, s0
	s_lshl_b64 s[0:1], s[90:91], 11
	v_mul_f32_e32 v133, v133, v134
	global_store_short v[106:107], v117, off
	v_lshl_add_u64 v[116:117], v[60:61], 0, s[0:1]
	v_cvt_pk_bf16_f32 v133, v133, s0
	global_load_dword v34, v[50:51], off offset:2048
	global_load_dword v79, v[58:59], off offset:2048
	s_nop 0
	global_store_short v[116:117], v133, off
	global_load_ushort v2, v[2:3], off offset:1024
	s_nop 0
	global_load_ushort v3, v[4:5], off offset:1024
	s_nop 0
	global_load_ushort v4, v[6:7], off offset:1024
	global_load_ushort v5, v[8:9], off offset:1024
	s_nop 0
	global_load_ushort v6, v[10:11], off offset:1024
	global_load_ushort v7, v[12:13], off offset:1024
	global_load_ushort v8, v[14:15], off offset:1024
	global_load_ushort v9, v[16:17], off offset:1024
	s_nop 0
	global_load_ushort v10, v[80:81], off offset:1024
	global_load_ushort v11, v[82:83], off offset:1024
	global_load_ushort v12, v[84:85], off offset:1024
	global_load_ushort v13, v[86:87], off offset:1024
	global_load_ushort v14, v[88:89], off offset:1024
	global_load_ushort v15, v[90:91], off offset:1024
	global_load_ushort v16, v[92:93], off offset:1024
	global_load_ushort v17, v[94:95], off offset:1024
	global_load_ushort v80, v[96:97], off offset:1024
	global_load_ushort v81, v[98:99], off offset:1024
	global_load_dword v82, v[62:63], off
	global_load_dword v83, v[64:65], off
	global_load_dword v84, v[66:67], off
	s_waitcnt vmcnt(39)
	v_lshlrev_b32_e32 v85, 16, v132
	v_cndmask_b32_e64 v85, 0, v85, s[4:5]
	s_waitcnt vmcnt(20)
	v_lshlrev_b32_e32 v2, 16, v2
	s_waitcnt vmcnt(19)
	v_lshlrev_b32_e32 v3, 16, v3
	v_cndmask_b32_e64 v3, 0, v3, s[2:3]
	v_cndmask_b32_e32 v2, 0, v2, vcc
	s_waitcnt vmcnt(18)
	v_lshlrev_b32_e32 v4, 16, v4
	v_cndmask_b32_e64 v4, 0, v4, s[40:41]
	s_waitcnt vmcnt(17)
	v_lshlrev_b32_e32 v5, 16, v5
	v_cndmask_b32_e64 v5, 0, v5, s[42:43]
	s_waitcnt vmcnt(16)
	v_lshlrev_b32_e32 v6, 16, v6
	v_cndmask_b32_e64 v6, 0, v6, s[44:45]
	s_waitcnt vmcnt(15)
	v_lshlrev_b32_e32 v7, 16, v7
	v_cndmask_b32_e64 v7, 0, v7, s[46:47]
	s_waitcnt vmcnt(14)
	v_lshlrev_b32_e32 v8, 16, v8
	v_cndmask_b32_e64 v8, 0, v8, s[48:49]
	s_waitcnt vmcnt(13)
	v_lshlrev_b32_e32 v9, 16, v9
	v_cndmask_b32_e64 v9, 0, v9, s[50:51]
	s_waitcnt vmcnt(12)
	v_lshlrev_b32_e32 v10, 16, v10
	v_cndmask_b32_e64 v10, 0, v10, s[52:53]
	s_waitcnt vmcnt(2)
	v_mul_f32_e32 v86, v82, v3
	v_fmac_f32_e32 v86, v34, v2
	s_waitcnt vmcnt(1)
	v_fmac_f32_e32 v86, v83, v85
	v_mul_f32_e32 v87, v82, v85
	s_waitcnt vmcnt(0)
	v_fmac_f32_e32 v86, v84, v4
	v_fmac_f32_e32 v87, v34, v3
	v_add_f32_e32 v2, v79, v86
	v_fmac_f32_e32 v87, v83, v4
	v_mul_f32_e32 v86, 0xbfb8aa3b, v2
	v_fmac_f32_e32 v87, v84, v5
	v_exp_f32_e32 v86, v86
	v_add_f32_e32 v3, v79, v87
	v_mul_f32_e32 v87, 0xbfb8aa3b, v3
	v_exp_f32_e32 v87, v87
	v_add_f32_e32 v86, 1.0, v86
	v_rcp_f32_e32 v86, v86
	v_lshlrev_b32_e32 v11, 16, v11
	v_add_f32_e32 v87, 1.0, v87
	v_rcp_f32_e32 v87, v87
	v_mul_f32_e32 v2, v2, v86
	v_cvt_pk_bf16_f32 v2, v2, s0
	global_store_short v[100:101], v2, off offset:1024
	v_mul_f32_e32 v2, v3, v87
	v_mul_f32_e32 v3, v82, v4
	v_fmac_f32_e32 v3, v34, v85
	v_fmac_f32_e32 v3, v83, v5
	v_fmac_f32_e32 v3, v84, v6
	v_add_f32_e32 v3, v79, v3
	v_mul_f32_e32 v85, 0xbfb8aa3b, v3
	v_exp_f32_e32 v85, v85
	v_mul_f32_e32 v86, v82, v5
	v_fmac_f32_e32 v86, v34, v4
	v_fmac_f32_e32 v86, v83, v6
	v_fmac_f32_e32 v86, v84, v7
	v_add_f32_e32 v85, 1.0, v85
	v_add_f32_e32 v4, v79, v86
	v_rcp_f32_e32 v85, v85
	v_mul_f32_e32 v86, 0xbfb8aa3b, v4
	v_exp_f32_e32 v86, v86
	v_cvt_pk_bf16_f32 v2, v2, s0
	v_mul_f32_e32 v3, v3, v85
	v_cvt_pk_bf16_f32 v3, v3, s0
	global_store_short v[126:127], v2, off offset:1024
	v_add_f32_e32 v2, 1.0, v86
	global_store_short v[130:131], v3, off offset:1024
	v_mul_f32_e32 v3, v82, v6
	v_rcp_f32_e32 v2, v2
	v_fmac_f32_e32 v3, v34, v5
	v_fmac_f32_e32 v3, v83, v7
	v_fmac_f32_e32 v3, v84, v8
	v_add_f32_e32 v3, v79, v3
	v_mul_f32_e32 v2, v4, v2
	v_mul_f32_e32 v4, 0xbfb8aa3b, v3
	v_exp_f32_e32 v4, v4
	v_mul_f32_e32 v5, v82, v7
	v_fmac_f32_e32 v5, v34, v6
	v_fmac_f32_e32 v5, v83, v8
	v_add_f32_e32 v4, 1.0, v4
	v_rcp_f32_e32 v4, v4
	v_fmac_f32_e32 v5, v84, v9
	v_add_f32_e32 v5, v79, v5
	v_mul_f32_e32 v6, 0xbfb8aa3b, v5
	v_mul_f32_e32 v3, v3, v4
	v_exp_f32_e32 v6, v6
	v_cvt_pk_bf16_f32 v3, v3, s0
	global_store_short v[128:129], v3, off offset:1024
	v_mul_f32_e32 v3, v82, v8
	v_fmac_f32_e32 v3, v34, v7
	v_cvt_pk_bf16_f32 v2, v2, s0
	v_fmac_f32_e32 v3, v83, v9
	global_store_short v[122:123], v2, off offset:1024
	v_add_f32_e32 v2, 1.0, v6
	v_fmac_f32_e32 v3, v84, v10
	v_rcp_f32_e32 v2, v2
	v_add_f32_e32 v3, v79, v3
	v_mul_f32_e32 v4, 0xbfb8aa3b, v3
	v_exp_f32_e32 v4, v4
	v_mul_f32_e32 v2, v5, v2
	v_mul_f32_e32 v5, v82, v9
	v_fmac_f32_e32 v5, v34, v8
	v_cndmask_b32_e64 v11, 0, v11, s[54:55]
	v_fmac_f32_e32 v5, v83, v10
	v_add_f32_e32 v4, 1.0, v4
	v_fmac_f32_e32 v5, v84, v11
	v_rcp_f32_e32 v4, v4
	v_add_f32_e32 v5, v79, v5
	v_mul_f32_e32 v6, 0xbfb8aa3b, v5
	v_exp_f32_e32 v6, v6
	v_mul_f32_e32 v3, v3, v4
	v_cvt_pk_bf16_f32 v3, v3, s0
	v_cvt_pk_bf16_f32 v2, v2, s0
	global_store_short v[124:125], v3, off offset:1024
	v_mul_f32_e32 v3, v82, v10
	v_lshlrev_b32_e32 v12, 16, v12
	global_store_short v[118:119], v2, off offset:1024
	v_add_f32_e32 v2, 1.0, v6
	v_fmac_f32_e32 v3, v34, v9
	v_cndmask_b32_e64 v12, 0, v12, s[56:57]
	v_rcp_f32_e32 v2, v2
	v_fmac_f32_e32 v3, v83, v11
	v_fmac_f32_e32 v3, v84, v12
	v_add_f32_e32 v3, v79, v3
	v_mul_f32_e32 v4, 0xbfb8aa3b, v3
	v_mul_f32_e32 v2, v5, v2
	v_exp_f32_e32 v4, v4
	v_mul_f32_e32 v5, v82, v11
	v_lshlrev_b32_e32 v13, 16, v13
	v_fmac_f32_e32 v5, v34, v10
	v_cndmask_b32_e64 v13, 0, v13, s[58:59]
	v_fmac_f32_e32 v5, v83, v12
	v_fmac_f32_e32 v5, v84, v13
	v_add_f32_e32 v5, v79, v5
	v_add_f32_e32 v4, 1.0, v4
	v_mul_f32_e32 v6, 0xbfb8aa3b, v5
	v_rcp_f32_e32 v4, v4
	v_exp_f32_e32 v6, v6
	v_cvt_pk_bf16_f32 v2, v2, s0
	global_store_short v[112:113], v2, off offset:1024
	v_mul_f32_e32 v3, v3, v4
	v_add_f32_e32 v2, 1.0, v6
	v_cvt_pk_bf16_f32 v3, v3, s0
	v_rcp_f32_e32 v2, v2
	global_store_short v[120:121], v3, off offset:1024
	v_mul_f32_e32 v3, v82, v12
	v_lshlrev_b32_e32 v14, 16, v14
	v_fmac_f32_e32 v3, v34, v11
	v_cndmask_b32_e64 v14, 0, v14, s[60:61]
	v_fmac_f32_e32 v3, v83, v13
	v_fmac_f32_e32 v3, v84, v14
	v_mul_f32_e32 v2, v5, v2
	v_add_f32_e32 v3, v79, v3
	v_mul_f32_e32 v5, v82, v13
	v_lshlrev_b32_e32 v15, 16, v15
	v_mul_f32_e32 v4, 0xbfb8aa3b, v3
	v_fmac_f32_e32 v5, v34, v12
	v_cndmask_b32_e64 v15, 0, v15, s[62:63]
	v_exp_f32_e32 v4, v4
	v_fmac_f32_e32 v5, v83, v14
	v_fmac_f32_e32 v5, v84, v15
	v_add_f32_e32 v5, v79, v5
	v_mul_f32_e32 v6, 0xbfb8aa3b, v5
	v_exp_f32_e32 v6, v6
	v_add_f32_e32 v4, 1.0, v4
	v_rcp_f32_e32 v4, v4
	v_cvt_pk_bf16_f32 v2, v2, s0
	global_store_short v[108:109], v2, off offset:1024
	v_add_f32_e32 v2, 1.0, v6
	v_rcp_f32_e32 v2, v2
	v_mul_f32_e32 v3, v3, v4
	v_cvt_pk_bf16_f32 v3, v3, s0
	global_store_short v[114:115], v3, off offset:1024
	v_mul_f32_e32 v3, v82, v14
	v_lshlrev_b32_e32 v16, 16, v16
	v_fmac_f32_e32 v3, v34, v13
	v_cndmask_b32_e64 v16, 0, v16, s[64:65]
	v_mul_f32_e32 v2, v5, v2
	v_fmac_f32_e32 v3, v83, v15
	v_mul_f32_e32 v5, v82, v15
	v_lshlrev_b32_e32 v17, 16, v17
	v_fmac_f32_e32 v3, v84, v16
	v_fmac_f32_e32 v5, v34, v14
	v_cndmask_b32_e64 v17, 0, v17, s[66:67]
	v_add_f32_e32 v3, v79, v3
	v_fmac_f32_e32 v5, v83, v16
	v_mul_f32_e32 v4, 0xbfb8aa3b, v3
	v_fmac_f32_e32 v5, v84, v17
	v_exp_f32_e32 v4, v4
	v_add_f32_e32 v5, v79, v5
	v_mul_f32_e32 v6, 0xbfb8aa3b, v5
	v_exp_f32_e32 v6, v6
	v_add_f32_e32 v4, 1.0, v4
	v_cvt_pk_bf16_f32 v2, v2, s0
	v_rcp_f32_e32 v4, v4
	global_store_short v[104:105], v2, off offset:1024
	v_add_f32_e32 v2, 1.0, v6
	v_rcp_f32_e32 v2, v2
	v_mul_f32_e32 v3, v3, v4
	v_cvt_pk_bf16_f32 v3, v3, s0
	v_lshlrev_b32_e32 v80, 16, v80
	global_store_short v[110:111], v3, off offset:1024
	v_mul_f32_e32 v2, v5, v2
	v_mul_f32_e32 v3, v82, v16
	v_mul_f32_e32 v5, v82, v17
	v_cndmask_b32_e64 v80, 0, v80, s[70:71]
	v_lshlrev_b32_e32 v81, 16, v81
	v_fmac_f32_e32 v3, v34, v15
	v_fmac_f32_e32 v5, v34, v16
	v_cndmask_b32_e64 v81, 0, v81, s[68:69]
	v_fmac_f32_e32 v3, v83, v17
	v_fmac_f32_e32 v5, v83, v80
	v_fmac_f32_e32 v3, v84, v80
	v_fmac_f32_e32 v5, v84, v81
	v_add_f32_e32 v3, v79, v3
	v_add_f32_e32 v5, v79, v5
	v_mul_f32_e32 v4, 0xbfb8aa3b, v3
	v_mul_f32_e32 v6, 0xbfb8aa3b, v5
	v_exp_f32_e32 v4, v4
	v_exp_f32_e32 v6, v6
	v_cvt_pk_bf16_f32 v2, v2, s0
	global_store_short v[102:103], v2, off offset:1024
	v_add_f32_e32 v4, 1.0, v4
	v_add_f32_e32 v2, 1.0, v6
	v_rcp_f32_e32 v4, v4
	v_rcp_f32_e32 v2, v2
	v_mul_f32_e32 v3, v3, v4
	v_mul_f32_e32 v2, v5, v2
	v_cvt_pk_bf16_f32 v3, v3, s0
	v_cvt_pk_bf16_f32 v2, v2, s0
	global_store_short v[106:107], v3, off offset:1024
	global_store_short v[116:117], v2, off offset:1024
	s_and_saveexec_b64 s[0:1], s[38:39]
	s_movk_i32 s90, 0x1a00
	s_cbranch_execz .LBB0_247
	v_readlane_b32 s2, v255, 48
	v_readlane_b32 s3, v255, 49
	v_add_u32_e32 v2, s88, v19
	v_mov_b32_e32 v79, v35
	v_mov_b64_e32 v[4:5], s[2:3]
	v_mad_i64_i32 v[4:5], s[2:3], v2, s90, v[4:5]
	v_lshl_add_u64 v[4:5], v[4:5], 0, v[78:79]
	v_add_co_u32_e32 v4, vcc, 0x1000, v4
	s_nop 1
	v_addc_co_u32_e32 v5, vcc, 0, v5, vcc
	global_load_ushort v3, v[4:5], off offset:2432
	s_nop 0
	global_load_dword v4, v[68:69], off
	s_waitcnt vmcnt(1)
	v_lshlrev_b32_e32 v3, 16, v3
	s_waitcnt vmcnt(0)
	v_add_f32_e32 v4, v4, v3
	v_mul_f32_e64 v3, |v4|, s97
	v_exp_f32_e32 v3, v3
	v_max_f32_e32 v4, 0, v4
	v_add_f32_e32 v3, 1.0, v3
	v_log_f32_e32 v5, v3
	v_ashrrev_i32_e32 v3, 31, v2
	v_lshlrev_b64 v[2:3], 6, v[2:3]
	v_lshl_add_u64 v[2:3], v[70:71], 0, v[2:3]
	v_fmac_f32_e32 v4, 0x3f317218, v5
	global_store_dword v[2:3], v4, off
	s_branch .LBB0_247

.LBB0_1234:
	v_and_b32_e32 v230, 15, v203
	v_lshrrev_b32_e32 v224, 4, v203
	v_lshlrev_b32_e32 v2, 8, v230
	v_lshl_add_u32 v2, v224, 6, v2
	ds_read_b128 v[194:197], v2
	ds_read_b128 v[204:207], v2 offset:16
	ds_read_b128 v[226:229], v2 offset:32
	ds_read_b128 v[68:71], v2 offset:48
	v_readfirstlane_b32 s0, v0
	v_lshlrev_b32_e32 v3, 14, v224
	s_lshr_b32 s0, s0, 6
	s_lshl_b32 s0, s0, 7
	v_lshl_add_u32 v230, v230, 3, v3
	v_add_u32_e32 v230, s0, v230
	v_add_u32_e32 v230, 0x2000, v230
	ds_read_b64 v[54:55], v230 offset:0
	ds_read_b64 v[60:61], v230 offset:1024
	ds_read_b64 v[198:199], v230 offset:2048
	ds_read_b64 v[208:209], v230 offset:3072
	s_waitcnt lgkmcnt(0)
	v_mfma_f32_16x16x4_f32 v[64:67], v194, v54, 0
	v_mfma_f32_16x16x4_f32 v[2:5], v194, v55, 0
	v_mfma_f32_16x16x4_f32 v[64:67], v195, v60, v[64:67]
	v_mfma_f32_16x16x4_f32 v[2:5], v195, v61, v[2:5]
	v_mfma_f32_16x16x4_f32 v[64:67], v196, v198, v[64:67]
	v_mfma_f32_16x16x4_f32 v[2:5], v196, v199, v[2:5]
	v_mfma_f32_16x16x4_f32 v[64:67], v197, v208, v[64:67]
	v_mfma_f32_16x16x4_f32 v[2:5], v197, v209, v[2:5]
	s_nop 7
	ds_read_b64 v[54:55], v230 offset:4096
	ds_read_b64 v[60:61], v230 offset:5120
	ds_read_b64 v[198:199], v230 offset:6144
	ds_read_b64 v[208:209], v230 offset:7168
	s_waitcnt lgkmcnt(0)
	v_mfma_f32_16x16x4_f32 v[64:67], v204, v54, v[64:67]
	v_mfma_f32_16x16x4_f32 v[2:5], v204, v55, v[2:5]
	v_mfma_f32_16x16x4_f32 v[64:67], v205, v60, v[64:67]
	v_mfma_f32_16x16x4_f32 v[2:5], v205, v61, v[2:5]
	v_mfma_f32_16x16x4_f32 v[64:67], v206, v198, v[64:67]
	v_mfma_f32_16x16x4_f32 v[2:5], v206, v199, v[2:5]
	v_mfma_f32_16x16x4_f32 v[64:67], v207, v208, v[64:67]
	v_mfma_f32_16x16x4_f32 v[2:5], v207, v209, v[2:5]
	s_nop 7
	ds_read_b64 v[54:55], v230 offset:8192
	ds_read_b64 v[60:61], v230 offset:9216
	ds_read_b64 v[198:199], v230 offset:10240
	ds_read_b64 v[208:209], v230 offset:11264
	s_waitcnt lgkmcnt(0)
	v_mfma_f32_16x16x4_f32 v[64:67], v226, v54, v[64:67]
	v_mfma_f32_16x16x4_f32 v[2:5], v226, v55, v[2:5]
	v_mfma_f32_16x16x4_f32 v[64:67], v227, v60, v[64:67]
	v_mfma_f32_16x16x4_f32 v[2:5], v227, v61, v[2:5]
	v_mfma_f32_16x16x4_f32 v[64:67], v228, v198, v[64:67]
	v_mfma_f32_16x16x4_f32 v[2:5], v228, v199, v[2:5]
	v_mfma_f32_16x16x4_f32 v[64:67], v229, v208, v[64:67]
	v_mfma_f32_16x16x4_f32 v[2:5], v229, v209, v[2:5]
	s_nop 7
	ds_read_b64 v[54:55], v230 offset:12288
	ds_read_b64 v[60:61], v230 offset:13312
	ds_read_b64 v[198:199], v230 offset:14336
	ds_read_b64 v[208:209], v230 offset:15360
	s_waitcnt lgkmcnt(0)
	v_mfma_f32_16x16x4_f32 v[64:67], v68, v54, v[64:67]
	v_mfma_f32_16x16x4_f32 v[2:5], v68, v55, v[2:5]
	v_mfma_f32_16x16x4_f32 v[64:67], v69, v60, v[64:67]
	v_mfma_f32_16x16x4_f32 v[2:5], v69, v61, v[2:5]
	v_mfma_f32_16x16x4_f32 v[64:67], v70, v198, v[64:67]
	v_mfma_f32_16x16x4_f32 v[2:5], v70, v199, v[2:5]
	v_mfma_f32_16x16x4_f32 v[64:67], v71, v208, v[64:67]
	v_mfma_f32_16x16x4_f32 v[2:5], v71, v209, v[2:5]
	s_nop 7
	v_and_b32_e32 v230, 15, v203
	v_lshrrev_b32_e32 v224, 4, v203
	v_lshlrev_b32_e32 v224, 4, v224
	v_lshl_add_u32 v224, v230, 7, v224
	s_lshl_b32 s0, s0, 4
	v_add_u32_e32 v224, s0, v224
	v_add_u32_e32 v224, 0x14000, v224
	s_nop 15
	s_nop 15
	ds_write_b128 v224, v[64:67]
	ds_write_b128 v224, v[2:5] offset:64
	v_and_b32_e32 v230, 0xff, v0
	v_lshrrev_b32_e32 v198, 8, v0
	v_lshlrev_b32_e32 v230, 6, v230
	v_lshl_add_u32 v230, v198, 5, v230
	v_add_u32_e32 v230, 0x14000, v230
	s_waitcnt lgkmcnt(0)
	s_barrier
	ds_read_b64 v[66:67], v230
	ds_read_b64 v[64:65], v230 offset:8
	ds_read_b64 v[60:61], v230 offset:16
	ds_read_b64 v[54:55], v230 offset:24
	s_movk_i32 s0, 0x100
	s_waitcnt lgkmcnt(0)
	v_lshlrev_b32_e32 v196, 16, v170
	v_lshlrev_b32_e32 v237, 16, v172
	v_lshlrev_b32_e32 v236, 16, v173
	v_lshlrev_b32_e32 v233, 16, v176
	global_load_dword v176, v[20:21], off
	global_load_dword v173, v[22:23], off
	global_load_dword v170, v[24:25], off
	global_load_dword v172, v[26:27], off
	v_and_b32_e32 v2, 64, v203
	v_add_u32_e32 v69, 64, v2
	v_xor_b32_e32 v2, 1, v203
	v_cmp_lt_i32_e64 s[2:3], v2, v69
	v_xor_b32_e32 v3, 2, v203
	v_xor_b32_e32 v4, 4, v203
	v_cndmask_b32_e64 v2, v203, v2, s[2:3]
	v_cmp_lt_i32_e64 s[2:3], v3, v69
	v_xor_b32_e32 v5, 8, v203
	v_xor_b32_e32 v68, 16, v203
	v_cndmask_b32_e64 v3, v203, v3, s[2:3]
	v_cmp_lt_i32_e64 s[2:3], v4, v69
	v_lshlrev_b32_e32 v194, 16, v163
	v_lshlrev_b32_e32 v224, 16, v191
	v_cndmask_b32_e64 v4, v203, v4, s[2:3]
	v_cmp_lt_i32_e64 s[2:3], v5, v69
	v_lshlrev_b32_e32 v191, 16, v192
	v_xor_b32_e32 v192, 32, v203
	v_cndmask_b32_e64 v5, v203, v5, s[2:3]
	v_cmp_lt_i32_e64 s[2:3], v68, v69
	v_lshlrev_b32_e32 v183, 16, v183
	v_add_f32_e32 v183, v183, v194
	v_cndmask_b32_e64 v68, v203, v68, s[2:3]
	v_cmp_lt_i32_e64 s[2:3], v192, v69
	v_lshlrev_b32_e32 v2, 2, v2
	v_lshlrev_b32_e32 v3, 2, v3
	v_cndmask_b32_e64 v69, v203, v192, s[2:3]
	v_mul_f32_e32 v192, v183, v183
	s_nop 1
	v_mov_b32_dpp v192, v192 quad_perm:[1,0,3,2] row_mask:0xf bank_mask:0xf
	v_lshlrev_b32_e32 v225, 16, v190
	v_lshlrev_b32_e32 v190, 16, v193
	v_lshlrev_b32_e32 v4, 2, v4
	v_lshlrev_b32_e32 v5, 2, v5
	s_waitcnt lgkmcnt(0)
	v_fmac_f32_e32 v192, v183, v183
	s_nop 1
	v_lshlrev_b32_e32 v68, 2, v68
	v_lshlrev_b32_e32 v69, 2, v69
	v_lshlrev_b32_e32 v184, 16, v184
	v_lshlrev_b32_e32 v195, 16, v169
	s_waitcnt lgkmcnt(0)
	v_add_f32_dpp v192, v192, v192 quad_perm:[2,3,0,1] row_mask:0xf bank_mask:0xf
	s_nop 1
	v_lshlrev_b32_e32 v181, 16, v181
	v_add_f32_e32 v181, v181, v195
	v_lshlrev_b32_e32 v179, 16, v179
	v_mul_f32_e32 v179, v196, v179
	s_waitcnt lgkmcnt(0)
	v_add_f32_dpp v192, v192, v192 row_half_mirror row_mask:0xf bank_mask:0xf
	s_nop 1
	v_lshlrev_b32_e32 v238, 16, v171
	v_lshlrev_b64 v[62:63], 11, v[62:63]
	v_lshl_add_u64 v[62:63], v[28:29], 0, v[62:63]
	v_lshlrev_b32_e32 v235, 16, v174
	s_waitcnt lgkmcnt(0)
	v_add_f32_dpp v192, v192, v192 row_mirror row_mask:0xf bank_mask:0xf
	v_mov_b32_e32 v193, v192
	s_nop 1
	v_permlane16_swap_b32_e32 v193, v192
	v_lshlrev_b32_e32 v234, 16, v175
	v_lshlrev_b64 v[58:59], 11, v[58:59]
	v_lshl_add_u64 v[58:59], v[28:29], 0, v[58:59]
	v_lshlrev_b32_e32 v232, 16, v180
	s_waitcnt lgkmcnt(0)
	v_add_f32_e32 v192, v192, v193
	v_mov_b32_e32 v193, v192
	s_nop 1
	v_permlane32_swap_b32_e32 v193, v192
	v_lshlrev_b32_e32 v231, 16, v182
	v_lshlrev_b32_e32 v230, 16, v185
	v_lshlrev_b64 v[56:57], 11, v[56:57]
	v_lshl_add_u64 v[56:57], v[28:29], 0, v[56:57]
	s_waitcnt lgkmcnt(0)
	v_add_f32_e32 v192, v192, v193
	v_fmamk_f32 v192, v192, 0x3c800000, v165
	v_rsq_f32_e32 v192, v192
	v_lshlrev_b32_e32 v229, 16, v186
	v_lshlrev_b32_e32 v228, 16, v187
	v_lshlrev_b32_e32 v227, 16, v188
	v_mul_f32_e32 v183, v183, v192
	v_mul_f32_e32 v192, 0xbfb8aa3b, v184
	v_exp_f32_e32 v192, v192
	v_lshlrev_b32_e32 v226, 16, v189
	v_lshlrev_b64 v[52:53], 11, v[52:53]
	v_lshl_add_u64 v[52:53], v[28:29], 0, v[52:53]
	v_add_f32_e32 v192, 1.0, v192
	v_rcp_f32_e32 v192, v192
	s_waitcnt vmcnt(3)
	v_mul_f32_e32 v183, v176, v183
	v_lshlrev_b64 v[50:51], 11, v[50:51]
	v_lshl_add_u64 v[50:51], v[28:29], 0, v[50:51]
	v_mul_f32_e32 v184, v192, v184
	v_mul_f32_e32 v183, v184, v183
	s_nop 1
	v_lshlrev_b32_e32 v189, 16, v210
	v_lshlrev_b32_e32 v188, 16, v211
	v_lshlrev_b32_e32 v187, 16, v212
	v_lshlrev_b32_e32 v186, 16, v213
	s_waitcnt lgkmcnt(0)
	v_add_f32_dpp v184, v181, v181 quad_perm:[1,0,3,2] row_mask:0xf bank_mask:0xf
	s_nop 1
	v_lshlrev_b64 v[48:49], 11, v[48:49]
	v_lshl_add_u64 v[48:49], v[28:29], 0, v[48:49]
	v_lshlrev_b32_e32 v185, 16, v214
	v_lshlrev_b32_e32 v182, 16, v215
	s_waitcnt lgkmcnt(0)
	v_add_f32_dpp v184, v184, v184 quad_perm:[2,3,0,1] row_mask:0xf bank_mask:0xf
	s_nop 1
	v_lshlrev_b32_e32 v180, 16, v216
	v_lshlrev_b32_e32 v175, 16, v217
	v_lshlrev_b64 v[46:47], 11, v[46:47]
	v_lshl_add_u64 v[46:47], v[28:29], 0, v[46:47]
	s_waitcnt lgkmcnt(0)
	v_add_f32_dpp v184, v184, v184 row_half_mirror row_mask:0xf bank_mask:0xf
	s_nop 1
	v_lshlrev_b32_e32 v174, 16, v218
	v_lshlrev_b32_e32 v171, 16, v219
	v_lshlrev_b32_e32 v169, 16, v220
	v_lshlrev_b32_e32 v163, 16, v221
	s_waitcnt lgkmcnt(0)
	v_add_f32_dpp v184, v184, v184 row_mirror row_mask:0xf bank_mask:0xf
	v_mov_b32_e32 v192, v184
	s_nop 1
	v_permlane16_swap_b32_e32 v192, v184
	v_lshlrev_b64 v[44:45], 11, v[44:45]
	v_lshl_add_u64 v[44:45], v[28:29], 0, v[44:45]
	v_lshlrev_b32_e32 v71, 16, v222
	v_lshlrev_b32_e32 v70, 16, v223
	s_waitcnt lgkmcnt(0)
	v_add_f32_e32 v184, v184, v192
	v_mov_b32_e32 v192, v184
	s_nop 1
	v_permlane32_swap_b32_e32 v192, v184
	s_waitcnt lgkmcnt(0)
	v_add_f32_e32 v184, v184, v192
	v_fmac_f32_e32 v181, 0xbc800000, v184
	v_mul_f32_e32 v184, v181, v181
	s_nop 1
	v_mov_b32_dpp v184, v184 quad_perm:[1,0,3,2] row_mask:0xf bank_mask:0xf
	s_waitcnt lgkmcnt(0)
	v_fmac_f32_e32 v184, v181, v181
	s_nop 1
	s_waitcnt lgkmcnt(0)
	v_add_f32_dpp v184, v184, v184 quad_perm:[2,3,0,1] row_mask:0xf bank_mask:0xf
	s_nop 1
	s_waitcnt lgkmcnt(0)
	v_add_f32_dpp v184, v184, v184 row_half_mirror row_mask:0xf bank_mask:0xf
	s_nop 1
	s_waitcnt lgkmcnt(0)
	v_add_f32_dpp v184, v184, v184 row_mirror row_mask:0xf bank_mask:0xf
	v_mov_b32_e32 v192, v184
	s_nop 1
	v_permlane16_swap_b32_e32 v192, v184
	s_waitcnt lgkmcnt(0)
	v_add_f32_e32 v184, v184, v192
	v_mov_b32_e32 v192, v184
	s_nop 1
	v_permlane32_swap_b32_e32 v192, v184
	s_waitcnt lgkmcnt(0)
	v_add_f32_e32 v184, v184, v192
	v_fmamk_f32 v184, v184, 0x3c800000, v164
	v_rsq_f32_e32 v184, v184
	s_nop 0
	v_mul_f32_e32 v181, v181, v184
	s_waitcnt vmcnt(0)
	v_mul_f32_e32 v184, v179, v172
	s_nop 1
	v_mov_b32_dpp v184, v184 quad_perm:[1,0,3,2] row_mask:0xf bank_mask:0xf
	v_fma_f32 v181, v173, v181, v170
	s_waitcnt lgkmcnt(0)
	v_fmac_f32_e32 v184, v179, v172
	s_nop 1
	s_waitcnt lgkmcnt(0)
	v_add_f32_dpp v179, v184, v184 quad_perm:[2,3,0,1] row_mask:0xf bank_mask:0xf
	s_nop 1
	s_waitcnt lgkmcnt(0)
	v_add_f32_dpp v179, v179, v179 row_half_mirror row_mask:0xf bank_mask:0xf
	s_nop 1
	s_waitcnt lgkmcnt(0)
	v_add_f32_dpp v179, v179, v179 row_mirror row_mask:0xf bank_mask:0xf
	v_mov_b32_e32 v184, v179
	s_nop 1
	v_permlane16_swap_b32_e32 v184, v179
	s_waitcnt lgkmcnt(0)
	v_add_f32_e32 v179, v179, v184
	v_mov_b32_e32 v184, v179
	s_nop 1
	v_permlane32_swap_b32_e32 v184, v179
	s_waitcnt lgkmcnt(0)
	v_add_f32_e32 v179, v179, v184
	v_fmac_f32_e32 v181, v179, v238
	v_mul_f32_e32 v66, v66, v181
	v_cvt_pk_bf16_f32 v179, v183, s0
	v_cvt_pk_bf16_f32 v66, v66, s0
	global_store_short v[62:63], v179, off
	global_store_short v[62:63], v66, off offset:512
	v_lshlrev_b32_e32 v62, 16, v177
	v_add_f32_e32 v62, v62, v237
	v_mul_f32_e32 v63, v62, v62
	s_nop 1
	v_mov_b32_dpp v63, v63 quad_perm:[1,0,3,2] row_mask:0xf bank_mask:0xf
	s_waitcnt lgkmcnt(0)
	v_fmac_f32_e32 v63, v62, v62
	s_nop 1
	s_waitcnt lgkmcnt(0)
	v_add_f32_dpp v63, v63, v63 quad_perm:[2,3,0,1] row_mask:0xf bank_mask:0xf
	s_nop 1
	s_waitcnt lgkmcnt(0)
	v_add_f32_dpp v63, v63, v63 row_half_mirror row_mask:0xf bank_mask:0xf
	s_nop 1
	s_waitcnt lgkmcnt(0)
	v_add_f32_dpp v63, v63, v63 row_mirror row_mask:0xf bank_mask:0xf
	v_mov_b32_e32 v66, v63
	s_nop 1
	v_permlane16_swap_b32_e32 v66, v63
	s_waitcnt lgkmcnt(0)
	v_add_f32_e32 v63, v63, v66
	v_mov_b32_e32 v66, v63
	s_nop 1
	v_permlane32_swap_b32_e32 v66, v63
	s_waitcnt lgkmcnt(0)
	v_add_f32_e32 v63, v63, v66
	v_fmamk_f32 v63, v63, 0x3c800000, v165
	v_rsq_f32_e32 v63, v63
	s_nop 0
	v_mul_f32_e32 v62, v62, v63
	v_lshlrev_b32_e32 v63, 16, v178
	v_mul_f32_e32 v66, 0xbfb8aa3b, v63
	v_exp_f32_e32 v66, v66
	v_mul_f32_e32 v62, v176, v62
	v_add_f32_e32 v66, 1.0, v66
	v_rcp_f32_e32 v66, v66
	s_nop 0
	v_mul_f32_e32 v63, v66, v63
	v_mul_f32_e32 v62, v63, v62
	v_lshlrev_b32_e32 v63, 16, v162
	v_add_f32_e32 v63, v63, v236
	s_nop 1
	v_cvt_pk_bf16_f32 v62, v62, s0
	global_store_short v[58:59], v62, off
	s_waitcnt lgkmcnt(0)
	v_add_f32_dpp v66, v63, v63 quad_perm:[1,0,3,2] row_mask:0xf bank_mask:0xf
	s_nop 1
	s_waitcnt lgkmcnt(0)
	v_add_f32_dpp v66, v66, v66 quad_perm:[2,3,0,1] row_mask:0xf bank_mask:0xf
	s_nop 1
	s_waitcnt lgkmcnt(0)
	v_add_f32_dpp v66, v66, v66 row_half_mirror row_mask:0xf bank_mask:0xf
	s_nop 1
	s_waitcnt lgkmcnt(0)
	v_add_f32_dpp v66, v66, v66 row_mirror row_mask:0xf bank_mask:0xf
	v_mov_b32_e32 v162, v66
	s_nop 1
	v_permlane16_swap_b32_e32 v162, v66
	s_waitcnt lgkmcnt(0)
	v_add_f32_e32 v66, v66, v162
	v_mov_b32_e32 v162, v66
	s_nop 1
	v_permlane32_swap_b32_e32 v162, v66
	s_waitcnt lgkmcnt(0)
	v_add_f32_e32 v66, v66, v162
	v_fmac_f32_e32 v63, 0xbc800000, v66
	v_mul_f32_e32 v66, v63, v63
	s_nop 1
	v_mov_b32_dpp v66, v66 quad_perm:[1,0,3,2] row_mask:0xf bank_mask:0xf
	s_waitcnt lgkmcnt(0)
	v_fmac_f32_e32 v66, v63, v63
	s_nop 1
	s_waitcnt lgkmcnt(0)
	v_add_f32_dpp v66, v66, v66 quad_perm:[2,3,0,1] row_mask:0xf bank_mask:0xf
	s_nop 1
	s_waitcnt lgkmcnt(0)
	v_add_f32_dpp v66, v66, v66 row_half_mirror row_mask:0xf bank_mask:0xf
	s_nop 1
	s_waitcnt lgkmcnt(0)
	v_add_f32_dpp v66, v66, v66 row_mirror row_mask:0xf bank_mask:0xf
	v_mov_b32_e32 v162, v66
	s_nop 1
	v_permlane16_swap_b32_e32 v162, v66
	s_waitcnt lgkmcnt(0)
	v_add_f32_e32 v66, v66, v162
	v_mov_b32_e32 v162, v66
	s_nop 1
	v_permlane32_swap_b32_e32 v162, v66
	s_waitcnt lgkmcnt(0)
	v_add_f32_e32 v66, v66, v162
	v_fmamk_f32 v66, v66, 0x3c800000, v164
	v_rsq_f32_e32 v66, v66
	s_nop 0
	v_mul_f32_e32 v63, v63, v66
	v_lshlrev_b32_e32 v66, 16, v161
	v_mul_f32_e32 v66, v235, v66
	v_mul_f32_e32 v161, v66, v172
	s_nop 1
	v_mov_b32_dpp v161, v161 quad_perm:[1,0,3,2] row_mask:0xf bank_mask:0xf
	v_fma_f32 v63, v173, v63, v170
	s_waitcnt lgkmcnt(0)
	v_fmac_f32_e32 v161, v66, v172
	s_nop 1
	s_waitcnt lgkmcnt(0)
	v_add_f32_dpp v66, v161, v161 quad_perm:[2,3,0,1] row_mask:0xf bank_mask:0xf
	s_nop 1
	s_waitcnt lgkmcnt(0)
	v_add_f32_dpp v66, v66, v66 row_half_mirror row_mask:0xf bank_mask:0xf
	s_nop 1
	s_waitcnt lgkmcnt(0)
	v_add_f32_dpp v66, v66, v66 row_mirror row_mask:0xf bank_mask:0xf
	v_mov_b32_e32 v161, v66
	s_nop 1
	v_permlane16_swap_b32_e32 v161, v66
	s_waitcnt lgkmcnt(0)
	v_add_f32_e32 v66, v66, v161
	v_mov_b32_e32 v161, v66
	s_nop 1
	v_permlane32_swap_b32_e32 v161, v66
	s_waitcnt lgkmcnt(0)
	v_add_f32_e32 v66, v66, v161
	v_fmac_f32_e32 v63, v66, v234
	v_mul_f32_e32 v63, v67, v63
	v_cvt_pk_bf16_f32 v62, v63, s0
	global_store_short v[58:59], v62, off offset:512
	v_lshlrev_b32_e32 v58, 16, v159
	v_add_f32_e32 v58, v58, v233
	v_mul_f32_e32 v59, v58, v58
	s_nop 1
	v_mov_b32_dpp v59, v59 quad_perm:[1,0,3,2] row_mask:0xf bank_mask:0xf
	s_waitcnt lgkmcnt(0)
	v_fmac_f32_e32 v59, v58, v58
	s_nop 1
	s_waitcnt lgkmcnt(0)
	v_add_f32_dpp v59, v59, v59 quad_perm:[2,3,0,1] row_mask:0xf bank_mask:0xf
	s_nop 1
	s_waitcnt lgkmcnt(0)
	v_add_f32_dpp v59, v59, v59 row_half_mirror row_mask:0xf bank_mask:0xf
	s_nop 1
	s_waitcnt lgkmcnt(0)
	v_add_f32_dpp v59, v59, v59 row_mirror row_mask:0xf bank_mask:0xf
	v_mov_b32_e32 v62, v59
	s_nop 1
	v_permlane16_swap_b32_e32 v62, v59
	s_waitcnt lgkmcnt(0)
	v_add_f32_e32 v59, v59, v62
	v_mov_b32_e32 v62, v59
	s_nop 1
	v_permlane32_swap_b32_e32 v62, v59
	s_waitcnt lgkmcnt(0)
	v_add_f32_e32 v59, v59, v62
	v_fmamk_f32 v59, v59, 0x3c800000, v165
	v_rsq_f32_e32 v59, v59
	s_nop 0
	v_mul_f32_e32 v58, v58, v59
	v_lshlrev_b32_e32 v59, 16, v160
	v_mul_f32_e32 v62, 0xbfb8aa3b, v59
	v_exp_f32_e32 v62, v62
	v_mul_f32_e32 v58, v176, v58
	v_add_f32_e32 v62, 1.0, v62
	v_rcp_f32_e32 v62, v62
	s_nop 0
	v_mul_f32_e32 v59, v62, v59
	v_mul_f32_e32 v58, v59, v58
	v_lshlrev_b32_e32 v59, 16, v158
	v_add_f32_e32 v59, v59, v232
	s_nop 1
	v_cvt_pk_bf16_f32 v58, v58, s0
	global_store_short v[56:57], v58, off
	s_waitcnt lgkmcnt(0)
	v_add_f32_dpp v62, v59, v59 quad_perm:[1,0,3,2] row_mask:0xf bank_mask:0xf
	s_nop 1
	s_waitcnt lgkmcnt(0)
	v_add_f32_dpp v62, v62, v62 quad_perm:[2,3,0,1] row_mask:0xf bank_mask:0xf
	s_nop 1
	s_waitcnt lgkmcnt(0)
	v_add_f32_dpp v62, v62, v62 row_half_mirror row_mask:0xf bank_mask:0xf
	s_nop 1
	s_waitcnt lgkmcnt(0)
	v_add_f32_dpp v62, v62, v62 row_mirror row_mask:0xf bank_mask:0xf
	v_mov_b32_e32 v63, v62
	s_nop 1
	v_permlane16_swap_b32_e32 v63, v62
	s_waitcnt lgkmcnt(0)
	v_add_f32_e32 v62, v62, v63
	v_mov_b32_e32 v63, v62
	s_nop 1
	v_permlane32_swap_b32_e32 v63, v62
	s_waitcnt lgkmcnt(0)
	v_add_f32_e32 v62, v62, v63
	v_fmac_f32_e32 v59, 0xbc800000, v62
	v_mul_f32_e32 v62, v59, v59
	s_nop 1
	v_mov_b32_dpp v62, v62 quad_perm:[1,0,3,2] row_mask:0xf bank_mask:0xf
	s_waitcnt lgkmcnt(0)
	v_fmac_f32_e32 v62, v59, v59
	s_nop 1
	s_waitcnt lgkmcnt(0)
	v_add_f32_dpp v62, v62, v62 quad_perm:[2,3,0,1] row_mask:0xf bank_mask:0xf
	s_nop 1
	s_waitcnt lgkmcnt(0)
	v_add_f32_dpp v62, v62, v62 row_half_mirror row_mask:0xf bank_mask:0xf
	s_nop 1
	s_waitcnt lgkmcnt(0)
	v_add_f32_dpp v62, v62, v62 row_mirror row_mask:0xf bank_mask:0xf
	v_mov_b32_e32 v63, v62
	s_nop 1
	v_permlane16_swap_b32_e32 v63, v62
	s_waitcnt lgkmcnt(0)
	v_add_f32_e32 v62, v62, v63
	v_mov_b32_e32 v63, v62
	s_nop 1
	v_permlane32_swap_b32_e32 v63, v62
	s_waitcnt lgkmcnt(0)
	v_add_f32_e32 v62, v62, v63
	v_fmamk_f32 v62, v62, 0x3c800000, v164
	v_rsq_f32_e32 v62, v62
	s_nop 0
	v_mul_f32_e32 v59, v59, v62
	v_lshlrev_b32_e32 v62, 16, v157
	v_mul_f32_e32 v62, v231, v62
	v_mul_f32_e32 v63, v62, v172
	s_nop 1
	v_mov_b32_dpp v63, v63 quad_perm:[1,0,3,2] row_mask:0xf bank_mask:0xf
	v_fma_f32 v59, v173, v59, v170
	s_waitcnt lgkmcnt(0)
	v_fmac_f32_e32 v63, v62, v172
	s_nop 1
	s_waitcnt lgkmcnt(0)
	v_add_f32_dpp v62, v63, v63 quad_perm:[2,3,0,1] row_mask:0xf bank_mask:0xf
	s_nop 1
	s_waitcnt lgkmcnt(0)
	v_add_f32_dpp v62, v62, v62 row_half_mirror row_mask:0xf bank_mask:0xf
	s_nop 1
	s_waitcnt lgkmcnt(0)
	v_add_f32_dpp v62, v62, v62 row_mirror row_mask:0xf bank_mask:0xf
	v_mov_b32_e32 v63, v62
	s_nop 1
	v_permlane16_swap_b32_e32 v63, v62
	s_waitcnt lgkmcnt(0)
	v_add_f32_e32 v62, v62, v63
	v_mov_b32_e32 v63, v62
	s_nop 1
	v_permlane32_swap_b32_e32 v63, v62
	s_waitcnt lgkmcnt(0)
	v_add_f32_e32 v62, v62, v63
	v_fmac_f32_e32 v59, v62, v230
	v_mul_f32_e32 v59, v64, v59
	v_cvt_pk_bf16_f32 v58, v59, s0
	global_store_short v[56:57], v58, off offset:512
	v_lshlrev_b32_e32 v56, 16, v155
	v_add_f32_e32 v56, v56, v229
	v_mul_f32_e32 v57, v56, v56
	s_nop 1
	v_mov_b32_dpp v57, v57 quad_perm:[1,0,3,2] row_mask:0xf bank_mask:0xf
	s_waitcnt lgkmcnt(0)
	v_fmac_f32_e32 v57, v56, v56
	s_nop 1
	s_waitcnt lgkmcnt(0)
	v_add_f32_dpp v57, v57, v57 quad_perm:[2,3,0,1] row_mask:0xf bank_mask:0xf
	s_nop 1
	s_waitcnt lgkmcnt(0)
	v_add_f32_dpp v57, v57, v57 row_half_mirror row_mask:0xf bank_mask:0xf
	s_nop 1
	s_waitcnt lgkmcnt(0)
	v_add_f32_dpp v57, v57, v57 row_mirror row_mask:0xf bank_mask:0xf
	v_mov_b32_e32 v58, v57
	s_nop 1
	v_permlane16_swap_b32_e32 v58, v57
	s_waitcnt lgkmcnt(0)
	v_add_f32_e32 v57, v57, v58
	v_mov_b32_e32 v58, v57
	s_nop 1
	v_permlane32_swap_b32_e32 v58, v57
	s_waitcnt lgkmcnt(0)
	v_add_f32_e32 v57, v57, v58
	v_fmamk_f32 v57, v57, 0x3c800000, v165
	v_rsq_f32_e32 v57, v57
	s_nop 0
	v_mul_f32_e32 v56, v56, v57
	v_lshlrev_b32_e32 v57, 16, v156
	v_mul_f32_e32 v58, 0xbfb8aa3b, v57
	v_exp_f32_e32 v58, v58
	v_mul_f32_e32 v56, v176, v56
	v_add_f32_e32 v58, 1.0, v58
	v_rcp_f32_e32 v58, v58
	s_nop 0
	v_mul_f32_e32 v57, v58, v57
	v_mul_f32_e32 v56, v57, v56
	v_lshlrev_b32_e32 v57, 16, v154
	v_add_f32_e32 v57, v57, v228
	s_nop 1
	v_cvt_pk_bf16_f32 v56, v56, s0
	global_store_short v[52:53], v56, off
	s_waitcnt lgkmcnt(0)
	v_add_f32_dpp v58, v57, v57 quad_perm:[1,0,3,2] row_mask:0xf bank_mask:0xf
	s_nop 1
	s_waitcnt lgkmcnt(0)
	v_add_f32_dpp v58, v58, v58 quad_perm:[2,3,0,1] row_mask:0xf bank_mask:0xf
	s_nop 1
	s_waitcnt lgkmcnt(0)
	v_add_f32_dpp v58, v58, v58 row_half_mirror row_mask:0xf bank_mask:0xf
	s_nop 1
	s_waitcnt lgkmcnt(0)
	v_add_f32_dpp v58, v58, v58 row_mirror row_mask:0xf bank_mask:0xf
	v_mov_b32_e32 v59, v58
	s_nop 1
	v_permlane16_swap_b32_e32 v59, v58
	s_waitcnt lgkmcnt(0)
	v_add_f32_e32 v58, v58, v59
	v_mov_b32_e32 v59, v58
	s_nop 1
	v_permlane32_swap_b32_e32 v59, v58
	s_waitcnt lgkmcnt(0)
	v_add_f32_e32 v58, v58, v59
	v_fmac_f32_e32 v57, 0xbc800000, v58
	v_mul_f32_e32 v58, v57, v57
	s_nop 1
	v_mov_b32_dpp v58, v58 quad_perm:[1,0,3,2] row_mask:0xf bank_mask:0xf
	s_waitcnt lgkmcnt(0)
	v_fmac_f32_e32 v58, v57, v57
	s_nop 1
	s_waitcnt lgkmcnt(0)
	v_add_f32_dpp v58, v58, v58 quad_perm:[2,3,0,1] row_mask:0xf bank_mask:0xf
	s_nop 1
	s_waitcnt lgkmcnt(0)
	v_add_f32_dpp v58, v58, v58 row_half_mirror row_mask:0xf bank_mask:0xf
	s_nop 1
	s_waitcnt lgkmcnt(0)
	v_add_f32_dpp v58, v58, v58 row_mirror row_mask:0xf bank_mask:0xf
	v_mov_b32_e32 v59, v58
	s_nop 1
	v_permlane16_swap_b32_e32 v59, v58
	s_waitcnt lgkmcnt(0)
	v_add_f32_e32 v58, v58, v59
	v_mov_b32_e32 v59, v58
	s_nop 1
	v_permlane32_swap_b32_e32 v59, v58
	s_waitcnt lgkmcnt(0)
	v_add_f32_e32 v58, v58, v59
	v_fmamk_f32 v58, v58, 0x3c800000, v164
	v_rsq_f32_e32 v58, v58
	s_nop 0
	v_mul_f32_e32 v57, v57, v58
	v_lshlrev_b32_e32 v58, 16, v153
	v_mul_f32_e32 v58, v227, v58
	v_mul_f32_e32 v59, v58, v172
	s_nop 1
	v_mov_b32_dpp v59, v59 quad_perm:[1,0,3,2] row_mask:0xf bank_mask:0xf
	v_fma_f32 v57, v173, v57, v170
	s_waitcnt lgkmcnt(0)
	v_fmac_f32_e32 v59, v58, v172
	s_nop 1
	s_waitcnt lgkmcnt(0)
	v_add_f32_dpp v58, v59, v59 quad_perm:[2,3,0,1] row_mask:0xf bank_mask:0xf
	s_nop 1
	s_waitcnt lgkmcnt(0)
	v_add_f32_dpp v58, v58, v58 row_half_mirror row_mask:0xf bank_mask:0xf
	s_nop 1
	s_waitcnt lgkmcnt(0)
	v_add_f32_dpp v58, v58, v58 row_mirror row_mask:0xf bank_mask:0xf
	v_mov_b32_e32 v59, v58
	s_nop 1
	v_permlane16_swap_b32_e32 v59, v58
	s_waitcnt lgkmcnt(0)
	v_add_f32_e32 v58, v58, v59
	v_mov_b32_e32 v59, v58
	s_nop 1
	v_permlane32_swap_b32_e32 v59, v58
	s_waitcnt lgkmcnt(0)
	v_add_f32_e32 v58, v58, v59
	v_fmac_f32_e32 v57, v58, v226
	v_mul_f32_e32 v57, v65, v57
	v_cvt_pk_bf16_f32 v56, v57, s0
	global_store_short v[52:53], v56, off offset:512
	v_lshlrev_b32_e32 v52, 16, v151
	v_add_f32_e32 v52, v52, v225
	v_mul_f32_e32 v53, v52, v52
	s_nop 1
	v_mov_b32_dpp v53, v53 quad_perm:[1,0,3,2] row_mask:0xf bank_mask:0xf
	s_waitcnt lgkmcnt(0)
	v_fmac_f32_e32 v53, v52, v52
	s_nop 1
	s_waitcnt lgkmcnt(0)
	v_add_f32_dpp v53, v53, v53 quad_perm:[2,3,0,1] row_mask:0xf bank_mask:0xf
	s_nop 1
	s_waitcnt lgkmcnt(0)
	v_add_f32_dpp v53, v53, v53 row_half_mirror row_mask:0xf bank_mask:0xf
	s_nop 1
	s_waitcnt lgkmcnt(0)
	v_add_f32_dpp v53, v53, v53 row_mirror row_mask:0xf bank_mask:0xf
	v_mov_b32_e32 v56, v53
	s_nop 1
	v_permlane16_swap_b32_e32 v56, v53
	s_waitcnt lgkmcnt(0)
	v_add_f32_e32 v53, v53, v56
	v_mov_b32_e32 v56, v53
	s_nop 1
	v_permlane32_swap_b32_e32 v56, v53
	s_waitcnt lgkmcnt(0)
	v_add_f32_e32 v53, v53, v56
	v_fmamk_f32 v53, v53, 0x3c800000, v165
	v_rsq_f32_e32 v53, v53
	s_nop 0
	v_mul_f32_e32 v52, v52, v53
	v_lshlrev_b32_e32 v53, 16, v152
	v_mul_f32_e32 v56, 0xbfb8aa3b, v53
	v_exp_f32_e32 v56, v56
	v_mul_f32_e32 v52, v176, v52
	v_add_f32_e32 v56, 1.0, v56
	v_rcp_f32_e32 v56, v56
	s_nop 0
	v_mul_f32_e32 v53, v56, v53
	v_mul_f32_e32 v52, v53, v52
	v_lshlrev_b32_e32 v53, 16, v150
	v_add_f32_e32 v53, v53, v224
	s_nop 1
	v_cvt_pk_bf16_f32 v52, v52, s0
	global_store_short v[50:51], v52, off
	s_waitcnt lgkmcnt(0)
	v_add_f32_dpp v56, v53, v53 quad_perm:[1,0,3,2] row_mask:0xf bank_mask:0xf
	s_nop 1
	s_waitcnt lgkmcnt(0)
	v_add_f32_dpp v56, v56, v56 quad_perm:[2,3,0,1] row_mask:0xf bank_mask:0xf
	s_nop 1
	s_waitcnt lgkmcnt(0)
	v_add_f32_dpp v56, v56, v56 row_half_mirror row_mask:0xf bank_mask:0xf
	s_nop 1
	s_waitcnt lgkmcnt(0)
	v_add_f32_dpp v56, v56, v56 row_mirror row_mask:0xf bank_mask:0xf
	v_mov_b32_e32 v57, v56
	s_nop 1
	v_permlane16_swap_b32_e32 v57, v56
	s_waitcnt lgkmcnt(0)
	v_add_f32_e32 v56, v56, v57
	v_mov_b32_e32 v57, v56
	s_nop 1
	v_permlane32_swap_b32_e32 v57, v56
	s_waitcnt lgkmcnt(0)
	v_add_f32_e32 v56, v56, v57
	v_fmac_f32_e32 v53, 0xbc800000, v56
	v_mul_f32_e32 v56, v53, v53
	s_nop 1
	v_mov_b32_dpp v56, v56 quad_perm:[1,0,3,2] row_mask:0xf bank_mask:0xf
	s_waitcnt lgkmcnt(0)
	v_fmac_f32_e32 v56, v53, v53
	s_nop 1
	s_waitcnt lgkmcnt(0)
	v_add_f32_dpp v56, v56, v56 quad_perm:[2,3,0,1] row_mask:0xf bank_mask:0xf
	s_nop 1
	s_waitcnt lgkmcnt(0)
	v_add_f32_dpp v56, v56, v56 row_half_mirror row_mask:0xf bank_mask:0xf
	s_nop 1
	s_waitcnt lgkmcnt(0)
	v_add_f32_dpp v56, v56, v56 row_mirror row_mask:0xf bank_mask:0xf
	v_mov_b32_e32 v57, v56
	s_nop 1
	v_permlane16_swap_b32_e32 v57, v56
	s_waitcnt lgkmcnt(0)
	v_add_f32_e32 v56, v56, v57
	v_mov_b32_e32 v57, v56
	s_nop 1
	v_permlane32_swap_b32_e32 v57, v56
	s_waitcnt lgkmcnt(0)
	v_add_f32_e32 v56, v56, v57
	v_fmamk_f32 v56, v56, 0x3c800000, v164
	v_rsq_f32_e32 v56, v56
	s_nop 0
	v_mul_f32_e32 v53, v53, v56
	v_lshlrev_b32_e32 v56, 16, v149
	v_mul_f32_e32 v56, v191, v56
	v_mul_f32_e32 v57, v56, v172
	s_nop 1
	v_mov_b32_dpp v57, v57 quad_perm:[1,0,3,2] row_mask:0xf bank_mask:0xf
	v_fma_f32 v53, v173, v53, v170
	s_waitcnt lgkmcnt(0)
	v_fmac_f32_e32 v57, v56, v172
	s_nop 1
	s_waitcnt lgkmcnt(0)
	v_add_f32_dpp v56, v57, v57 quad_perm:[2,3,0,1] row_mask:0xf bank_mask:0xf
	s_nop 1
	s_waitcnt lgkmcnt(0)
	v_add_f32_dpp v56, v56, v56 row_half_mirror row_mask:0xf bank_mask:0xf
	s_nop 1
	s_waitcnt lgkmcnt(0)
	v_add_f32_dpp v56, v56, v56 row_mirror row_mask:0xf bank_mask:0xf
	v_mov_b32_e32 v57, v56
	s_nop 1
	v_permlane16_swap_b32_e32 v57, v56
	s_waitcnt lgkmcnt(0)
	v_add_f32_e32 v56, v56, v57
	v_mov_b32_e32 v57, v56
	s_nop 1
	v_permlane32_swap_b32_e32 v57, v56
	s_waitcnt lgkmcnt(0)
	v_add_f32_e32 v56, v56, v57
	v_fmac_f32_e32 v53, v56, v190
	v_mul_f32_e32 v53, v60, v53
	v_cvt_pk_bf16_f32 v52, v53, s0
	global_store_short v[50:51], v52, off offset:512
	v_lshlrev_b32_e32 v50, 16, v147
	v_add_f32_e32 v50, v50, v189
	v_mul_f32_e32 v51, v50, v50
	s_nop 1
	v_mov_b32_dpp v51, v51 quad_perm:[1,0,3,2] row_mask:0xf bank_mask:0xf
	s_waitcnt lgkmcnt(0)
	v_fmac_f32_e32 v51, v50, v50
	s_nop 1
	s_waitcnt lgkmcnt(0)
	v_add_f32_dpp v51, v51, v51 quad_perm:[2,3,0,1] row_mask:0xf bank_mask:0xf
	s_nop 1
	s_waitcnt lgkmcnt(0)
	v_add_f32_dpp v51, v51, v51 row_half_mirror row_mask:0xf bank_mask:0xf
	s_nop 1
	s_waitcnt lgkmcnt(0)
	v_add_f32_dpp v51, v51, v51 row_mirror row_mask:0xf bank_mask:0xf
	v_mov_b32_e32 v52, v51
	s_nop 1
	v_permlane16_swap_b32_e32 v52, v51
	s_waitcnt lgkmcnt(0)
	v_add_f32_e32 v51, v51, v52
	v_mov_b32_e32 v52, v51
	s_nop 1
	v_permlane32_swap_b32_e32 v52, v51
	s_waitcnt lgkmcnt(0)
	v_add_f32_e32 v51, v51, v52
	v_fmamk_f32 v51, v51, 0x3c800000, v165
	v_rsq_f32_e32 v51, v51
	s_nop 0
	v_mul_f32_e32 v50, v50, v51
	v_lshlrev_b32_e32 v51, 16, v148
	v_mul_f32_e32 v52, 0xbfb8aa3b, v51
	v_exp_f32_e32 v52, v52
	v_mul_f32_e32 v50, v176, v50
	v_add_f32_e32 v52, 1.0, v52
	v_rcp_f32_e32 v52, v52
	s_nop 0
	v_mul_f32_e32 v51, v52, v51
	v_mul_f32_e32 v50, v51, v50
	v_lshlrev_b32_e32 v51, 16, v146
	v_add_f32_e32 v51, v51, v188
	s_nop 1
	v_cvt_pk_bf16_f32 v50, v50, s0
	global_store_short v[48:49], v50, off
	s_waitcnt lgkmcnt(0)
	v_add_f32_dpp v52, v51, v51 quad_perm:[1,0,3,2] row_mask:0xf bank_mask:0xf
	s_nop 1
	s_waitcnt lgkmcnt(0)
	v_add_f32_dpp v52, v52, v52 quad_perm:[2,3,0,1] row_mask:0xf bank_mask:0xf
	s_nop 1
	s_waitcnt lgkmcnt(0)
	v_add_f32_dpp v52, v52, v52 row_half_mirror row_mask:0xf bank_mask:0xf
	s_nop 1
	s_waitcnt lgkmcnt(0)
	v_add_f32_dpp v52, v52, v52 row_mirror row_mask:0xf bank_mask:0xf
	v_mov_b32_e32 v53, v52
	s_nop 1
	v_permlane16_swap_b32_e32 v53, v52
	s_waitcnt lgkmcnt(0)
	v_add_f32_e32 v52, v52, v53
	v_mov_b32_e32 v53, v52
	s_nop 1
	v_permlane32_swap_b32_e32 v53, v52
	s_waitcnt lgkmcnt(0)
	v_add_f32_e32 v52, v52, v53
	v_fmac_f32_e32 v51, 0xbc800000, v52
	v_mul_f32_e32 v52, v51, v51
	s_nop 1
	v_mov_b32_dpp v52, v52 quad_perm:[1,0,3,2] row_mask:0xf bank_mask:0xf
	s_waitcnt lgkmcnt(0)
	v_fmac_f32_e32 v52, v51, v51
	s_nop 1
	s_waitcnt lgkmcnt(0)
	v_add_f32_dpp v52, v52, v52 quad_perm:[2,3,0,1] row_mask:0xf bank_mask:0xf
	s_nop 1
	s_waitcnt lgkmcnt(0)
	v_add_f32_dpp v52, v52, v52 row_half_mirror row_mask:0xf bank_mask:0xf
	s_nop 1
	s_waitcnt lgkmcnt(0)
	v_add_f32_dpp v52, v52, v52 row_mirror row_mask:0xf bank_mask:0xf
	v_mov_b32_e32 v53, v52
	s_nop 1
	v_permlane16_swap_b32_e32 v53, v52
	s_waitcnt lgkmcnt(0)
	v_add_f32_e32 v52, v52, v53
	v_mov_b32_e32 v53, v52
	s_nop 1
	v_permlane32_swap_b32_e32 v53, v52
	s_waitcnt lgkmcnt(0)
	v_add_f32_e32 v52, v52, v53
	v_fmamk_f32 v52, v52, 0x3c800000, v164
	v_rsq_f32_e32 v52, v52
	s_nop 0
	v_mul_f32_e32 v51, v51, v52
	v_lshlrev_b32_e32 v52, 16, v145
	v_mul_f32_e32 v52, v187, v52
	v_mul_f32_e32 v53, v52, v172
	s_nop 1
	v_mov_b32_dpp v53, v53 quad_perm:[1,0,3,2] row_mask:0xf bank_mask:0xf
	v_fma_f32 v51, v173, v51, v170
	s_waitcnt lgkmcnt(0)
	v_fmac_f32_e32 v53, v52, v172
	s_nop 1
	s_waitcnt lgkmcnt(0)
	v_add_f32_dpp v52, v53, v53 quad_perm:[2,3,0,1] row_mask:0xf bank_mask:0xf
	s_nop 1
	s_waitcnt lgkmcnt(0)
	v_add_f32_dpp v52, v52, v52 row_half_mirror row_mask:0xf bank_mask:0xf
	s_nop 1
	s_waitcnt lgkmcnt(0)
	v_add_f32_dpp v52, v52, v52 row_mirror row_mask:0xf bank_mask:0xf
	v_mov_b32_e32 v53, v52
	s_nop 1
	v_permlane16_swap_b32_e32 v53, v52
	s_waitcnt lgkmcnt(0)
	v_add_f32_e32 v52, v52, v53
	v_mov_b32_e32 v53, v52
	s_nop 1
	v_permlane32_swap_b32_e32 v53, v52
	s_waitcnt lgkmcnt(0)
	v_add_f32_e32 v52, v52, v53
	v_fmac_f32_e32 v51, v52, v186
	v_mul_f32_e32 v51, v61, v51
	v_cvt_pk_bf16_f32 v50, v51, s0
	global_store_short v[48:49], v50, off offset:512
	v_lshlrev_b32_e32 v48, 16, v143
	v_add_f32_e32 v48, v48, v185
	v_mul_f32_e32 v49, v48, v48
	s_nop 1
	v_mov_b32_dpp v49, v49 quad_perm:[1,0,3,2] row_mask:0xf bank_mask:0xf
	s_waitcnt lgkmcnt(0)
	v_fmac_f32_e32 v49, v48, v48
	s_nop 1
	s_waitcnt lgkmcnt(0)
	v_add_f32_dpp v49, v49, v49 quad_perm:[2,3,0,1] row_mask:0xf bank_mask:0xf
	s_nop 1
	s_waitcnt lgkmcnt(0)
	v_add_f32_dpp v49, v49, v49 row_half_mirror row_mask:0xf bank_mask:0xf
	s_nop 1
	s_waitcnt lgkmcnt(0)
	v_add_f32_dpp v49, v49, v49 row_mirror row_mask:0xf bank_mask:0xf
	v_mov_b32_e32 v50, v49
	s_nop 1
	v_permlane16_swap_b32_e32 v50, v49
	s_waitcnt lgkmcnt(0)
	v_add_f32_e32 v49, v49, v50
	v_mov_b32_e32 v50, v49
	s_nop 1
	v_permlane32_swap_b32_e32 v50, v49
	s_waitcnt lgkmcnt(0)
	v_add_f32_e32 v49, v49, v50
	v_fmamk_f32 v49, v49, 0x3c800000, v165
	v_rsq_f32_e32 v49, v49
	s_nop 0
	v_mul_f32_e32 v48, v48, v49
	v_lshlrev_b32_e32 v49, 16, v144
	v_mul_f32_e32 v50, 0xbfb8aa3b, v49
	v_exp_f32_e32 v50, v50
	v_mul_f32_e32 v48, v176, v48
	v_add_f32_e32 v50, 1.0, v50
	v_rcp_f32_e32 v50, v50
	s_nop 0
	v_mul_f32_e32 v49, v50, v49
	v_mul_f32_e32 v48, v49, v48
	v_lshlrev_b32_e32 v49, 16, v142
	v_add_f32_e32 v49, v49, v182
	s_nop 1
	v_cvt_pk_bf16_f32 v48, v48, s0
	global_store_short v[46:47], v48, off
	s_waitcnt lgkmcnt(0)
	v_add_f32_dpp v50, v49, v49 quad_perm:[1,0,3,2] row_mask:0xf bank_mask:0xf
	s_nop 1
	s_waitcnt lgkmcnt(0)
	v_add_f32_dpp v50, v50, v50 quad_perm:[2,3,0,1] row_mask:0xf bank_mask:0xf
	s_nop 1
	s_waitcnt lgkmcnt(0)
	v_add_f32_dpp v50, v50, v50 row_half_mirror row_mask:0xf bank_mask:0xf
	s_nop 1
	s_waitcnt lgkmcnt(0)
	v_add_f32_dpp v50, v50, v50 row_mirror row_mask:0xf bank_mask:0xf
	v_mov_b32_e32 v51, v50
	s_nop 1
	v_permlane16_swap_b32_e32 v51, v50
	s_waitcnt lgkmcnt(0)
	v_add_f32_e32 v50, v50, v51
	v_mov_b32_e32 v51, v50
	s_nop 1
	v_permlane32_swap_b32_e32 v51, v50
	s_waitcnt lgkmcnt(0)
	v_add_f32_e32 v50, v50, v51
	v_fmac_f32_e32 v49, 0xbc800000, v50
	v_mul_f32_e32 v50, v49, v49
	s_nop 1
	v_mov_b32_dpp v50, v50 quad_perm:[1,0,3,2] row_mask:0xf bank_mask:0xf
	s_waitcnt lgkmcnt(0)
	v_fmac_f32_e32 v50, v49, v49
	s_nop 1
	s_waitcnt lgkmcnt(0)
	v_add_f32_dpp v50, v50, v50 quad_perm:[2,3,0,1] row_mask:0xf bank_mask:0xf
	s_nop 1
	s_waitcnt lgkmcnt(0)
	v_add_f32_dpp v50, v50, v50 row_half_mirror row_mask:0xf bank_mask:0xf
	s_nop 1
	s_waitcnt lgkmcnt(0)
	v_add_f32_dpp v50, v50, v50 row_mirror row_mask:0xf bank_mask:0xf
	v_mov_b32_e32 v51, v50
	s_nop 1
	v_permlane16_swap_b32_e32 v51, v50
	s_waitcnt lgkmcnt(0)
	v_add_f32_e32 v50, v50, v51
	v_mov_b32_e32 v51, v50
	s_nop 1
	v_permlane32_swap_b32_e32 v51, v50
	s_waitcnt lgkmcnt(0)
	v_add_f32_e32 v50, v50, v51
	v_fmamk_f32 v50, v50, 0x3c800000, v164
	v_rsq_f32_e32 v50, v50
	s_nop 0
	v_mul_f32_e32 v49, v49, v50
	v_lshlrev_b32_e32 v50, 16, v141
	v_mul_f32_e32 v50, v180, v50
	v_mul_f32_e32 v51, v50, v172
	s_nop 1
	v_mov_b32_dpp v51, v51 quad_perm:[1,0,3,2] row_mask:0xf bank_mask:0xf
	v_fma_f32 v49, v173, v49, v170
	s_waitcnt lgkmcnt(0)
	v_fmac_f32_e32 v51, v50, v172
	s_nop 1
	s_waitcnt lgkmcnt(0)
	v_add_f32_dpp v50, v51, v51 quad_perm:[2,3,0,1] row_mask:0xf bank_mask:0xf
	s_nop 1
	s_waitcnt lgkmcnt(0)
	v_add_f32_dpp v50, v50, v50 row_half_mirror row_mask:0xf bank_mask:0xf
	s_nop 1
	s_waitcnt lgkmcnt(0)
	v_add_f32_dpp v50, v50, v50 row_mirror row_mask:0xf bank_mask:0xf
	v_mov_b32_e32 v51, v50
	s_nop 1
	v_permlane16_swap_b32_e32 v51, v50
	s_waitcnt lgkmcnt(0)
	v_add_f32_e32 v50, v50, v51
	v_mov_b32_e32 v51, v50
	s_nop 1
	v_permlane32_swap_b32_e32 v51, v50
	s_waitcnt lgkmcnt(0)
	v_add_f32_e32 v50, v50, v51
	v_fmac_f32_e32 v49, v50, v175
	v_mul_f32_e32 v49, v54, v49
	v_cvt_pk_bf16_f32 v48, v49, s0
	global_store_short v[46:47], v48, off offset:512
	v_lshlrev_b32_e32 v46, 16, v139
	v_add_f32_e32 v46, v46, v174
	v_mul_f32_e32 v47, v46, v46
	s_nop 1
	v_mov_b32_dpp v47, v47 quad_perm:[1,0,3,2] row_mask:0xf bank_mask:0xf
	s_waitcnt lgkmcnt(0)
	v_fmac_f32_e32 v47, v46, v46
	s_nop 1
	s_waitcnt lgkmcnt(0)
	v_add_f32_dpp v47, v47, v47 quad_perm:[2,3,0,1] row_mask:0xf bank_mask:0xf
	s_nop 1
	s_waitcnt lgkmcnt(0)
	v_add_f32_dpp v47, v47, v47 row_half_mirror row_mask:0xf bank_mask:0xf
	s_nop 1
	s_waitcnt lgkmcnt(0)
	v_add_f32_dpp v47, v47, v47 row_mirror row_mask:0xf bank_mask:0xf
	v_mov_b32_e32 v48, v47
	s_nop 1
	v_permlane16_swap_b32_e32 v48, v47
	s_waitcnt lgkmcnt(0)
	v_add_f32_e32 v47, v47, v48
	v_mov_b32_e32 v48, v47
	s_nop 1
	v_permlane32_swap_b32_e32 v48, v47
	s_waitcnt lgkmcnt(0)
	v_add_f32_e32 v47, v47, v48
	v_fmamk_f32 v47, v47, 0x3c800000, v165
	v_rsq_f32_e32 v47, v47
	s_nop 0
	v_mul_f32_e32 v46, v46, v47
	v_lshlrev_b32_e32 v47, 16, v140
	v_mul_f32_e32 v48, 0xbfb8aa3b, v47
	v_exp_f32_e32 v48, v48
	v_mul_f32_e32 v46, v176, v46
	v_add_f32_e32 v48, 1.0, v48
	v_rcp_f32_e32 v48, v48
	s_nop 0
	v_mul_f32_e32 v47, v48, v47
	v_mul_f32_e32 v46, v47, v46
	v_lshlrev_b32_e32 v47, 16, v138
	v_add_f32_e32 v47, v47, v171
	s_nop 1
	v_cvt_pk_bf16_f32 v46, v46, s0
	global_store_short v[44:45], v46, off
	s_waitcnt lgkmcnt(0)
	v_add_f32_dpp v48, v47, v47 quad_perm:[1,0,3,2] row_mask:0xf bank_mask:0xf
	s_nop 1
	s_waitcnt lgkmcnt(0)
	v_add_f32_dpp v48, v48, v48 quad_perm:[2,3,0,1] row_mask:0xf bank_mask:0xf
	s_nop 1
	s_waitcnt lgkmcnt(0)
	v_add_f32_dpp v48, v48, v48 row_half_mirror row_mask:0xf bank_mask:0xf
	s_nop 1
	s_waitcnt lgkmcnt(0)
	v_add_f32_dpp v48, v48, v48 row_mirror row_mask:0xf bank_mask:0xf
	v_mov_b32_e32 v49, v48
	s_nop 1
	v_permlane16_swap_b32_e32 v49, v48
	s_waitcnt lgkmcnt(0)
	v_add_f32_e32 v48, v48, v49
	v_mov_b32_e32 v49, v48
	s_nop 1
	v_permlane32_swap_b32_e32 v49, v48
	s_waitcnt lgkmcnt(0)
	v_add_f32_e32 v48, v48, v49
	v_fmac_f32_e32 v47, 0xbc800000, v48
	v_mul_f32_e32 v48, v47, v47
	s_nop 1
	v_mov_b32_dpp v48, v48 quad_perm:[1,0,3,2] row_mask:0xf bank_mask:0xf
	s_waitcnt lgkmcnt(0)
	v_fmac_f32_e32 v48, v47, v47
	s_nop 1
	s_waitcnt lgkmcnt(0)
	v_add_f32_dpp v48, v48, v48 quad_perm:[2,3,0,1] row_mask:0xf bank_mask:0xf
	s_nop 1
	s_waitcnt lgkmcnt(0)
	v_add_f32_dpp v48, v48, v48 row_half_mirror row_mask:0xf bank_mask:0xf
	s_nop 1
	s_waitcnt lgkmcnt(0)
	v_add_f32_dpp v48, v48, v48 row_mirror row_mask:0xf bank_mask:0xf
	v_mov_b32_e32 v49, v48
	s_nop 1
	v_permlane16_swap_b32_e32 v49, v48
	s_waitcnt lgkmcnt(0)
	v_add_f32_e32 v48, v48, v49
	v_mov_b32_e32 v49, v48
	s_nop 1
	v_permlane32_swap_b32_e32 v49, v48
	s_waitcnt lgkmcnt(0)
	v_add_f32_e32 v48, v48, v49
	v_fmamk_f32 v48, v48, 0x3c800000, v164
	v_rsq_f32_e32 v48, v48
	s_nop 0
	v_mul_f32_e32 v47, v47, v48
	v_fmac_f32_e32 v170, v173, v47
	v_lshlrev_b32_e32 v47, 16, v137
	v_mul_f32_e32 v47, v169, v47
	v_mul_f32_e32 v48, v47, v172
	s_nop 1
	v_mov_b32_dpp v48, v48 quad_perm:[1,0,3,2] row_mask:0xf bank_mask:0xf
	s_waitcnt lgkmcnt(0)
	v_fmac_f32_e32 v48, v47, v172
	s_nop 1
	s_waitcnt lgkmcnt(0)
	v_add_f32_dpp v47, v48, v48 quad_perm:[2,3,0,1] row_mask:0xf bank_mask:0xf
	s_nop 1
	s_waitcnt lgkmcnt(0)
	v_add_f32_dpp v47, v47, v47 row_half_mirror row_mask:0xf bank_mask:0xf
	s_nop 1
	s_waitcnt lgkmcnt(0)
	v_add_f32_dpp v47, v47, v47 row_mirror row_mask:0xf bank_mask:0xf
	v_mov_b32_e32 v48, v47
	s_nop 1
	v_permlane16_swap_b32_e32 v48, v47
	s_waitcnt lgkmcnt(0)
	v_add_f32_e32 v47, v47, v48
	v_mov_b32_e32 v48, v47
	s_nop 1
	v_permlane32_swap_b32_e32 v48, v47
	s_waitcnt lgkmcnt(0)
	v_add_f32_e32 v47, v47, v48
	v_fmac_f32_e32 v170, v47, v163
	v_mul_f32_e32 v47, v55, v170
	v_cvt_pk_bf16_f32 v46, v47, s0
	global_store_short v[44:45], v46, off offset:512
	global_load_dword v45, v[30:31], off
	s_nop 0
	global_load_dword v44, v[32:33], off
	v_lshlrev_b32_e32 v46, 16, v135
	v_add_f32_e32 v46, v46, v71
	v_lshlrev_b32_e32 v47, 16, v136
	s_waitcnt vmcnt(1)
	v_fmac_f32_e32 v46, v45, v47
	v_mul_f32_e32 v47, 0xbfb8aa3b, v70
	v_exp_f32_e32 v47, v47
	s_nop 0
	v_add_f32_e32 v47, 1.0, v47
	v_rcp_f32_e32 v47, v47
	s_nop 0
	v_mul_f32_e32 v47, v47, v70
	v_mul_f32_e32 v46, v47, v46
	v_mul_f32_e32 v47, v46, v46
	s_nop 1
	v_mov_b32_dpp v47, v47 quad_perm:[1,0,3,2] row_mask:0xf bank_mask:0xf
	s_waitcnt lgkmcnt(0)
	v_fmac_f32_e32 v47, v46, v46
	s_nop 1
	s_waitcnt lgkmcnt(0)
	v_add_f32_dpp v47, v47, v47 quad_perm:[2,3,0,1] row_mask:0xf bank_mask:0xf
	s_nop 1
	s_waitcnt lgkmcnt(0)
	v_add_f32_dpp v47, v47, v47 row_half_mirror row_mask:0xf bank_mask:0xf
	s_nop 1
	s_waitcnt lgkmcnt(0)
	v_add_f32_dpp v47, v47, v47 row_mirror row_mask:0xf bank_mask:0xf
	v_mov_b32_e32 v48, v47
	s_nop 1
	v_permlane16_swap_b32_e32 v48, v47
	s_waitcnt lgkmcnt(0)
	v_add_f32_e32 v47, v47, v48
	v_mov_b32_e32 v48, v47
	s_nop 1
	v_permlane32_swap_b32_e32 v48, v47
	s_and_saveexec_b64 s[0:1], vcc
	s_cbranch_execz .LBB0_1237
	s_waitcnt lgkmcnt(0)
	v_add_f32_e32 v47, v47, v48
	v_mov_b32_e32 v48, s11
	ds_write_b32 v48, v47 offset:4096
.LBB0_1237:
	s_or_b64 exec, exec, s[0:1]
	v_lshlrev_b32_e32 v47, 16, v132
	v_lshlrev_b32_e32 v49, 16, v131
	s_waitcnt lgkmcnt(0)
	v_lshlrev_b32_e32 v48, 16, v134
	v_add_f32_e32 v47, v49, v47
	v_lshlrev_b32_e32 v49, 16, v133
	v_fmac_f32_e32 v47, v45, v49
	v_mul_f32_e32 v49, 0xbfb8aa3b, v48
	v_exp_f32_e32 v49, v49
	s_nop 0
	v_add_f32_e32 v49, 1.0, v49
	v_rcp_f32_e32 v49, v49
	s_nop 0
	v_mul_f32_e32 v48, v49, v48
	v_mul_f32_e32 v47, v48, v47
	v_mul_f32_e32 v48, v47, v47
	s_nop 1
	v_mov_b32_dpp v48, v48 quad_perm:[1,0,3,2] row_mask:0xf bank_mask:0xf
	s_waitcnt lgkmcnt(0)
	v_fmac_f32_e32 v48, v47, v47
	s_nop 1
	s_waitcnt lgkmcnt(0)
	v_add_f32_dpp v48, v48, v48 quad_perm:[2,3,0,1] row_mask:0xf bank_mask:0xf
	s_nop 1
	s_waitcnt lgkmcnt(0)
	v_add_f32_dpp v48, v48, v48 row_half_mirror row_mask:0xf bank_mask:0xf
	s_nop 1
	s_waitcnt lgkmcnt(0)
	v_add_f32_dpp v48, v48, v48 row_mirror row_mask:0xf bank_mask:0xf
	v_mov_b32_e32 v49, v48
	s_nop 1
	v_permlane16_swap_b32_e32 v49, v48
	s_waitcnt lgkmcnt(0)
	v_add_f32_e32 v48, v48, v49
	v_mov_b32_e32 v49, v48
	s_nop 1
	v_permlane32_swap_b32_e32 v49, v48
	s_and_saveexec_b64 s[0:1], vcc
	s_cbranch_execz .LBB0_1239
	s_waitcnt lgkmcnt(0)
	v_add_f32_e32 v48, v48, v49
	v_mov_b32_e32 v49, s11
	ds_write_b32 v49, v48 offset:4128
.LBB0_1239:
	s_or_b64 exec, exec, s[0:1]
	v_lshlrev_b32_e32 v48, 16, v128
	v_lshlrev_b32_e32 v50, 16, v127
	s_waitcnt lgkmcnt(0)
	v_lshlrev_b32_e32 v49, 16, v130
	v_add_f32_e32 v48, v50, v48
	v_lshlrev_b32_e32 v50, 16, v129
	v_fmac_f32_e32 v48, v45, v50
	v_mul_f32_e32 v50, 0xbfb8aa3b, v49
	v_exp_f32_e32 v50, v50
	s_nop 0
	v_add_f32_e32 v50, 1.0, v50
	v_rcp_f32_e32 v50, v50
	s_nop 0
	v_mul_f32_e32 v49, v50, v49
	v_mul_f32_e32 v48, v49, v48
	v_mul_f32_e32 v49, v48, v48
	s_nop 1
	v_mov_b32_dpp v49, v49 quad_perm:[1,0,3,2] row_mask:0xf bank_mask:0xf
	s_waitcnt lgkmcnt(0)
	v_fmac_f32_e32 v49, v48, v48
	s_nop 1
	s_waitcnt lgkmcnt(0)
	v_add_f32_dpp v49, v49, v49 quad_perm:[2,3,0,1] row_mask:0xf bank_mask:0xf
	s_nop 1
	s_waitcnt lgkmcnt(0)
	v_add_f32_dpp v49, v49, v49 row_half_mirror row_mask:0xf bank_mask:0xf
	s_nop 1
	s_waitcnt lgkmcnt(0)
	v_add_f32_dpp v49, v49, v49 row_mirror row_mask:0xf bank_mask:0xf
	v_mov_b32_e32 v50, v49
	s_nop 1
	v_permlane16_swap_b32_e32 v50, v49
	s_waitcnt lgkmcnt(0)
	v_add_f32_e32 v49, v49, v50
	v_mov_b32_e32 v50, v49
	s_nop 1
	v_permlane32_swap_b32_e32 v50, v49
	s_and_saveexec_b64 s[0:1], vcc
	s_cbranch_execz .LBB0_1241
	s_waitcnt lgkmcnt(0)
	v_add_f32_e32 v49, v49, v50
	v_mov_b32_e32 v50, s11
	ds_write_b32 v50, v49 offset:4160
.LBB0_1241:
	s_or_b64 exec, exec, s[0:1]
	v_lshlrev_b32_e32 v49, 16, v124
	v_lshlrev_b32_e32 v51, 16, v123
	s_waitcnt lgkmcnt(0)
	v_lshlrev_b32_e32 v50, 16, v126
	v_add_f32_e32 v49, v51, v49
	v_lshlrev_b32_e32 v51, 16, v125
	v_fmac_f32_e32 v49, v45, v51
	v_mul_f32_e32 v51, 0xbfb8aa3b, v50
	v_exp_f32_e32 v51, v51
	s_nop 0
	v_add_f32_e32 v51, 1.0, v51
	v_rcp_f32_e32 v51, v51
	s_nop 0
	v_mul_f32_e32 v50, v51, v50
	v_mul_f32_e32 v49, v50, v49
	v_mul_f32_e32 v50, v49, v49
	s_nop 1
	v_mov_b32_dpp v50, v50 quad_perm:[1,0,3,2] row_mask:0xf bank_mask:0xf
	s_waitcnt lgkmcnt(0)
	v_fmac_f32_e32 v50, v49, v49
	s_nop 1
	s_waitcnt lgkmcnt(0)
	v_add_f32_dpp v50, v50, v50 quad_perm:[2,3,0,1] row_mask:0xf bank_mask:0xf
	s_nop 1
	s_waitcnt lgkmcnt(0)
	v_add_f32_dpp v50, v50, v50 row_half_mirror row_mask:0xf bank_mask:0xf
	s_nop 1
	s_waitcnt lgkmcnt(0)
	v_add_f32_dpp v50, v50, v50 row_mirror row_mask:0xf bank_mask:0xf
	v_mov_b32_e32 v51, v50
	s_nop 1
	v_permlane16_swap_b32_e32 v51, v50
	s_waitcnt lgkmcnt(0)
	v_add_f32_e32 v50, v50, v51
	v_mov_b32_e32 v51, v50
	s_nop 1
	v_permlane32_swap_b32_e32 v51, v50
	s_and_saveexec_b64 s[0:1], vcc
	s_cbranch_execz .LBB0_1243
	s_waitcnt lgkmcnt(0)
	v_add_f32_e32 v50, v50, v51
	v_mov_b32_e32 v51, s11
	ds_write_b32 v51, v50 offset:4192
.LBB0_1243:
	s_or_b64 exec, exec, s[0:1]
	v_lshlrev_b32_e32 v50, 16, v120
	v_lshlrev_b32_e32 v52, 16, v119
	s_waitcnt lgkmcnt(0)
	v_lshlrev_b32_e32 v51, 16, v122
	v_add_f32_e32 v50, v52, v50
	v_lshlrev_b32_e32 v52, 16, v121
	v_fmac_f32_e32 v50, v45, v52
	v_mul_f32_e32 v52, 0xbfb8aa3b, v51
	v_exp_f32_e32 v52, v52
	s_nop 0
	v_add_f32_e32 v52, 1.0, v52
	v_rcp_f32_e32 v52, v52
	s_nop 0
	v_mul_f32_e32 v51, v52, v51
	v_mul_f32_e32 v50, v51, v50
	v_mul_f32_e32 v51, v50, v50
	s_nop 1
	v_mov_b32_dpp v51, v51 quad_perm:[1,0,3,2] row_mask:0xf bank_mask:0xf
	s_waitcnt lgkmcnt(0)
	v_fmac_f32_e32 v51, v50, v50
	s_nop 1
	s_waitcnt lgkmcnt(0)
	v_add_f32_dpp v51, v51, v51 quad_perm:[2,3,0,1] row_mask:0xf bank_mask:0xf
	s_nop 1
	s_waitcnt lgkmcnt(0)
	v_add_f32_dpp v51, v51, v51 row_half_mirror row_mask:0xf bank_mask:0xf
	s_nop 1
	s_waitcnt lgkmcnt(0)
	v_add_f32_dpp v51, v51, v51 row_mirror row_mask:0xf bank_mask:0xf
	v_mov_b32_e32 v52, v51
	s_nop 1
	v_permlane16_swap_b32_e32 v52, v51
	s_waitcnt lgkmcnt(0)
	v_add_f32_e32 v51, v51, v52
	v_mov_b32_e32 v52, v51
	s_nop 1
	v_permlane32_swap_b32_e32 v52, v51
	s_and_saveexec_b64 s[0:1], vcc
	s_cbranch_execz .LBB0_1245
	s_waitcnt lgkmcnt(0)
	v_add_f32_e32 v51, v51, v52
	v_mov_b32_e32 v52, s11
	ds_write_b32 v52, v51 offset:4224
.LBB0_1245:
	s_or_b64 exec, exec, s[0:1]
	v_lshlrev_b32_e32 v51, 16, v116
	v_lshlrev_b32_e32 v53, 16, v115
	s_waitcnt lgkmcnt(0)
	v_lshlrev_b32_e32 v52, 16, v118
	v_add_f32_e32 v51, v53, v51
	v_lshlrev_b32_e32 v53, 16, v117
	v_fmac_f32_e32 v51, v45, v53
	v_mul_f32_e32 v53, 0xbfb8aa3b, v52
	v_exp_f32_e32 v53, v53
	s_nop 0
	v_add_f32_e32 v53, 1.0, v53
	v_rcp_f32_e32 v53, v53
	s_nop 0
	v_mul_f32_e32 v52, v53, v52
	v_mul_f32_e32 v51, v52, v51
	v_mul_f32_e32 v52, v51, v51
	s_nop 1
	v_mov_b32_dpp v52, v52 quad_perm:[1,0,3,2] row_mask:0xf bank_mask:0xf
	s_waitcnt lgkmcnt(0)
	v_fmac_f32_e32 v52, v51, v51
	s_nop 1
	s_waitcnt lgkmcnt(0)
	v_add_f32_dpp v52, v52, v52 quad_perm:[2,3,0,1] row_mask:0xf bank_mask:0xf
	s_nop 1
	s_waitcnt lgkmcnt(0)
	v_add_f32_dpp v52, v52, v52 row_half_mirror row_mask:0xf bank_mask:0xf
	s_nop 1
	s_waitcnt lgkmcnt(0)
	v_add_f32_dpp v52, v52, v52 row_mirror row_mask:0xf bank_mask:0xf
	v_mov_b32_e32 v53, v52
	s_nop 1
	v_permlane16_swap_b32_e32 v53, v52
	s_waitcnt lgkmcnt(0)
	v_add_f32_e32 v52, v52, v53
	v_mov_b32_e32 v53, v52
	s_nop 1
	v_permlane32_swap_b32_e32 v53, v52
	s_and_saveexec_b64 s[0:1], vcc
	s_cbranch_execz .LBB0_1247
	s_waitcnt lgkmcnt(0)
	v_add_f32_e32 v52, v52, v53
	v_mov_b32_e32 v53, s11
	ds_write_b32 v53, v52 offset:4256
.LBB0_1247:
	s_or_b64 exec, exec, s[0:1]
	v_lshlrev_b32_e32 v52, 16, v112
	v_lshlrev_b32_e32 v54, 16, v111
	s_waitcnt lgkmcnt(0)
	v_lshlrev_b32_e32 v53, 16, v114
	v_add_f32_e32 v52, v54, v52
	v_lshlrev_b32_e32 v54, 16, v113
	v_fmac_f32_e32 v52, v45, v54
	v_mul_f32_e32 v54, 0xbfb8aa3b, v53
	v_exp_f32_e32 v54, v54
	s_nop 0
	v_add_f32_e32 v54, 1.0, v54
	v_rcp_f32_e32 v54, v54
	s_nop 0
	v_mul_f32_e32 v53, v54, v53
	v_mul_f32_e32 v52, v53, v52
	v_mul_f32_e32 v53, v52, v52
	s_nop 1
	v_mov_b32_dpp v53, v53 quad_perm:[1,0,3,2] row_mask:0xf bank_mask:0xf
	s_waitcnt lgkmcnt(0)
	v_fmac_f32_e32 v53, v52, v52
	s_nop 1
	s_waitcnt lgkmcnt(0)
	v_add_f32_dpp v53, v53, v53 quad_perm:[2,3,0,1] row_mask:0xf bank_mask:0xf
	s_nop 1
	s_waitcnt lgkmcnt(0)
	v_add_f32_dpp v53, v53, v53 row_half_mirror row_mask:0xf bank_mask:0xf
	s_nop 1
	s_waitcnt lgkmcnt(0)
	v_add_f32_dpp v53, v53, v53 row_mirror row_mask:0xf bank_mask:0xf
	v_mov_b32_e32 v54, v53
	s_nop 1
	v_permlane16_swap_b32_e32 v54, v53
	s_waitcnt lgkmcnt(0)
	v_add_f32_e32 v53, v53, v54
	v_mov_b32_e32 v54, v53
	s_nop 1
	v_permlane32_swap_b32_e32 v54, v53
	s_and_saveexec_b64 s[0:1], vcc
	s_cbranch_execz .LBB0_1249
	s_waitcnt lgkmcnt(0)
	v_add_f32_e32 v53, v53, v54
	v_mov_b32_e32 v54, s11
	ds_write_b32 v54, v53 offset:4288
.LBB0_1249:
	s_or_b64 exec, exec, s[0:1]
	v_lshlrev_b32_e32 v53, 16, v108
	v_lshlrev_b32_e32 v55, 16, v107
	s_waitcnt lgkmcnt(0)
	v_lshlrev_b32_e32 v54, 16, v110
	v_add_f32_e32 v53, v55, v53
	v_lshlrev_b32_e32 v55, 16, v109
	v_fmac_f32_e32 v53, v45, v55
	v_mul_f32_e32 v55, 0xbfb8aa3b, v54
	v_exp_f32_e32 v55, v55
	s_nop 0
	v_add_f32_e32 v55, 1.0, v55
	v_rcp_f32_e32 v55, v55
	s_nop 0
	v_mul_f32_e32 v54, v55, v54
	v_mul_f32_e32 v53, v54, v53
	v_mul_f32_e32 v54, v53, v53
	s_nop 1
	v_mov_b32_dpp v54, v54 quad_perm:[1,0,3,2] row_mask:0xf bank_mask:0xf
	s_waitcnt lgkmcnt(0)
	v_fmac_f32_e32 v54, v53, v53
	s_nop 1
	s_waitcnt lgkmcnt(0)
	v_add_f32_dpp v54, v54, v54 quad_perm:[2,3,0,1] row_mask:0xf bank_mask:0xf
	s_nop 1
	s_waitcnt lgkmcnt(0)
	v_add_f32_dpp v54, v54, v54 row_half_mirror row_mask:0xf bank_mask:0xf
	s_nop 1
	s_waitcnt lgkmcnt(0)
	v_add_f32_dpp v54, v54, v54 row_mirror row_mask:0xf bank_mask:0xf
	v_mov_b32_e32 v55, v54
	s_nop 1
	v_permlane16_swap_b32_e32 v55, v54
	s_waitcnt lgkmcnt(0)
	v_add_f32_e32 v54, v54, v55
	v_mov_b32_e32 v55, v54
	s_nop 1
	v_permlane32_swap_b32_e32 v55, v54
	s_and_saveexec_b64 s[0:1], vcc
	s_cbranch_execz .LBB0_1251
	s_waitcnt lgkmcnt(0)
	v_add_f32_e32 v54, v54, v55
	v_mov_b32_e32 v55, s11
	ds_write_b32 v55, v54 offset:4320
.LBB0_1251:
	s_or_b64 exec, exec, s[0:1]
	v_lshlrev_b32_e32 v54, 16, v104
	v_lshlrev_b32_e32 v56, 16, v103
	s_waitcnt lgkmcnt(0)
	v_lshlrev_b32_e32 v55, 16, v106
	v_add_f32_e32 v54, v56, v54
	v_lshlrev_b32_e32 v56, 16, v105
	v_fmac_f32_e32 v54, v45, v56
	v_mul_f32_e32 v56, 0xbfb8aa3b, v55
	v_exp_f32_e32 v56, v56
	s_nop 0
	v_add_f32_e32 v56, 1.0, v56
	v_rcp_f32_e32 v56, v56
	s_nop 0
	v_mul_f32_e32 v55, v56, v55
	v_mul_f32_e32 v54, v55, v54
	v_mul_f32_e32 v55, v54, v54
	s_nop 1
	v_mov_b32_dpp v55, v55 quad_perm:[1,0,3,2] row_mask:0xf bank_mask:0xf
	s_waitcnt lgkmcnt(0)
	v_fmac_f32_e32 v55, v54, v54
	s_nop 1
	s_waitcnt lgkmcnt(0)
	v_add_f32_dpp v55, v55, v55 quad_perm:[2,3,0,1] row_mask:0xf bank_mask:0xf
	s_nop 1
	s_waitcnt lgkmcnt(0)
	v_add_f32_dpp v55, v55, v55 row_half_mirror row_mask:0xf bank_mask:0xf
	s_nop 1
	s_waitcnt lgkmcnt(0)
	v_add_f32_dpp v55, v55, v55 row_mirror row_mask:0xf bank_mask:0xf
	v_mov_b32_e32 v56, v55
	s_nop 1
	v_permlane16_swap_b32_e32 v56, v55
	s_waitcnt lgkmcnt(0)
	v_add_f32_e32 v55, v55, v56
	v_mov_b32_e32 v56, v55
	s_nop 1
	v_permlane32_swap_b32_e32 v56, v55
	s_and_saveexec_b64 s[0:1], vcc
	s_cbranch_execz .LBB0_1253
	s_waitcnt lgkmcnt(0)
	v_add_f32_e32 v55, v55, v56
	v_mov_b32_e32 v56, s11
	ds_write_b32 v56, v55 offset:4352
.LBB0_1253:
	s_or_b64 exec, exec, s[0:1]
	v_lshlrev_b32_e32 v55, 16, v100
	v_lshlrev_b32_e32 v57, 16, v99
	s_waitcnt lgkmcnt(0)
	v_lshlrev_b32_e32 v56, 16, v102
	v_add_f32_e32 v55, v57, v55
	v_lshlrev_b32_e32 v57, 16, v101
	v_fmac_f32_e32 v55, v45, v57
	v_mul_f32_e32 v57, 0xbfb8aa3b, v56
	v_exp_f32_e32 v57, v57
	s_nop 0
	v_add_f32_e32 v57, 1.0, v57
	v_rcp_f32_e32 v57, v57
	s_nop 0
	v_mul_f32_e32 v56, v57, v56
	v_mul_f32_e32 v55, v56, v55
	v_mul_f32_e32 v56, v55, v55
	s_nop 1
	v_mov_b32_dpp v56, v56 quad_perm:[1,0,3,2] row_mask:0xf bank_mask:0xf
	s_waitcnt lgkmcnt(0)
	v_fmac_f32_e32 v56, v55, v55
	s_nop 1
	s_waitcnt lgkmcnt(0)
	v_add_f32_dpp v56, v56, v56 quad_perm:[2,3,0,1] row_mask:0xf bank_mask:0xf
	s_nop 1
	s_waitcnt lgkmcnt(0)
	v_add_f32_dpp v56, v56, v56 row_half_mirror row_mask:0xf bank_mask:0xf
	s_nop 1
	s_waitcnt lgkmcnt(0)
	v_add_f32_dpp v56, v56, v56 row_mirror row_mask:0xf bank_mask:0xf
	v_mov_b32_e32 v57, v56
	s_nop 1
	v_permlane16_swap_b32_e32 v57, v56
	s_waitcnt lgkmcnt(0)
	v_add_f32_e32 v56, v56, v57
	v_mov_b32_e32 v57, v56
	s_nop 1
	v_permlane32_swap_b32_e32 v57, v56
	s_and_saveexec_b64 s[0:1], vcc
	s_cbranch_execz .LBB0_1255
	s_waitcnt lgkmcnt(0)
	v_add_f32_e32 v56, v56, v57
	v_mov_b32_e32 v57, s11
	ds_write_b32 v57, v56 offset:4384
.LBB0_1255:
	s_or_b64 exec, exec, s[0:1]
	v_lshlrev_b32_e32 v56, 16, v96
	v_lshlrev_b32_e32 v58, 16, v95
	s_waitcnt lgkmcnt(0)
	v_lshlrev_b32_e32 v57, 16, v98
	v_add_f32_e32 v56, v58, v56
	v_lshlrev_b32_e32 v58, 16, v97
	v_fmac_f32_e32 v56, v45, v58
	v_mul_f32_e32 v58, 0xbfb8aa3b, v57
	v_exp_f32_e32 v58, v58
	s_nop 0
	v_add_f32_e32 v58, 1.0, v58
	v_rcp_f32_e32 v58, v58
	s_nop 0
	v_mul_f32_e32 v57, v58, v57
	v_mul_f32_e32 v56, v57, v56
	v_mul_f32_e32 v57, v56, v56
	s_nop 1
	v_mov_b32_dpp v57, v57 quad_perm:[1,0,3,2] row_mask:0xf bank_mask:0xf
	s_waitcnt lgkmcnt(0)
	v_fmac_f32_e32 v57, v56, v56
	s_nop 1
	s_waitcnt lgkmcnt(0)
	v_add_f32_dpp v57, v57, v57 quad_perm:[2,3,0,1] row_mask:0xf bank_mask:0xf
	s_nop 1
	s_waitcnt lgkmcnt(0)
	v_add_f32_dpp v57, v57, v57 row_half_mirror row_mask:0xf bank_mask:0xf
	s_nop 1
	s_waitcnt lgkmcnt(0)
	v_add_f32_dpp v57, v57, v57 row_mirror row_mask:0xf bank_mask:0xf
	v_mov_b32_e32 v58, v57
	s_nop 1
	v_permlane16_swap_b32_e32 v58, v57
	s_waitcnt lgkmcnt(0)
	v_add_f32_e32 v57, v57, v58
	v_mov_b32_e32 v58, v57
	s_nop 1
	v_permlane32_swap_b32_e32 v58, v57
	s_and_saveexec_b64 s[0:1], vcc
	s_cbranch_execz .LBB0_1257
	s_waitcnt lgkmcnt(0)
	v_add_f32_e32 v57, v57, v58
	v_mov_b32_e32 v58, s11
	ds_write_b32 v58, v57 offset:4416
.LBB0_1257:
	s_or_b64 exec, exec, s[0:1]
	v_lshlrev_b32_e32 v57, 16, v92
	v_lshlrev_b32_e32 v59, 16, v91
	s_waitcnt lgkmcnt(0)
	v_lshlrev_b32_e32 v58, 16, v94
	v_add_f32_e32 v57, v59, v57
	v_lshlrev_b32_e32 v59, 16, v93
	v_fmac_f32_e32 v57, v45, v59
	v_mul_f32_e32 v59, 0xbfb8aa3b, v58
	v_exp_f32_e32 v59, v59
	s_nop 0
	v_add_f32_e32 v59, 1.0, v59
	v_rcp_f32_e32 v59, v59
	s_nop 0
	v_mul_f32_e32 v58, v59, v58
	v_mul_f32_e32 v57, v58, v57
	v_mul_f32_e32 v58, v57, v57
	s_nop 1
	v_mov_b32_dpp v58, v58 quad_perm:[1,0,3,2] row_mask:0xf bank_mask:0xf
	s_waitcnt lgkmcnt(0)
	v_fmac_f32_e32 v58, v57, v57
	s_nop 1
	s_waitcnt lgkmcnt(0)
	v_add_f32_dpp v58, v58, v58 quad_perm:[2,3,0,1] row_mask:0xf bank_mask:0xf
	s_nop 1
	s_waitcnt lgkmcnt(0)
	v_add_f32_dpp v58, v58, v58 row_half_mirror row_mask:0xf bank_mask:0xf
	s_nop 1
	s_waitcnt lgkmcnt(0)
	v_add_f32_dpp v58, v58, v58 row_mirror row_mask:0xf bank_mask:0xf
	v_mov_b32_e32 v59, v58
	s_nop 1
	v_permlane16_swap_b32_e32 v59, v58
	s_waitcnt lgkmcnt(0)
	v_add_f32_e32 v58, v58, v59
	v_mov_b32_e32 v59, v58
	s_nop 1
	v_permlane32_swap_b32_e32 v59, v58
	s_and_saveexec_b64 s[0:1], vcc
	s_cbranch_execz .LBB0_1259
	s_waitcnt lgkmcnt(0)
	v_add_f32_e32 v58, v58, v59
	v_mov_b32_e32 v59, s11
	ds_write_b32 v59, v58 offset:4448
.LBB0_1259:
	s_or_b64 exec, exec, s[0:1]
	v_lshlrev_b32_e32 v58, 16, v88
	v_lshlrev_b32_e32 v60, 16, v87
	s_waitcnt lgkmcnt(0)
	v_lshlrev_b32_e32 v59, 16, v90
	v_add_f32_e32 v58, v60, v58
	v_lshlrev_b32_e32 v60, 16, v89
	v_fmac_f32_e32 v58, v45, v60
	v_mul_f32_e32 v60, 0xbfb8aa3b, v59
	v_exp_f32_e32 v60, v60
	s_nop 0
	v_add_f32_e32 v60, 1.0, v60
	v_rcp_f32_e32 v60, v60
	s_nop 0
	v_mul_f32_e32 v59, v60, v59
	v_mul_f32_e32 v58, v59, v58
	v_mul_f32_e32 v59, v58, v58
	s_nop 1
	v_mov_b32_dpp v59, v59 quad_perm:[1,0,3,2] row_mask:0xf bank_mask:0xf
	s_waitcnt lgkmcnt(0)
	v_fmac_f32_e32 v59, v58, v58
	s_nop 1
	s_waitcnt lgkmcnt(0)
	v_add_f32_dpp v59, v59, v59 quad_perm:[2,3,0,1] row_mask:0xf bank_mask:0xf
	s_nop 1
	s_waitcnt lgkmcnt(0)
	v_add_f32_dpp v59, v59, v59 row_half_mirror row_mask:0xf bank_mask:0xf
	s_nop 1
	s_waitcnt lgkmcnt(0)
	v_add_f32_dpp v59, v59, v59 row_mirror row_mask:0xf bank_mask:0xf
	v_mov_b32_e32 v60, v59
	s_nop 1
	v_permlane16_swap_b32_e32 v60, v59
	s_waitcnt lgkmcnt(0)
	v_add_f32_e32 v59, v59, v60
	v_mov_b32_e32 v60, v59
	s_nop 1
	v_permlane32_swap_b32_e32 v60, v59
	s_and_saveexec_b64 s[0:1], vcc
	s_cbranch_execz .LBB0_1261
	s_waitcnt lgkmcnt(0)
	v_add_f32_e32 v59, v59, v60
	v_mov_b32_e32 v60, s11
	ds_write_b32 v60, v59 offset:4480
.LBB0_1261:
	s_or_b64 exec, exec, s[0:1]
	v_lshlrev_b32_e32 v59, 16, v84
	v_lshlrev_b32_e32 v61, 16, v83
	s_waitcnt lgkmcnt(0)
	v_lshlrev_b32_e32 v60, 16, v86
	v_add_f32_e32 v59, v61, v59
	v_lshlrev_b32_e32 v61, 16, v85
	v_fmac_f32_e32 v59, v45, v61
	v_mul_f32_e32 v61, 0xbfb8aa3b, v60
	v_exp_f32_e32 v61, v61
	s_nop 0
	v_add_f32_e32 v61, 1.0, v61
	v_rcp_f32_e32 v61, v61
	s_nop 0
	v_mul_f32_e32 v60, v61, v60
	v_mul_f32_e32 v59, v60, v59
	v_mul_f32_e32 v60, v59, v59
	s_nop 1
	v_mov_b32_dpp v60, v60 quad_perm:[1,0,3,2] row_mask:0xf bank_mask:0xf
	s_waitcnt lgkmcnt(0)
	v_fmac_f32_e32 v60, v59, v59
	s_nop 1
	s_waitcnt lgkmcnt(0)
	v_add_f32_dpp v60, v60, v60 quad_perm:[2,3,0,1] row_mask:0xf bank_mask:0xf
	s_nop 1
	s_waitcnt lgkmcnt(0)
	v_add_f32_dpp v60, v60, v60 row_half_mirror row_mask:0xf bank_mask:0xf
	s_nop 1
	s_waitcnt lgkmcnt(0)
	v_add_f32_dpp v60, v60, v60 row_mirror row_mask:0xf bank_mask:0xf
	v_mov_b32_e32 v61, v60
	s_nop 1
	v_permlane16_swap_b32_e32 v61, v60
	s_waitcnt lgkmcnt(0)
	v_add_f32_e32 v60, v60, v61
	v_mov_b32_e32 v61, v60
	s_nop 1
	v_permlane32_swap_b32_e32 v61, v60
	s_and_saveexec_b64 s[0:1], vcc
	s_cbranch_execz .LBB0_1263
	s_waitcnt lgkmcnt(0)
	v_add_f32_e32 v60, v60, v61
	v_mov_b32_e32 v61, s11
	ds_write_b32 v61, v60 offset:4512
.LBB0_1263:
	s_or_b64 exec, exec, s[0:1]
	v_lshlrev_b32_e32 v60, 16, v80
	v_lshlrev_b32_e32 v62, 16, v79
	s_waitcnt lgkmcnt(0)
	v_lshlrev_b32_e32 v61, 16, v82
	v_add_f32_e32 v60, v62, v60
	v_lshlrev_b32_e32 v62, 16, v81
	v_fmac_f32_e32 v60, v45, v62
	v_mul_f32_e32 v62, 0xbfb8aa3b, v61
	v_exp_f32_e32 v62, v62
	s_nop 0
	v_add_f32_e32 v62, 1.0, v62
	v_rcp_f32_e32 v62, v62
	s_nop 0
	v_mul_f32_e32 v61, v62, v61
	v_mul_f32_e32 v60, v61, v60
	v_mul_f32_e32 v61, v60, v60
	s_nop 1
	v_mov_b32_dpp v61, v61 quad_perm:[1,0,3,2] row_mask:0xf bank_mask:0xf
	s_waitcnt lgkmcnt(0)
	v_fmac_f32_e32 v61, v60, v60
	s_nop 1
	s_waitcnt lgkmcnt(0)
	v_add_f32_dpp v61, v61, v61 quad_perm:[2,3,0,1] row_mask:0xf bank_mask:0xf
	s_nop 1
	s_waitcnt lgkmcnt(0)
	v_add_f32_dpp v61, v61, v61 row_half_mirror row_mask:0xf bank_mask:0xf
	s_nop 1
	s_waitcnt lgkmcnt(0)
	v_add_f32_dpp v61, v61, v61 row_mirror row_mask:0xf bank_mask:0xf
	v_mov_b32_e32 v62, v61
	s_nop 1
	v_permlane16_swap_b32_e32 v62, v61
	s_waitcnt lgkmcnt(0)
	v_add_f32_e32 v61, v61, v62
	v_mov_b32_e32 v62, v61
	s_nop 1
	v_permlane32_swap_b32_e32 v62, v61
	s_and_saveexec_b64 s[0:1], vcc
	s_cbranch_execz .LBB0_1265
	s_waitcnt lgkmcnt(0)
	v_add_f32_e32 v61, v61, v62
	v_mov_b32_e32 v62, s11
	ds_write_b32 v62, v61 offset:4544
.LBB0_1265:
	s_or_b64 exec, exec, s[0:1]
	v_lshlrev_b32_e32 v61, 16, v77
	v_lshlrev_b32_e32 v34, 16, v34
	s_waitcnt lgkmcnt(0)
	v_lshlrev_b32_e32 v62, 16, v78
	v_add_f32_e32 v34, v34, v61
	v_lshlrev_b32_e32 v61, 16, v76
	v_fmac_f32_e32 v34, v45, v61
	v_mul_f32_e32 v45, 0xbfb8aa3b, v62
	v_exp_f32_e32 v45, v45
	s_nop 0
	v_add_f32_e32 v45, 1.0, v45
	v_rcp_f32_e32 v45, v45
	s_nop 0
	v_mul_f32_e32 v45, v45, v62
	v_mul_f32_e32 v34, v45, v34
	v_mul_f32_e32 v45, v34, v34
	s_nop 1
	v_mov_b32_dpp v2, v45 quad_perm:[1,0,3,2] row_mask:0xf bank_mask:0xf
	s_waitcnt lgkmcnt(0)
	v_fmac_f32_e32 v2, v34, v34
	s_nop 1
	s_waitcnt lgkmcnt(0)
	v_add_f32_dpp v2, v2, v2 quad_perm:[2,3,0,1] row_mask:0xf bank_mask:0xf
	s_nop 1
	s_waitcnt lgkmcnt(0)
	v_add_f32_dpp v2, v2, v2 row_half_mirror row_mask:0xf bank_mask:0xf
	s_nop 1
	s_waitcnt lgkmcnt(0)
	v_add_f32_dpp v2, v2, v2 row_mirror row_mask:0xf bank_mask:0xf
	v_mov_b32_e32 v3, v2
	s_nop 1
	v_permlane16_swap_b32_e32 v3, v2
	s_waitcnt lgkmcnt(0)
	v_add_f32_e32 v2, v2, v3
	v_mov_b32_e32 v3, v2
	s_nop 1
	v_permlane32_swap_b32_e32 v3, v2
	s_and_saveexec_b64 s[0:1], vcc
	s_cbranch_execz .LBB0_1232
	s_waitcnt lgkmcnt(0)
	v_add_f32_e32 v2, v2, v3
	v_mov_b32_e32 v3, s11
	ds_write_b32 v3, v2 offset:4576
	s_branch .LBB0_1232

.LBB0_1418:
	s_ashr_i32 s11, s10, 31
	s_lshl_b64 s[2:3], s[10:11], 11
	v_lshl_add_u64 v[2:3], v[18:19], 0, s[2:3]
	global_load_dwordx2 v[4:5], v[2:3], off
	s_waitcnt lgkmcnt(1)
	global_load_dwordx2 v[8:9], v[2:3], off offset:512
	global_load_dwordx2 v[28:29], v[2:3], off offset:1024
	s_lshr_b32 s2, s11, 20
	global_load_dwordx2 v[2:3], v[2:3], off offset:1536
	s_add_i32 s2, s10, s2
	s_ashr_i32 s2, s2, 12
	s_cmpk_lt_i32 s10, 0x4000
	s_cselect_b32 s2, s2, 4
	s_mul_hi_i32 s3, s2, 0x6000
	s_mulk_i32 s2, 0x6000
	s_add_u32 s2, s1, s2
	s_addc_u32 s3, s8, s3
	s_add_u32 s4, s2, 0x3000
	s_addc_u32 s5, s3, 0
	s_add_u32 s2, s2, 0x4000
	s_addc_u32 s3, s3, 0
	s_lshl_b64 s[6:7], s[10:11], 10
	s_waitcnt vmcnt(1)
	v_lshlrev_b32_e32 v30, 16, v28
	v_and_b32_e32 v31, 0xffff0000, v28
	s_waitcnt vmcnt(0) lgkmcnt(0)
	v_lshlrev_b32_e32 v10, 16, v2
	v_and_b32_e32 v17, 0xffff0000, v2
	v_lshlrev_b32_e32 v12, 16, v3
	v_and_b32_e32 v13, 0xffff0000, v3
	v_lshlrev_b32_e32 v3, 16, v5
	v_lshlrev_b32_e32 v2, 16, v4
	v_and_b32_e32 v5, 0xffff0000, v5
	v_and_b32_e32 v4, 0xffff0000, v4
	v_pk_mul_f32 v[6:7], v[4:5], v[4:5]
	v_mul_f32_e32 v11, v30, v30
	v_pk_fma_f32 v[6:7], v[2:3], v[2:3], v[6:7]
	v_mul_f32_e32 v117, v31, v31
	v_pk_add_f32 v[36:37], v[6:7], v[6:7] op_sel_hi:[0,1]
	v_lshlrev_b32_e32 v7, 16, v9
	v_lshlrev_b32_e32 v6, 16, v8
	v_and_b32_e32 v9, 0xffff0000, v9
	v_and_b32_e32 v8, 0xffff0000, v8
	v_pk_mul_f32 v[32:33], v[8:9], v[8:9]
	v_mov_b32_e32 v116, v10
	v_pk_fma_f32 v[32:33], v[6:7], v[6:7], v[32:33]
	v_pk_add_f32 v[116:117], v[10:11], v[116:117]
	v_pk_add_f32 v[114:115], v[32:33], v[32:33] op_sel_hi:[0,1]
	v_lshlrev_b32_e32 v32, 16, v29
	v_and_b32_e32 v33, 0xffff0000, v29
	v_mul_f32_e32 v28, v32, v32
	v_pk_fma_f32 v[28:29], v[32:33], v[32:33], v[28:29] op_sel_hi:[1,1,0]
	v_mul_f32_e32 v36, v12, v12
	v_mul_f32_e32 v28, v17, v17
	v_mul_f32_e32 v114, v13, v13
	v_mul_f32_e32 v118, v10, v10
	v_mov_b32_e32 v119, v117
	v_pk_add_f32 v[28:29], v[118:119], v[28:29]
	v_pk_add_f32 v[36:37], v[36:37], v[114:115]
	global_load_dwordx4 v[114:117], v[22:23], off
	global_load_dwordx4 v[118:121], v21, s[4:5]
	global_load_dwordx4 v[122:125], v21, s[2:3]
	global_load_dwordx4 v[128:131], v[22:23], off offset:1024
	global_load_dwordx4 v[132:135], v34, s[4:5]
	global_load_dwordx4 v[136:139], v34, s[2:3]
	global_load_dwordx4 v[140:143], v[22:23], off offset:2048
	global_load_dwordx4 v[144:147], v109, s[4:5]
	global_load_dwordx4 v[148:151], v109, s[2:3]
	global_load_dwordx4 v[152:155], v[22:23], off offset:3072
	global_load_dwordx4 v[156:159], v110, s[4:5]
	global_load_dwordx4 v[160:163], v110, s[2:3]
	v_pk_add_f32 v[28:29], v[28:29], v[36:37]
	v_mov_b32_e32 v36, v3
	v_add_f32_e32 v11, v28, v29
	s_nop 1
	v_mov_b32_e32 v3, v4
	v_mov_b32_e32 v37, v5
	v_mov_b32_e32 v126, v7
	v_mov_b32_e32 v127, v9
	s_waitcnt lgkmcnt(0)
	v_add_f32_dpp v11, v11, v11 quad_perm:[1,0,3,2] row_mask:0xf bank_mask:0xf
	s_nop 1
	v_mov_b32_e32 v7, v8
	s_waitcnt lgkmcnt(0)
	v_add_f32_dpp v11, v11, v11 quad_perm:[2,3,0,1] row_mask:0xf bank_mask:0xf
	s_nop 1
	s_waitcnt lgkmcnt(0)
	v_add_f32_dpp v11, v11, v11 row_half_mirror row_mask:0xf bank_mask:0xf
	s_nop 1
	s_waitcnt lgkmcnt(0)
	v_add_f32_dpp v11, v11, v11 row_mirror row_mask:0xf bank_mask:0xf
	v_mov_b32_e32 v27, v11
	s_nop 1
	v_permlane16_swap_b32_e32 v27, v11
	s_waitcnt lgkmcnt(0)
	v_add_f32_e32 v11, v11, v27
	v_mov_b32_e32 v27, v11
	s_nop 1
	v_permlane32_swap_b32_e32 v27, v11
	s_waitcnt lgkmcnt(0)
	v_add_f32_e32 v11, v11, v27
	v_fmamk_f32 v11, v11, 0x3a800000, v165
	v_rsq_f32_e32 v28, v11
	s_nop 0
	v_pk_mul_f32 v[2:3], v[2:3], v[28:29] op_sel_hi:[1,0]
	v_pk_mul_f32 v[36:37], v[36:37], v[28:29] op_sel_hi:[1,0]
	s_waitcnt vmcnt(11)
	v_pk_mul_f32 v[2:3], v[114:115], v[2:3]
	v_pk_mul_f32 v[4:5], v[116:117], v[36:37]
	s_waitcnt vmcnt(9)
	v_pk_add_f32 v[114:115], v[122:123], 1.0 op_sel_hi:[1,0]
	v_pk_add_f32 v[36:37], v[124:125], 1.0 op_sel_hi:[1,0]
	v_pk_fma_f32 v[2:3], v[114:115], v[2:3], v[118:119]
	v_mov_b32_e32 v114, v35
	v_med3_f32 v11, v2, s13, v200
	v_med3_f32 v27, v3, s13, v200
	v_cvt_pk_fp8_f32 v114, v11, v27
	v_pk_fma_f32 v[4:5], v[36:37], v[4:5], v[120:121]
	s_nop 0
	v_med3_f32 v29, v4, s13, v200
	v_med3_f32 v36, v5, s13, v200
	v_cvt_pk_fp8_f32 v114, v29, v36 op_sel:[0,0,1]
	v_lshl_add_u64 v[36:37], v[24:25], 0, s[6:7]
	v_pk_mul_f32 v[126:127], v[126:127], v[28:29] op_sel_hi:[1,0]
	v_pk_mul_f32 v[6:7], v[6:7], v[28:29] op_sel_hi:[1,0]
	global_store_dword v[36:37], v114, off
	s_waitcnt vmcnt(7)
	v_mov_b64_e32 v[114:115], v[128:129]
	v_mov_b64_e32 v[116:117], v[130:131]
	v_mov_b64_e32 v[118:119], v[132:133]
	v_mov_b64_e32 v[120:121], v[134:135]
	v_mov_b64_e32 v[122:123], v[136:137]
	v_mov_b64_e32 v[124:125], v[138:139]
	s_add_i32 s6, s10, 1
	s_ashr_i32 s7, s6, 31
	s_nop 0
	v_pk_mul_f32 v[6:7], v[114:115], v[6:7]
	v_pk_mul_f32 v[8:9], v[116:117], v[126:127]
	s_nop 0
	v_pk_add_f32 v[116:117], v[122:123], 1.0 op_sel_hi:[1,0]
	v_pk_add_f32 v[114:115], v[124:125], 1.0 op_sel_hi:[1,0]
	v_pk_fma_f32 v[6:7], v[116:117], v[6:7], v[118:119]
	v_pk_fma_f32 v[8:9], v[114:115], v[8:9], v[120:121]
	v_med3_f32 v11, v6, s13, v200
	v_med3_f32 v27, v7, s13, v200
	v_mov_b32_e32 v115, v35
	v_cvt_pk_fp8_f32 v115, v11, v27
	v_med3_f32 v29, v8, s13, v200
	v_med3_f32 v114, v9, s13, v200
	v_pk_mul_f32 v[32:33], v[32:33], v[28:29] op_sel_hi:[1,0]
	v_cvt_pk_fp8_f32 v115, v29, v114 op_sel:[0,0,1]
	v_pk_mul_f32 v[30:31], v[30:31], v[28:29] op_sel_hi:[1,0]
	global_store_dword v[36:37], v115, off offset:256
	s_waitcnt vmcnt(5)
	v_mov_b64_e32 v[114:115], v[140:141]
	v_mov_b64_e32 v[116:117], v[142:143]
	v_mov_b64_e32 v[118:119], v[144:145]
	v_mov_b64_e32 v[120:121], v[146:147]
	v_mov_b64_e32 v[122:123], v[148:149]
	v_mov_b64_e32 v[124:125], v[150:151]
	s_nop 0
	v_pk_mul_f32 v[30:31], v[30:31], v[114:115]
	v_pk_mul_f32 v[32:33], v[32:33], v[116:117]
	s_nop 0
	v_pk_add_f32 v[116:117], v[122:123], 1.0 op_sel_hi:[1,0]
	v_pk_add_f32 v[114:115], v[124:125], 1.0 op_sel_hi:[1,0]
	v_pk_fma_f32 v[30:31], v[30:31], v[116:117], v[118:119]
	v_pk_fma_f32 v[32:33], v[32:33], v[114:115], v[120:121]
	v_med3_f32 v11, v30, s13, v200
	v_med3_f32 v27, v31, s13, v200
	v_mov_b32_e32 v115, v35
	v_cvt_pk_fp8_f32 v115, v11, v27
	v_med3_f32 v29, v32, s13, v200
	v_med3_f32 v114, v33, s13, v200
	v_mov_b32_e32 v11, v17
	v_cvt_pk_fp8_f32 v115, v29, v114 op_sel:[0,0,1]
	v_pk_mul_f32 v[10:11], v[10:11], v[28:29] op_sel_hi:[1,0]
	v_pk_mul_f32 v[12:13], v[12:13], v[28:29] op_sel_hi:[1,0]
	global_store_dword v[36:37], v115, off offset:512
	s_waitcnt vmcnt(3)
	v_mov_b64_e32 v[114:115], v[152:153]
	v_mov_b64_e32 v[116:117], v[154:155]
	v_mov_b64_e32 v[118:119], v[156:157]
	v_mov_b64_e32 v[120:121], v[158:159]
	v_mov_b64_e32 v[122:123], v[160:161]
	v_mov_b64_e32 v[124:125], v[162:163]
	s_lshl_b64 s[2:3], s[6:7], 11
	s_nop 0
	v_pk_mul_f32 v[10:11], v[10:11], v[114:115]
	v_pk_mul_f32 v[12:13], v[12:13], v[116:117]
	s_nop 0
	v_pk_add_f32 v[114:115], v[122:123], 1.0 op_sel_hi:[1,0]
	v_pk_add_f32 v[28:29], v[124:125], 1.0 op_sel_hi:[1,0]
	v_pk_fma_f32 v[10:11], v[10:11], v[114:115], v[118:119]
	v_mov_b32_e32 v114, v35
	v_med3_f32 v17, v10, s13, v200
	v_med3_f32 v27, v11, s13, v200
	v_cvt_pk_fp8_f32 v114, v17, v27
	v_pk_fma_f32 v[12:13], v[12:13], v[28:29], v[120:121]
	v_add_u32_e32 v17, s9, v20
	v_med3_f32 v28, v12, s13, v200
	v_med3_f32 v29, v13, s13, v200
	v_cvt_pk_fp8_f32 v114, v28, v29 op_sel:[0,0,1]
	global_store_dword v[36:37], v114, off offset:768
	ds_write_b128 v17, v[2:5]
	ds_write_b128 v17, v[6:9] offset:1024
	ds_write_b128 v17, v[30:33] offset:2048
	ds_write_b128 v17, v[10:13] offset:3072
	v_lshl_add_u64 v[2:3], v[18:19], 0, s[2:3]
	global_load_dwordx2 v[4:5], v[2:3], off
	global_load_dwordx2 v[8:9], v[2:3], off offset:512
	global_load_dwordx2 v[12:13], v[2:3], off offset:1024
	s_lshr_b32 s2, s7, 20
	global_load_dwordx2 v[2:3], v[2:3], off offset:1536
	s_add_i32 s2, s6, s2
	s_ashr_i32 s2, s2, 12
	s_cmpk_lt_i32 s6, 0x4000
	s_cselect_b32 s2, s2, 4
	s_mul_hi_i32 s3, s2, 0x6000
	s_mulk_i32 s2, 0x6000
	s_add_u32 s2, s1, s2
	s_addc_u32 s3, s8, s3
	s_add_u32 s4, s2, 0x3000
	s_addc_u32 s5, s3, 0
	s_add_u32 s2, s2, 0x4000
	s_addc_u32 s3, s3, 0
	s_lshl_b64 s[6:7], s[6:7], 10
	s_waitcnt vmcnt(1)
	v_lshlrev_b32_e32 v10, 16, v12
	v_and_b32_e32 v11, 0xffff0000, v12
	s_waitcnt vmcnt(0)
	v_lshlrev_b32_e32 v28, 16, v2
	v_and_b32_e32 v17, 0xffff0000, v2
	v_lshlrev_b32_e32 v30, 16, v3
	v_and_b32_e32 v31, 0xffff0000, v3
	v_lshlrev_b32_e32 v3, 16, v5
	v_lshlrev_b32_e32 v2, 16, v4
	v_and_b32_e32 v5, 0xffff0000, v5
	v_and_b32_e32 v4, 0xffff0000, v4
	v_pk_mul_f32 v[6:7], v[4:5], v[4:5]
	v_lshlrev_b32_e32 v12, 16, v13
	v_pk_fma_f32 v[6:7], v[2:3], v[2:3], v[6:7]
	v_mul_f32_e32 v29, v10, v10
	v_pk_add_f32 v[32:33], v[6:7], v[6:7] op_sel_hi:[0,1]
	v_lshlrev_b32_e32 v7, 16, v9
	v_lshlrev_b32_e32 v6, 16, v8
	v_and_b32_e32 v9, 0xffff0000, v9
	v_and_b32_e32 v8, 0xffff0000, v8
	v_pk_mul_f32 v[36:37], v[8:9], v[8:9]
	v_mul_f32_e32 v115, v11, v11
	v_pk_fma_f32 v[36:37], v[6:7], v[6:7], v[36:37]
	v_and_b32_e32 v13, 0xffff0000, v13
	v_mul_f32_e32 v32, v12, v12
	v_mov_b32_e32 v114, v28
	v_pk_add_f32 v[36:37], v[36:37], v[36:37] op_sel_hi:[0,1]
	v_pk_fma_f32 v[116:117], v[12:13], v[12:13], v[32:33] op_sel_hi:[1,1,0]
	v_pk_add_f32 v[114:115], v[28:29], v[114:115]
	v_mul_f32_e32 v116, v17, v17
	v_mul_f32_e32 v32, v30, v30
	v_mul_f32_e32 v36, v31, v31
	v_mul_f32_e32 v118, v28, v28
	v_mov_b32_e32 v119, v115
	v_pk_add_f32 v[114:115], v[118:119], v[116:117]
	v_pk_add_f32 v[32:33], v[32:33], v[36:37]
	v_mov_b32_e32 v36, v3
	v_pk_add_f32 v[32:33], v[114:115], v[32:33]
	global_load_dwordx4 v[114:117], v[22:23], off
	global_load_dwordx4 v[118:121], v21, s[4:5]
	global_load_dwordx4 v[122:125], v21, s[2:3]
	global_load_dwordx4 v[128:131], v[22:23], off offset:1024
	global_load_dwordx4 v[132:135], v34, s[4:5]
	global_load_dwordx4 v[136:139], v34, s[2:3]
	global_load_dwordx4 v[140:143], v[22:23], off offset:2048
	global_load_dwordx4 v[144:147], v109, s[4:5]
	global_load_dwordx4 v[148:151], v109, s[2:3]
	global_load_dwordx4 v[152:155], v[22:23], off offset:3072
	global_load_dwordx4 v[156:159], v110, s[4:5]
	global_load_dwordx4 v[160:163], v110, s[2:3]
	v_add_f32_e32 v27, v32, v33
	s_nop 1
	v_mov_b32_e32 v3, v4
	v_mov_b32_e32 v37, v5
	v_mov_b32_e32 v126, v7
	v_mov_b32_e32 v127, v9
	s_waitcnt lgkmcnt(0)
	v_add_f32_dpp v27, v27, v27 quad_perm:[1,0,3,2] row_mask:0xf bank_mask:0xf
	s_nop 1
	v_mov_b32_e32 v7, v8
	s_waitcnt lgkmcnt(0)
	v_add_f32_dpp v27, v27, v27 quad_perm:[2,3,0,1] row_mask:0xf bank_mask:0xf
	s_nop 1
	s_waitcnt lgkmcnt(0)
	v_add_f32_dpp v27, v27, v27 row_half_mirror row_mask:0xf bank_mask:0xf
	s_nop 1
	s_waitcnt lgkmcnt(0)
	v_add_f32_dpp v27, v27, v27 row_mirror row_mask:0xf bank_mask:0xf
	v_mov_b32_e32 v29, v27
	s_nop 1
	v_permlane16_swap_b32_e32 v29, v27
	s_waitcnt lgkmcnt(0)
	v_add_f32_e32 v27, v27, v29
	v_mov_b32_e32 v29, v27
	s_nop 1
	v_permlane32_swap_b32_e32 v29, v27
	s_waitcnt lgkmcnt(0)
	v_add_f32_e32 v27, v27, v29
	v_fmamk_f32 v27, v27, 0x3a800000, v165
	v_rsq_f32_e32 v32, v27
	s_nop 0
	v_pk_mul_f32 v[2:3], v[2:3], v[32:33] op_sel_hi:[1,0]
	v_pk_mul_f32 v[36:37], v[36:37], v[32:33] op_sel_hi:[1,0]
	s_waitcnt vmcnt(11)
	v_pk_mul_f32 v[2:3], v[114:115], v[2:3]
	v_pk_mul_f32 v[4:5], v[116:117], v[36:37]
	s_waitcnt vmcnt(9)
	v_pk_add_f32 v[114:115], v[122:123], 1.0 op_sel_hi:[1,0]
	v_pk_add_f32 v[36:37], v[124:125], 1.0 op_sel_hi:[1,0]
	v_pk_fma_f32 v[2:3], v[114:115], v[2:3], v[118:119]
	v_mov_b32_e32 v114, v35
	v_med3_f32 v27, v2, s13, v200
	v_med3_f32 v29, v3, s13, v200
	v_cvt_pk_fp8_f32 v114, v27, v29
	v_pk_fma_f32 v[4:5], v[36:37], v[4:5], v[120:121]
	s_nop 0
	v_med3_f32 v33, v4, s13, v200
	v_med3_f32 v36, v5, s13, v200
	v_cvt_pk_fp8_f32 v114, v33, v36 op_sel:[0,0,1]
	v_lshl_add_u64 v[36:37], v[24:25], 0, s[6:7]
	v_pk_mul_f32 v[126:127], v[126:127], v[32:33] op_sel_hi:[1,0]
	v_pk_mul_f32 v[6:7], v[6:7], v[32:33] op_sel_hi:[1,0]
	global_store_dword v[36:37], v114, off
	s_waitcnt vmcnt(7)
	v_mov_b64_e32 v[114:115], v[128:129]
	v_mov_b64_e32 v[116:117], v[130:131]
	v_mov_b64_e32 v[118:119], v[132:133]
	v_mov_b64_e32 v[120:121], v[134:135]
	v_mov_b64_e32 v[122:123], v[136:137]
	v_mov_b64_e32 v[124:125], v[138:139]
	s_nop 0
	v_pk_mul_f32 v[6:7], v[114:115], v[6:7]
	v_pk_mul_f32 v[8:9], v[116:117], v[126:127]
	s_nop 0
	v_pk_add_f32 v[116:117], v[122:123], 1.0 op_sel_hi:[1,0]
	v_pk_add_f32 v[114:115], v[124:125], 1.0 op_sel_hi:[1,0]
	v_pk_fma_f32 v[6:7], v[116:117], v[6:7], v[118:119]
	v_pk_fma_f32 v[8:9], v[114:115], v[8:9], v[120:121]
	v_med3_f32 v27, v6, s13, v200
	v_med3_f32 v29, v7, s13, v200
	v_mov_b32_e32 v115, v35
	v_cvt_pk_fp8_f32 v115, v27, v29
	v_med3_f32 v33, v8, s13, v200
	v_med3_f32 v114, v9, s13, v200
	v_pk_mul_f32 v[12:13], v[12:13], v[32:33] op_sel_hi:[1,0]
	v_cvt_pk_fp8_f32 v115, v33, v114 op_sel:[0,0,1]
	v_pk_mul_f32 v[10:11], v[10:11], v[32:33] op_sel_hi:[1,0]
	global_store_dword v[36:37], v115, off offset:256
	s_waitcnt vmcnt(5)
	v_mov_b64_e32 v[114:115], v[140:141]
	v_mov_b64_e32 v[116:117], v[142:143]
	v_mov_b64_e32 v[118:119], v[144:145]
	v_mov_b64_e32 v[120:121], v[146:147]
	v_mov_b64_e32 v[122:123], v[148:149]
	v_mov_b64_e32 v[124:125], v[150:151]
	s_nop 0
	v_pk_mul_f32 v[10:11], v[10:11], v[114:115]
	v_pk_mul_f32 v[12:13], v[12:13], v[116:117]
	s_nop 0
	v_pk_add_f32 v[116:117], v[122:123], 1.0 op_sel_hi:[1,0]
	v_pk_add_f32 v[114:115], v[124:125], 1.0 op_sel_hi:[1,0]
	v_pk_fma_f32 v[10:11], v[10:11], v[116:117], v[118:119]
	v_pk_fma_f32 v[12:13], v[12:13], v[114:115], v[120:121]
	v_med3_f32 v27, v10, s13, v200
	v_med3_f32 v29, v11, s13, v200
	v_mov_b32_e32 v115, v35
	v_cvt_pk_fp8_f32 v115, v27, v29
	v_med3_f32 v33, v12, s13, v200
	v_med3_f32 v114, v13, s13, v200
	v_mov_b32_e32 v29, v17
	v_cvt_pk_fp8_f32 v115, v33, v114 op_sel:[0,0,1]
	v_pk_mul_f32 v[28:29], v[28:29], v[32:33] op_sel_hi:[1,0]
	v_pk_mul_f32 v[30:31], v[30:31], v[32:33] op_sel_hi:[1,0]
	global_store_dword v[36:37], v115, off offset:512
	s_waitcnt vmcnt(3)
	v_mov_b64_e32 v[114:115], v[152:153]
	v_mov_b64_e32 v[116:117], v[154:155]
	v_mov_b64_e32 v[118:119], v[156:157]
	v_mov_b64_e32 v[120:121], v[158:159]
	v_mov_b64_e32 v[122:123], v[160:161]
	v_mov_b64_e32 v[124:125], v[162:163]
	s_nop 0
	v_pk_mul_f32 v[28:29], v[28:29], v[114:115]
	v_pk_mul_f32 v[30:31], v[30:31], v[116:117]
	s_nop 0
	v_pk_add_f32 v[114:115], v[122:123], 1.0 op_sel_hi:[1,0]
	v_pk_add_f32 v[32:33], v[124:125], 1.0 op_sel_hi:[1,0]
	v_pk_fma_f32 v[28:29], v[28:29], v[114:115], v[118:119]
	v_mov_b32_e32 v114, v35
	v_med3_f32 v17, v28, s13, v200
	v_med3_f32 v27, v29, s13, v200
	v_cvt_pk_fp8_f32 v114, v17, v27
	v_pk_fma_f32 v[30:31], v[30:31], v[32:33], v[120:121]
	v_add_u32_e32 v17, s14, v20
	v_med3_f32 v32, v30, s13, v200
	v_med3_f32 v33, v31, s13, v200
	v_cvt_pk_fp8_f32 v114, v32, v33 op_sel:[0,0,1]
	global_store_dword v[36:37], v114, off offset:768
	ds_write_b128 v17, v[2:5]
	ds_write_b128 v17, v[6:9] offset:1024
	ds_write_b128 v17, v[10:13] offset:2048
	ds_write_b128 v17, v[28:31] offset:3072
	s_waitcnt lgkmcnt(0)
	s_barrier
	ds_read2_b32 v[10:11], v111 offset1:4
	ds_read2_b32 v[12:13], v111 offset0:8 offset1:12
	s_waitcnt lgkmcnt(1)
	v_mfma_f32_16x16x4_f32 v[2:5], v10, v39, 0
	v_mfma_f32_16x16x4_f32 v[6:9], v10, v46, 0
	v_mfma_f32_16x16x4_f32 v[2:5], v11, v40, v[2:5]
	v_mfma_f32_16x16x4_f32 v[6:9], v11, v45, v[6:9]
	ds_read2_b32 v[10:11], v111 offset0:16 offset1:20
	s_waitcnt lgkmcnt(1)
	v_mfma_f32_16x16x4_f32 v[2:5], v12, v41, v[2:5]
	v_mfma_f32_16x16x4_f32 v[6:9], v12, v44, v[6:9]
	v_mfma_f32_16x16x4_f32 v[2:5], v13, v42, v[2:5]
	v_mfma_f32_16x16x4_f32 v[6:9], v13, v43, v[6:9]
	s_waitcnt lgkmcnt(0)
	v_mfma_f32_16x16x4_f32 v[2:5], v10, v47, v[2:5]
	v_mfma_f32_16x16x4_f32 v[6:9], v10, v54, v[6:9]
	v_mfma_f32_16x16x4_f32 v[2:5], v11, v48, v[2:5]
	v_mfma_f32_16x16x4_f32 v[6:9], v11, v53, v[6:9]
	ds_read2_b32 v[10:11], v111 offset0:24 offset1:28
	s_waitcnt lgkmcnt(0)
	v_mfma_f32_16x16x4_f32 v[2:5], v10, v49, v[2:5]
	v_mfma_f32_16x16x4_f32 v[6:9], v10, v52, v[6:9]
	v_mfma_f32_16x16x4_f32 v[2:5], v11, v50, v[2:5]
	v_mfma_f32_16x16x4_f32 v[6:9], v11, v51, v[6:9]
	ds_read2_b32 v[10:11], v111 offset0:32 offset1:36
	s_waitcnt lgkmcnt(0)
	v_mfma_f32_16x16x4_f32 v[2:5], v10, v55, v[2:5]
	v_mfma_f32_16x16x4_f32 v[6:9], v10, v62, v[6:9]
	v_mfma_f32_16x16x4_f32 v[2:5], v11, v56, v[2:5]
	v_mfma_f32_16x16x4_f32 v[6:9], v11, v61, v[6:9]
	ds_read2_b32 v[10:11], v111 offset0:40 offset1:44
	s_waitcnt lgkmcnt(0)
	v_mfma_f32_16x16x4_f32 v[2:5], v10, v57, v[2:5]
	v_mfma_f32_16x16x4_f32 v[6:9], v10, v60, v[6:9]
	v_mfma_f32_16x16x4_f32 v[2:5], v11, v58, v[2:5]
	v_mfma_f32_16x16x4_f32 v[6:9], v11, v59, v[6:9]
	ds_read2_b32 v[10:11], v111 offset0:48 offset1:52
	s_waitcnt lgkmcnt(0)
	v_mfma_f32_16x16x4_f32 v[2:5], v10, v63, v[2:5]
	v_mfma_f32_16x16x4_f32 v[6:9], v10, v70, v[6:9]
	v_mfma_f32_16x16x4_f32 v[2:5], v11, v64, v[2:5]
	v_mfma_f32_16x16x4_f32 v[6:9], v11, v69, v[6:9]
	ds_read2_b32 v[10:11], v111 offset0:56 offset1:60
	s_waitcnt lgkmcnt(0)
	v_mfma_f32_16x16x4_f32 v[2:5], v10, v65, v[2:5]
	v_mfma_f32_16x16x4_f32 v[6:9], v10, v68, v[6:9]
	v_mfma_f32_16x16x4_f32 v[2:5], v11, v66, v[2:5]
	v_mfma_f32_16x16x4_f32 v[6:9], v11, v67, v[6:9]
	ds_read2_b32 v[10:11], v111 offset0:64 offset1:68
	s_waitcnt lgkmcnt(0)
	v_mfma_f32_16x16x4_f32 v[2:5], v10, v71, v[2:5]
	v_mfma_f32_16x16x4_f32 v[6:9], v10, v78, v[6:9]
	v_mfma_f32_16x16x4_f32 v[2:5], v11, v72, v[2:5]
	v_mfma_f32_16x16x4_f32 v[6:9], v11, v77, v[6:9]
	ds_read2_b32 v[10:11], v111 offset0:72 offset1:76
	s_waitcnt lgkmcnt(0)
	v_mfma_f32_16x16x4_f32 v[2:5], v10, v73, v[2:5]
	v_mfma_f32_16x16x4_f32 v[6:9], v10, v76, v[6:9]
	v_mfma_f32_16x16x4_f32 v[2:5], v11, v74, v[2:5]
	v_mfma_f32_16x16x4_f32 v[6:9], v11, v75, v[6:9]
	ds_read2_b32 v[10:11], v111 offset0:80 offset1:84
	s_waitcnt lgkmcnt(0)
	v_mfma_f32_16x16x4_f32 v[2:5], v10, v79, v[2:5]
	v_mfma_f32_16x16x4_f32 v[6:9], v10, v86, v[6:9]
	v_mfma_f32_16x16x4_f32 v[2:5], v11, v80, v[2:5]
	v_mfma_f32_16x16x4_f32 v[6:9], v11, v85, v[6:9]
	ds_read2_b32 v[10:11], v111 offset0:88 offset1:92
	s_waitcnt lgkmcnt(0)
	v_mfma_f32_16x16x4_f32 v[2:5], v10, v81, v[2:5]
	v_mfma_f32_16x16x4_f32 v[6:9], v10, v84, v[6:9]
	v_mfma_f32_16x16x4_f32 v[2:5], v11, v82, v[2:5]
	v_mfma_f32_16x16x4_f32 v[6:9], v11, v83, v[6:9]
	ds_read2_b32 v[10:11], v111 offset0:96 offset1:100
	s_waitcnt lgkmcnt(0)
	v_mfma_f32_16x16x4_f32 v[2:5], v10, v87, v[2:5]
	v_mfma_f32_16x16x4_f32 v[6:9], v10, v94, v[6:9]
	v_mfma_f32_16x16x4_f32 v[2:5], v11, v88, v[2:5]
	v_mfma_f32_16x16x4_f32 v[6:9], v11, v93, v[6:9]
	ds_read2_b32 v[10:11], v111 offset0:104 offset1:108
	s_waitcnt lgkmcnt(0)
	v_mfma_f32_16x16x4_f32 v[2:5], v10, v89, v[2:5]
	v_mfma_f32_16x16x4_f32 v[6:9], v10, v92, v[6:9]
	v_mfma_f32_16x16x4_f32 v[2:5], v11, v90, v[2:5]
	v_mfma_f32_16x16x4_f32 v[6:9], v11, v91, v[6:9]
	ds_read2_b32 v[10:11], v111 offset0:112 offset1:116
	s_waitcnt lgkmcnt(0)
	v_mfma_f32_16x16x4_f32 v[2:5], v10, v95, v[2:5]
	v_mfma_f32_16x16x4_f32 v[6:9], v10, v102, v[6:9]
	v_mfma_f32_16x16x4_f32 v[2:5], v11, v96, v[2:5]
	v_mfma_f32_16x16x4_f32 v[6:9], v11, v101, v[6:9]
	ds_read2_b32 v[10:11], v111 offset0:120 offset1:124
	s_waitcnt lgkmcnt(0)
	v_mfma_f32_16x16x4_f32 v[2:5], v10, v97, v[2:5]
	v_mfma_f32_16x16x4_f32 v[6:9], v10, v100, v[6:9]
	v_mfma_f32_16x16x4_f32 v[2:5], v11, v98, v[2:5]
	v_mfma_f32_16x16x4_f32 v[6:9], v11, v99, v[6:9]
	s_nop 9
	ds_write2_b32 v112, v2, v6 offset1:16
	ds_write2_b32 v112, v3, v7 offset0:33 offset1:49
	ds_write2_b32 v112, v4, v8 offset0:66 offset1:82
	ds_write2_b32 v112, v5, v9 offset0:99 offset1:115
	s_waitcnt lgkmcnt(0)
	s_barrier
	ds_read_b32 v2, v113
	ds_read_b32 v3, v113 offset:2112
	s_waitcnt lgkmcnt(1)
	v_add_f32_e32 v2, v38, v2
	s_waitcnt lgkmcnt(0)
	v_add_f32_e32 v2, v2, v3
	ds_read_b32 v3, v113 offset:4224
	s_waitcnt lgkmcnt(0)
	v_add_f32_e32 v2, v2, v3
	ds_read_b32 v3, v113 offset:6336
	s_waitcnt lgkmcnt(0)
	v_add_f32_e32 v2, v2, v3
	ds_read_b32 v3, v113 offset:8448
	s_waitcnt lgkmcnt(0)
	v_add_f32_e32 v2, v2, v3
	ds_read_b32 v3, v113 offset:10560
	s_waitcnt lgkmcnt(0)
	v_add_f32_e32 v2, v2, v3
	ds_read_b32 v3, v113 offset:12672
	s_waitcnt lgkmcnt(0)
	v_add_f32_e32 v2, v2, v3
	ds_read_b32 v3, v113 offset:14784
	s_waitcnt lgkmcnt(0)
	v_add_f32_e32 v2, v2, v3
	v_not_b32_e32 v3, v2
	v_or_b32_e32 v4, 0x80000000, v2
	v_cmp_gt_i32_e64 s[2:3], 0, v2
	s_nop 1
	v_mov_b32_dpp v2, v16 quad_perm:[1,0,3,2] row_mask:0xf bank_mask:0xf
	s_nop 0
	v_cndmask_b32_e64 v17, v4, v3, s[2:3]
	s_nop 1
	v_mov_b32_dpp v3, v17 quad_perm:[1,0,3,2] row_mask:0xf bank_mask:0xf
	s_waitcnt lgkmcnt(0)
	v_cmp_gt_u64_e64 s[2:3], v[2:3], v[16:17]
	s_nop 1
	v_cndmask_b32_e64 v3, v17, v3, s[2:3]
	v_cndmask_b32_e64 v2, v16, v2, s[2:3]
	s_nop 1
	v_mov_b32_dpp v4, v2 quad_perm:[2,3,0,1] row_mask:0xf bank_mask:0xf
	s_nop 1
	v_mov_b32_dpp v5, v3 quad_perm:[2,3,0,1] row_mask:0xf bank_mask:0xf
	s_waitcnt lgkmcnt(0)
	v_cmp_gt_u64_e64 s[2:3], v[4:5], v[2:3]
	s_nop 1
	v_cndmask_b32_e64 v3, v3, v5, s[2:3]
	v_cndmask_b32_e64 v2, v2, v4, s[2:3]
	s_nop 1
	v_mov_b32_dpp v4, v2 row_half_mirror row_mask:0xf bank_mask:0xf
	s_nop 1
	v_mov_b32_dpp v5, v3 row_half_mirror row_mask:0xf bank_mask:0xf
	s_waitcnt lgkmcnt(0)
	v_cmp_gt_u64_e64 s[2:3], v[4:5], v[2:3]
	s_nop 1
	v_cndmask_b32_e64 v3, v3, v5, s[2:3]
	v_cndmask_b32_e64 v2, v2, v4, s[2:3]
	s_nop 1
	v_mov_b32_dpp v4, v2 row_mirror row_mask:0xf bank_mask:0xf
	s_nop 1
	v_mov_b32_dpp v5, v3 row_mirror row_mask:0xf bank_mask:0xf
	s_waitcnt lgkmcnt(0)
	v_cmp_gt_u64_e64 s[2:3], v[4:5], v[2:3]
	s_nop 1
	v_cndmask_b32_e64 v3, v3, v5, s[2:3]
	v_cndmask_b32_e64 v2, v2, v4, s[2:3]
	ds_bpermute_b32 v4, v107, v2
	ds_bpermute_b32 v5, v107, v3
	s_waitcnt lgkmcnt(0)
	v_cmp_gt_u64_e64 s[2:3], v[4:5], v[2:3]
	s_nop 1
	v_cndmask_b32_e64 v2, v2, v4, s[2:3]
	v_sub_u32_e32 v30, 31, v2
	v_cmp_ne_u32_e64 s[4:5], v30, v15
	s_nop 1
	v_cndmask_b32_e64 v11, 0, v17, s[4:5]
	v_cndmask_b32_e64 v10, 0, v16, s[4:5]
	s_nop 1
	v_mov_b32_dpp v6, v10 quad_perm:[1,0,3,2] row_mask:0xf bank_mask:0xf
	s_nop 1
	v_mov_b32_dpp v7, v11 quad_perm:[1,0,3,2] row_mask:0xf bank_mask:0xf
	s_waitcnt lgkmcnt(0)
	v_cmp_gt_u64_e64 s[4:5], v[6:7], v[10:11]
	s_nop 1
	v_cndmask_b32_e64 v7, v11, v7, s[4:5]
	v_cndmask_b32_e64 v6, v10, v6, s[4:5]
	s_nop 1
	v_mov_b32_dpp v8, v6 quad_perm:[2,3,0,1] row_mask:0xf bank_mask:0xf
	s_nop 1
	v_mov_b32_dpp v9, v7 quad_perm:[2,3,0,1] row_mask:0xf bank_mask:0xf
	s_waitcnt lgkmcnt(0)
	v_cmp_gt_u64_e64 s[4:5], v[8:9], v[6:7]
	s_nop 1
	v_cndmask_b32_e64 v7, v7, v9, s[4:5]
	v_cndmask_b32_e64 v6, v6, v8, s[4:5]
	s_nop 1
	v_mov_b32_dpp v8, v6 row_half_mirror row_mask:0xf bank_mask:0xf
	s_nop 1
	v_mov_b32_dpp v9, v7 row_half_mirror row_mask:0xf bank_mask:0xf
	s_waitcnt lgkmcnt(0)
	v_cmp_gt_u64_e64 s[4:5], v[8:9], v[6:7]
	s_nop 1
	v_cndmask_b32_e64 v7, v7, v9, s[4:5]
	v_cndmask_b32_e64 v6, v6, v8, s[4:5]
	s_nop 1
	v_mov_b32_dpp v8, v6 row_mirror row_mask:0xf bank_mask:0xf
	s_nop 1
	v_mov_b32_dpp v9, v7 row_mirror row_mask:0xf bank_mask:0xf
	s_waitcnt lgkmcnt(0)
	v_cmp_gt_u64_e64 s[4:5], v[8:9], v[6:7]
	s_nop 1
	v_cndmask_b32_e64 v7, v7, v9, s[4:5]
	v_cndmask_b32_e64 v6, v6, v8, s[4:5]
	ds_bpermute_b32 v8, v107, v6
	ds_bpermute_b32 v9, v107, v7
	s_waitcnt lgkmcnt(0)
	v_cmp_gt_u64_e64 s[4:5], v[8:9], v[6:7]
	s_nop 1
	v_cndmask_b32_e64 v4, v6, v8, s[4:5]
	v_sub_u32_e32 v17, 31, v4
	v_cmp_ne_u32_e64 s[6:7], v17, v15
	s_nop 1
	v_cndmask_b32_e64 v29, 0, v11, s[6:7]
	v_cndmask_b32_e64 v28, 0, v10, s[6:7]
	s_nop 1
	v_mov_b32_dpp v10, v28 quad_perm:[1,0,3,2] row_mask:0xf bank_mask:0xf
	s_nop 1
	v_mov_b32_dpp v11, v29 quad_perm:[1,0,3,2] row_mask:0xf bank_mask:0xf
	s_waitcnt lgkmcnt(0)
	v_cmp_gt_u64_e64 s[6:7], v[10:11], v[28:29]
	s_nop 1
	v_cndmask_b32_e64 v11, v29, v11, s[6:7]
	v_cndmask_b32_e64 v10, v28, v10, s[6:7]
	s_nop 1
	v_mov_b32_dpp v12, v10 quad_perm:[2,3,0,1] row_mask:0xf bank_mask:0xf
	s_nop 1
	v_mov_b32_dpp v13, v11 quad_perm:[2,3,0,1] row_mask:0xf bank_mask:0xf
	s_waitcnt lgkmcnt(0)
	v_cmp_gt_u64_e64 s[6:7], v[12:13], v[10:11]
	s_nop 1
	v_cndmask_b32_e64 v11, v11, v13, s[6:7]
	v_cndmask_b32_e64 v10, v10, v12, s[6:7]
	s_nop 1
	v_mov_b32_dpp v12, v10 row_half_mirror row_mask:0xf bank_mask:0xf
	s_nop 1
	v_mov_b32_dpp v13, v11 row_half_mirror row_mask:0xf bank_mask:0xf
	s_waitcnt lgkmcnt(0)
	v_cmp_gt_u64_e64 s[6:7], v[12:13], v[10:11]
	s_nop 1
	v_cndmask_b32_e64 v11, v11, v13, s[6:7]
	v_cndmask_b32_e64 v10, v10, v12, s[6:7]
	s_nop 1
	v_mov_b32_dpp v12, v10 row_mirror row_mask:0xf bank_mask:0xf
	s_nop 1
	v_mov_b32_dpp v13, v11 row_mirror row_mask:0xf bank_mask:0xf
	s_waitcnt lgkmcnt(0)
	v_cmp_gt_u64_e64 s[6:7], v[12:13], v[10:11]
	s_nop 1
	v_cndmask_b32_e64 v11, v11, v13, s[6:7]
	v_cndmask_b32_e64 v10, v10, v12, s[6:7]
	ds_bpermute_b32 v12, v107, v10
	ds_bpermute_b32 v13, v107, v11
	s_waitcnt lgkmcnt(0)
	v_cmp_gt_u64_e64 s[40:41], v[12:13], v[10:11]
	s_nop 1
	v_cndmask_b32_e64 v6, v10, v12, s[40:41]
	v_sub_u32_e32 v12, 31, v6
	v_cmp_ne_u32_e64 s[6:7], v12, v15
	s_nop 1
	v_cndmask_b32_e64 v29, 0, v29, s[6:7]
	v_cndmask_b32_e64 v28, 0, v28, s[6:7]
	s_nop 1
	v_mov_b32_dpp v32, v28 quad_perm:[1,0,3,2] row_mask:0xf bank_mask:0xf
	s_nop 1
	v_mov_b32_dpp v33, v29 quad_perm:[1,0,3,2] row_mask:0xf bank_mask:0xf
	s_waitcnt lgkmcnt(0)
	v_cmp_gt_u64_e64 s[6:7], v[32:33], v[28:29]
	s_nop 1
	v_cndmask_b32_e64 v29, v29, v33, s[6:7]
	v_cndmask_b32_e64 v28, v28, v32, s[6:7]
	s_nop 1
	v_mov_b32_dpp v32, v28 quad_perm:[2,3,0,1] row_mask:0xf bank_mask:0xf
	s_nop 1
	v_mov_b32_dpp v33, v29 quad_perm:[2,3,0,1] row_mask:0xf bank_mask:0xf
	s_waitcnt lgkmcnt(0)
	v_cmp_gt_u64_e64 s[6:7], v[32:33], v[28:29]
	s_nop 1
	v_cndmask_b32_e64 v29, v29, v33, s[6:7]
	v_cndmask_b32_e64 v28, v28, v32, s[6:7]
	s_nop 1
	v_mov_b32_dpp v32, v28 row_half_mirror row_mask:0xf bank_mask:0xf
	s_nop 1
	v_mov_b32_dpp v33, v29 row_half_mirror row_mask:0xf bank_mask:0xf
	s_waitcnt lgkmcnt(0)
	v_cmp_gt_u64_e64 s[6:7], v[32:33], v[28:29]
	s_nop 1
	v_cndmask_b32_e64 v29, v29, v33, s[6:7]
	v_cndmask_b32_e64 v28, v28, v32, s[6:7]
	s_nop 1
	v_mov_b32_dpp v32, v28 row_mirror row_mask:0xf bank_mask:0xf
	s_nop 1
	v_mov_b32_dpp v33, v29 row_mirror row_mask:0xf bank_mask:0xf
	s_waitcnt lgkmcnt(0)
	v_cmp_gt_u64_e64 s[6:7], v[32:33], v[28:29]
	s_nop 1
	v_cndmask_b32_e64 v29, v29, v33, s[6:7]
	v_cndmask_b32_e64 v28, v28, v32, s[6:7]
	ds_bpermute_b32 v8, v107, v28
	ds_bpermute_b32 v10, v107, v29
	s_and_saveexec_b64 s[6:7], s[38:39]
	s_cbranch_execz .LBB0_1417
	v_cndmask_b32_e64 v3, v3, v5, s[2:3]
	v_cndmask_b32_e64 v5, v7, v9, s[4:5]
	s_waitcnt lgkmcnt(0)
	v_mov_b32_e32 v9, v10
	v_cmp_gt_u64_e64 s[2:3], v[8:9], v[28:29]
	v_cndmask_b32_e64 v7, v11, v13, s[40:41]
	v_ashrrev_i32_e32 v27, 31, v26
	v_cndmask_b32_e64 v9, v29, v10, s[2:3]
	v_cndmask_b32_e64 v8, v28, v8, s[2:3]
	v_not_b32_e32 v10, v9
	v_cmp_gt_i64_e64 s[2:3], 0, v[8:9]
	v_sub_u32_e32 v31, 31, v8
	s_nop 0
	v_cndmask_b32_e64 v9, v10, |v9|, s[2:3]
	v_not_b32_e32 v10, v7
	v_cmp_gt_i64_e64 s[2:3], 0, v[6:7]
	s_nop 1
	v_cndmask_b32_e64 v6, v10, |v7|, s[2:3]
	v_not_b32_e32 v7, v5
	v_cmp_gt_i64_e64 s[2:3], 0, v[4:5]
	s_nop 1
	v_cndmask_b32_e64 v4, v7, |v5|, s[2:3]
	v_not_b32_e32 v5, v3
	v_cmp_gt_i64_e64 s[2:3], 0, v[2:3]
	s_nop 1
	v_cndmask_b32_e64 v2, v5, |v3|, s[2:3]
	v_sub_f32_e32 v3, v4, v2
	v_mul_f32_e32 v3, 0x3fb8aa3b, v3
	v_exp_f32_e32 v13, v3
	v_sub_f32_e32 v3, v6, v2
	v_mul_f32_e32 v3, 0x3fb8aa3b, v3
	v_sub_f32_e32 v2, v9, v2
	v_exp_f32_e32 v28, v3
	v_mul_f32_e32 v2, 0x3fb8aa3b, v2
	v_exp_f32_e32 v29, v2
	v_add_f32_e32 v2, 1.0, v13
	v_add_f32_e32 v2, v2, v28
	s_add_i32 s2, 0, 0x20840
	v_add_f32_e32 v2, v2, v29
	v_rcp_f32_e32 v32, v2
	v_add_u32_e32 v2, -3, v26
	v_ashrrev_i32_e32 v3, 31, v2
	v_lshlrev_b64 v[2:3], 2, v[2:3]
	v_lshl_add_u64 v[4:5], s[28:29], 0, v[2:3]
	global_store_dword v[4:5], v30, off
	v_add_u32_e32 v4, -2, v26
	v_ashrrev_i32_e32 v5, 31, v4
	v_lshlrev_b64 v[4:5], 2, v[4:5]
	v_lshl_add_u64 v[6:7], s[28:29], 0, v[4:5]
	global_store_dword v[6:7], v17, off
	v_add_u32_e32 v6, -1, v26
	v_ashrrev_i32_e32 v7, 31, v6
	v_lshlrev_b64 v[6:7], 2, v[6:7]
	v_lshl_add_u64 v[8:9], s[28:29], 0, v[6:7]
	global_store_dword v[8:9], v12, off
	v_lshlrev_b64 v[8:9], 2, v[26:27]
	v_lshl_add_u64 v[10:11], s[28:29], 0, v[8:9]
	v_lshl_add_u64 v[2:3], s[42:43], 0, v[2:3]
	global_store_dword v[10:11], v31, off
	global_store_dword v[2:3], v32, off
	v_mul_f32_e32 v10, v13, v32
	v_lshl_add_u64 v[2:3], s[42:43], 0, v[4:5]
	global_store_dword v[2:3], v10, off
	v_mul_f32_e32 v4, v28, v32
	v_lshl_add_u64 v[2:3], s[42:43], 0, v[6:7]
	global_store_dword v[2:3], v4, off
	v_mul_f32_e32 v4, v29, v32
	v_lshl_add_u64 v[2:3], s[42:43], 0, v[8:9]
	global_store_dword v[2:3], v4, off
	v_lshl_add_u32 v2, v30, 2, s2
	ds_add_u32 v2, v250
	v_lshl_add_u32 v2, v17, 2, s2
	ds_add_u32 v2, v250
	v_lshl_add_u32 v2, v12, 2, s2
	ds_add_u32 v2, v250
	v_lshl_add_u32 v2, v31, 2, s2
	ds_add_u32 v2, v250
	s_branch .LBB0_1417

.LBB0_1731:
	s_add_u32 s0, s84, s6
	s_addc_u32 s1, s85, s7
	s_add_u32 s8, s0, 0x2bc10000
	s_addc_u32 s9, s1, 0
	v_mov_b32_e32 v11, 0x2bc10000
	global_load_dwordx4 v[2:5], v35, s[8:9] offset:16
	global_load_dwordx4 v[36:39], v11, s[0:1]
	v_lshl_add_u64 v[30:31], s[84:85], 0, v[28:29]
	s_mov_b32 s0, 0x178000
	v_add_co_u32_e32 v32, vcc, s0, v30
	v_lshlrev_b32_e32 v11, 1, v10
	s_nop 0
	v_addc_co_u32_e32 v33, vcc, 0, v31, vcc
	global_load_dwordx2 v[40:41], v[32:33], off
	v_lshlrev_b32_e32 v34, 2, v6
	v_lshlrev_b32_e32 v13, 2, v12
	v_lshlrev_b32_e32 v15, 2, v10
	s_waitcnt vmcnt(0)
	v_lshlrev_b32_e32 v76, 16, v40
	v_and_b32_e32 v77, 0xffff0000, v40
	v_lshlrev_b32_e32 v74, 16, v41
	v_and_b32_e32 v75, 0xffff0000, v41
	v_ashrrev_i32_e32 v41, 31, v36
	v_mov_b32_e32 v40, v36
	v_lshlrev_b64 v[40:41], 11, v[40:41]
	v_lshl_add_u64 v[42:43], v[8:9], 0, v[40:41]
	global_load_dwordx2 v[114:115], v[42:43], off
	v_ashrrev_i32_e32 v43, 31, v37
	v_mov_b32_e32 v42, v37
	v_lshlrev_b64 v[36:37], 11, v[42:43]
	v_lshl_add_u64 v[42:43], v[8:9], 0, v[36:37]
	global_load_dwordx2 v[116:117], v[42:43], off
	v_ashrrev_i32_e32 v43, 31, v38
	v_mov_b32_e32 v42, v38
	v_lshlrev_b64 v[42:43], 11, v[42:43]
	v_lshl_add_u64 v[44:45], v[8:9], 0, v[42:43]
	global_load_dwordx2 v[118:119], v[44:45], off
	v_ashrrev_i32_e32 v45, 31, v39
	v_mov_b32_e32 v44, v39
	v_lshl_add_u64 v[36:37], s[4:5], 0, v[36:37]
	v_lshlrev_b64 v[38:39], 11, v[44:45]
	v_readfirstlane_b32 s10, v36
	v_readfirstlane_b32 s11, v37
	v_lshl_add_u64 v[36:37], s[4:5], 0, v[42:43]
	v_lshl_add_u64 v[40:41], s[4:5], 0, v[40:41]
	v_readfirstlane_b32 s14, v36
	v_readfirstlane_b32 s15, v37
	v_lshl_add_u64 v[36:37], s[4:5], 0, v[38:39]
	v_lshl_add_u64 v[44:45], v[8:9], 0, v[38:39]
	v_readfirstlane_b32 s8, v40
	v_readfirstlane_b32 s9, v41
	v_readfirstlane_b32 s16, v36
	v_readfirstlane_b32 s17, v37
	global_load_dwordx2 v[120:121], v[44:45], off
	s_nop 0
	global_load_dwordx2 v[44:45], v[32:33], off offset:512
	global_load_dwordx2 v[106:107], v11, s[8:9] nt
	global_load_dwordx2 v[108:109], v11, s[10:11] nt
	global_load_dwordx2 v[110:111], v11, s[14:15] nt
	global_load_dwordx2 v[112:113], v11, s[16:17] nt
	global_load_dwordx2 v[36:37], v[32:33], off offset:1024
	s_waitcnt vmcnt(0)
	v_lshlrev_b32_e32 v122, 16, v120
	v_lshlrev_b32_e32 v80, 16, v44
	v_and_b32_e32 v81, 0xffff0000, v44
	v_lshlrev_b32_e32 v78, 16, v45
	v_and_b32_e32 v79, 0xffff0000, v45
	v_lshlrev_b32_e32 v84, 16, v36
	v_and_b32_e32 v85, 0xffff0000, v36
	v_lshlrev_b32_e32 v82, 16, v37
	v_and_b32_e32 v83, 0xffff0000, v37
	global_load_dwordx2 v[104:105], v1, s[8:9] nt
	global_load_dwordx2 v[102:103], v1, s[10:11] nt
	global_load_dwordx2 v[100:101], v1, s[14:15] nt
	global_load_dwordx2 v[90:91], v1, s[16:17] nt
	global_load_dwordx2 v[36:37], v[32:33], off offset:1536
	global_load_dwordx2 v[98:99], v7, s[8:9] nt
	global_load_dwordx2 v[96:97], v7, s[10:11] nt
	global_load_dwordx2 v[94:95], v7, s[14:15] nt
	global_load_dwordx2 v[92:93], v7, s[16:17] nt
	global_load_dwordx2 v[66:67], v[32:33], off offset:2048
	v_and_b32_e32 v123, 0xffff0000, v120
	s_waitcnt vmcnt(0)
	v_lshlrev_b32_e32 v86, 16, v36
	v_and_b32_e32 v87, 0xffff0000, v36
	v_lshlrev_b32_e32 v88, 16, v37
	v_and_b32_e32 v89, 0xffff0000, v37
	v_ashrrev_i32_e32 v37, 31, v2
	v_mov_b32_e32 v36, v2
	v_lshlrev_b64 v[36:37], 11, v[36:37]
	v_lshl_add_u64 v[38:39], v[8:9], 0, v[36:37]
	global_load_dwordx2 v[58:59], v[38:39], off
	v_ashrrev_i32_e32 v39, 31, v3
	v_mov_b32_e32 v38, v3
	v_lshlrev_b64 v[2:3], 11, v[38:39]
	v_lshl_add_u64 v[38:39], v[8:9], 0, v[2:3]
	global_load_dwordx2 v[60:61], v[38:39], off
	v_ashrrev_i32_e32 v39, 31, v4
	v_mov_b32_e32 v38, v4
	v_lshlrev_b64 v[38:39], 11, v[38:39]
	v_lshl_add_u64 v[40:41], v[8:9], 0, v[38:39]
	global_load_dwordx2 v[62:63], v[40:41], off
	v_ashrrev_i32_e32 v41, 31, v5
	v_mov_b32_e32 v40, v5
	v_lshl_add_u64 v[2:3], s[4:5], 0, v[2:3]
	v_lshlrev_b64 v[4:5], 11, v[40:41]
	v_readfirstlane_b32 s8, v2
	v_readfirstlane_b32 s9, v3
	v_lshl_add_u64 v[2:3], s[4:5], 0, v[38:39]
	v_lshl_add_u64 v[36:37], s[4:5], 0, v[36:37]
	v_readfirstlane_b32 s10, v2
	v_readfirstlane_b32 s11, v3
	v_lshl_add_u64 v[2:3], s[4:5], 0, v[4:5]
	v_lshl_add_u64 v[40:41], v[8:9], 0, v[4:5]
	v_readfirstlane_b32 s0, v36
	v_readfirstlane_b32 s1, v37
	v_readfirstlane_b32 s14, v2
	v_readfirstlane_b32 s15, v3
	global_load_dwordx2 v[64:65], v[40:41], off
	global_load_dwordx2 v[68:69], v[32:33], off offset:2560
	global_load_dwordx2 v[52:53], v11, s[8:9] nt
	global_load_dwordx2 v[50:51], v11, s[0:1] nt
	global_load_dwordx2 v[54:55], v11, s[10:11] nt
	global_load_dwordx2 v[56:57], v11, s[14:15] nt
	global_load_dwordx2 v[70:71], v[32:33], off offset:3072
	global_load_dwordx2 v[48:49], v1, s[0:1] nt
	global_load_dwordx2 v[46:47], v1, s[8:9] nt
	global_load_dwordx2 v[44:45], v1, s[10:11] nt
	global_load_dwordx2 v[42:43], v1, s[14:15] nt
	global_load_dwordx2 v[72:73], v[32:33], off offset:3584
	global_load_dwordx2 v[40:41], v7, s[0:1] nt
	global_load_dwordx2 v[38:39], v7, s[8:9] nt
	global_load_dwordx2 v[36:37], v7, s[10:11] nt
	s_nop 0
	global_load_dwordx2 v[32:33], v7, s[14:15] nt
	s_ashr_i32 s0, s2, 31
	s_lshr_b32 s0, s0, 20
	s_add_i32 s0, s2, s0
	s_ashr_i32 s0, s0, 12
	s_cmpk_lt_i32 s2, 0x4000
	v_lshlrev_b32_e32 v2, 16, v114
	v_and_b32_e32 v3, 0xffff0000, v114
	v_lshlrev_b32_e32 v4, 16, v116
	v_and_b32_e32 v5, 0xffff0000, v116
	s_cselect_b32 s0, s0, 4
	v_pk_add_f32 v[2:3], v[2:3], v[4:5]
	v_lshlrev_b32_e32 v4, 16, v118
	v_and_b32_e32 v5, 0xffff0000, v118
	s_mul_i32 s10, s0, 0x6000
	v_pk_add_f32 v[4:5], v[4:5], v[122:123]
	s_mul_hi_i32 s3, s0, 0x6000
	s_add_u32 s8, s18, s10
	v_pk_add_f32 v[2:3], v[2:3], v[4:5]
	v_lshlrev_b32_e32 v4, 16, v115
	v_and_b32_e32 v5, 0xffff0000, v115
	v_lshlrev_b32_e32 v114, 16, v117
	v_and_b32_e32 v115, 0xffff0000, v117
	s_addc_u32 s9, s19, s3
	v_pk_add_f32 v[4:5], v[4:5], v[114:115]
	v_lshlrev_b32_e32 v114, 16, v119
	v_and_b32_e32 v115, 0xffff0000, v119
	v_lshlrev_b32_e32 v116, 16, v121
	v_and_b32_e32 v117, 0xffff0000, v121
	v_pk_add_f32 v[114:115], v[114:115], v[116:117]
	v_lshl_add_u64 v[116:117], s[8:9], 0, v[34:35]
	s_mov_b64 s[0:1], 0x5000
	v_pk_add_f32 v[4:5], v[4:5], v[114:115]
	v_lshl_add_u64 v[114:115], v[116:117], 0, s[0:1]
	v_add_co_u32_e32 v116, vcc, s28, v116
	v_readlane_b32 s8, v255, 48
	s_nop 0
	v_addc_co_u32_e32 v117, vcc, 0, v117, vcc
	global_load_dwordx4 v[116:119], v[116:117], off
	global_load_dwordx4 v[124:127], v[114:115], off offset:1024
	global_load_dwordx4 v[128:131], v[114:115], off offset:2048
	global_load_dwordx4 v[132:135], v[114:115], off offset:3072
	v_readlane_b32 s9, v255, 49
	s_mov_b64 s[0:1], -1
	s_and_b64 vcc, exec, s[8:9]
	v_lshlrev_b32_e32 v11, 2, v14
	s_waitcnt vmcnt(0)
	v_pk_fma_f32 v[74:75], v[4:5], v[118:119], v[74:75]
	v_pk_fma_f32 v[76:77], v[2:3], v[116:117], v[76:77]
	v_lshlrev_b32_e32 v2, 16, v106
	v_and_b32_e32 v3, 0xffff0000, v106
	v_lshlrev_b32_e32 v4, 16, v108
	v_and_b32_e32 v5, 0xffff0000, v108
	v_pk_add_f32 v[2:3], v[2:3], v[4:5]
	v_lshlrev_b32_e32 v4, 16, v110
	v_and_b32_e32 v5, 0xffff0000, v110
	v_lshlrev_b32_e32 v116, 16, v112
	v_and_b32_e32 v117, 0xffff0000, v112
	v_pk_add_f32 v[4:5], v[4:5], v[116:117]
	v_lshlrev_b32_e32 v106, 16, v113
	v_pk_add_f32 v[116:117], v[2:3], v[4:5]
	v_lshlrev_b32_e32 v2, 16, v107
	v_and_b32_e32 v3, 0xffff0000, v107
	v_lshlrev_b32_e32 v4, 16, v109
	v_and_b32_e32 v5, 0xffff0000, v109
	v_pk_add_f32 v[2:3], v[2:3], v[4:5]
	v_lshlrev_b32_e32 v4, 16, v111
	v_and_b32_e32 v5, 0xffff0000, v111
	v_and_b32_e32 v107, 0xffff0000, v113
	v_pk_add_f32 v[4:5], v[4:5], v[106:107]
	s_nop 0
	v_pk_add_f32 v[106:107], v[2:3], v[4:5]
	v_mov_b64_e32 v[2:3], v[124:125]
	v_mov_b64_e32 v[4:5], v[126:127]
	s_nop 0
	v_pk_fma_f32 v[78:79], v[106:107], v[4:5], v[78:79]
	v_pk_fma_f32 v[80:81], v[116:117], v[2:3], v[80:81]
	v_lshlrev_b32_e32 v2, 16, v104
	v_and_b32_e32 v3, 0xffff0000, v104
	v_lshlrev_b32_e32 v4, 16, v102
	v_and_b32_e32 v5, 0xffff0000, v102
	v_pk_add_f32 v[2:3], v[2:3], v[4:5]
	v_lshlrev_b32_e32 v4, 16, v100
	v_and_b32_e32 v5, 0xffff0000, v100
	v_lshlrev_b32_e32 v106, 16, v90
	v_and_b32_e32 v107, 0xffff0000, v90
	v_pk_add_f32 v[4:5], v[4:5], v[106:107]
	v_lshlrev_b32_e32 v90, 16, v91
	v_pk_add_f32 v[106:107], v[2:3], v[4:5]
	v_lshlrev_b32_e32 v2, 16, v105
	v_and_b32_e32 v3, 0xffff0000, v105
	v_lshlrev_b32_e32 v4, 16, v103
	v_and_b32_e32 v5, 0xffff0000, v103
	v_pk_add_f32 v[2:3], v[2:3], v[4:5]
	v_lshlrev_b32_e32 v4, 16, v101
	v_and_b32_e32 v5, 0xffff0000, v101
	v_and_b32_e32 v91, 0xffff0000, v91
	v_pk_add_f32 v[4:5], v[4:5], v[90:91]
	s_nop 0
	v_pk_add_f32 v[90:91], v[2:3], v[4:5]
	v_mov_b64_e32 v[2:3], v[128:129]
	v_mov_b64_e32 v[4:5], v[130:131]
	s_nop 0
	v_pk_fma_f32 v[82:83], v[90:91], v[4:5], v[82:83]
	v_pk_fma_f32 v[84:85], v[106:107], v[2:3], v[84:85]
	v_lshlrev_b32_e32 v2, 16, v98
	v_and_b32_e32 v3, 0xffff0000, v98
	v_lshlrev_b32_e32 v4, 16, v96
	v_and_b32_e32 v5, 0xffff0000, v96
	v_pk_add_f32 v[2:3], v[2:3], v[4:5]
	v_lshlrev_b32_e32 v4, 16, v94
	v_and_b32_e32 v5, 0xffff0000, v94
	v_lshlrev_b32_e32 v90, 16, v92
	v_and_b32_e32 v91, 0xffff0000, v92
	v_pk_add_f32 v[4:5], v[4:5], v[90:91]
	v_lshlrev_b32_e32 v92, 16, v93
	v_pk_add_f32 v[90:91], v[2:3], v[4:5]
	v_lshlrev_b32_e32 v2, 16, v99
	v_and_b32_e32 v3, 0xffff0000, v99
	v_lshlrev_b32_e32 v4, 16, v97
	v_and_b32_e32 v5, 0xffff0000, v97
	v_pk_add_f32 v[2:3], v[2:3], v[4:5]
	v_lshlrev_b32_e32 v4, 16, v95
	v_and_b32_e32 v5, 0xffff0000, v95
	v_and_b32_e32 v93, 0xffff0000, v93
	v_pk_add_f32 v[4:5], v[4:5], v[92:93]
	v_pk_mul_f32 v[96:97], v[76:77], v[76:77]
	v_pk_add_f32 v[92:93], v[2:3], v[4:5]
	v_mov_b64_e32 v[2:3], v[132:133]
	v_mov_b64_e32 v[4:5], v[134:135]
	v_pk_mul_f32 v[94:95], v[80:81], v[80:81]
	s_nop 0
	v_pk_fma_f32 v[88:89], v[92:93], v[4:5], v[88:89]
	v_pk_fma_f32 v[86:87], v[90:91], v[2:3], v[86:87]
	v_mul_f32_e32 v4, v88, v88
	v_mul_f32_e32 v92, v86, v86
	v_mul_f32_e32 v90, v87, v87
	v_mul_f32_e32 v2, v89, v89
	s_cbranch_vccz .LBB0_1733
	s_mov_b64 s[0:1], 0x178000
	v_lshl_add_u64 v[98:99], v[30:31], 0, s[0:1]
	s_mov_b64 s[0:1], 0x178200
	v_cvt_pk_bf16_f32 v106, v76, v77
	v_cvt_pk_bf16_f32 v107, v74, v75
	v_lshl_add_u64 v[100:101], v[30:31], 0, s[0:1]
	s_mov_b64 s[0:1], 0x178400
	global_store_dwordx2 v[98:99], v[106:107], off
	v_cvt_pk_bf16_f32 v98, v80, v81
	v_cvt_pk_bf16_f32 v99, v78, v79
	v_lshl_add_u64 v[102:103], v[30:31], 0, s[0:1]
	s_mov_b64 s[0:1], 0x178600
	global_store_dwordx2 v[100:101], v[98:99], off
	v_cvt_pk_bf16_f32 v98, v84, v85
	v_cvt_pk_bf16_f32 v99, v82, v83
	v_lshl_add_u64 v[104:105], v[30:31], 0, s[0:1]
	global_store_dwordx2 v[102:103], v[98:99], off
	v_cvt_pk_bf16_f32 v98, v86, v87
	v_cvt_pk_bf16_f32 v99, v88, v89
	global_store_dwordx2 v[104:105], v[98:99], off
	v_pk_mul_f32 v[98:99], v[74:75], v[74:75]
	v_mov_b32_e32 v100, v96
	v_mov_b32_e32 v101, v99
	v_pk_mov_b32 v[98:99], v[96:97], v[98:99] op_sel:[1,0]
	s_add_u32 s8, s22, s10
	v_pk_add_f32 v[98:99], v[98:99], v[100:101]
	v_mov_b32_e32 v100, v94
	v_pk_add_f32 v[110:111], v[98:99], v[98:99] op_sel_hi:[0,1]
	v_pk_mul_f32 v[98:99], v[78:79], v[78:79]
	s_addc_u32 s9, s23, s3
	v_mov_b32_e32 v101, v99
	v_pk_mov_b32 v[98:99], v[94:95], v[98:99] op_sel:[1,0]
	s_add_u32 s10, s8, 0x1000
	v_pk_add_f32 v[98:99], v[98:99], v[100:101]
	s_addc_u32 s11, s9, 0
	v_pk_add_f32 v[112:113], v[98:99], v[98:99] op_sel_hi:[0,1]
	v_mul_f32_e32 v98, v84, v84
	v_pk_fma_f32 v[114:115], v[84:85], v[84:85], v[98:99] op_sel_hi:[1,1,0]
	v_mul_f32_e32 v98, v82, v82
	v_pk_fma_f32 v[116:117], v[82:83], v[82:83], v[98:99] op_sel_hi:[1,1,0]
	global_load_dwordx4 v[98:101], v[16:17], off
	global_load_dwordx4 v[102:105], v34, s[8:9]
	global_load_dwordx4 v[106:109], v34, s[10:11]
	global_load_dwordx4 v[136:139], v[18:19], off
	global_load_dwordx4 v[140:143], v15, s[10:11]
	global_load_dwordx4 v[144:147], v34, s[8:9] offset:1024
	global_load_dwordx4 v[148:151], v[20:21], off
	global_load_dwordx4 v[152:155], v13, s[10:11]
	global_load_dwordx4 v[156:159], v34, s[8:9] offset:2048
	global_load_dwordx4 v[172:175], v[22:23], off
	global_load_dwordx4 v[176:179], v11, s[10:11]
	global_load_dwordx4 v[180:183], v34, s[8:9] offset:3072
	v_mov_b32_e32 v5, v111
	v_mov_b32_e32 v3, v113
	v_mov_b32_e32 v93, v115
	v_mov_b32_e32 v91, v117
	v_pk_add_f32 v[110:111], v[4:5], v[2:3]
	v_and_b32_e32 v5, 64, v203
	v_pk_add_f32 v[114:115], v[92:93], v[90:91]
	v_add_u32_e32 v5, 64, v5
	v_xor_b32_e32 v91, 1, v203
	v_cmp_lt_i32_e32 vcc, v91, v5
	v_pk_add_f32 v[110:111], v[114:115], v[110:111]
	s_mov_b32 s0, 0x4578000
	v_cndmask_b32_e32 v91, v203, v91, vcc
	v_add_f32_e32 v3, v110, v111
	v_lshlrev_b32_e32 v91, 2, v91
	s_nop 1
	s_waitcnt lgkmcnt(0)
	v_add_f32_dpp v3, v3, v3 quad_perm:[1,0,3,2] row_mask:0xf bank_mask:0xf
	v_xor_b32_e32 v91, 2, v203
	v_cmp_lt_i32_e32 vcc, v91, v5
	s_waitcnt vmcnt(0)
	v_pk_add_f32 v[108:109], v[108:109], 1.0 op_sel_hi:[1,0]
	v_cndmask_b32_e32 v91, v203, v91, vcc
	v_lshlrev_b32_e32 v91, 2, v91
	s_nop 1
	v_pk_add_f32 v[106:107], v[106:107], 1.0 op_sel_hi:[1,0]
	s_waitcnt lgkmcnt(0)
	v_add_f32_dpp v3, v3, v3 quad_perm:[2,3,0,1] row_mask:0xf bank_mask:0xf
	v_xor_b32_e32 v91, 4, v203
	v_cmp_lt_i32_e32 vcc, v91, v5
	s_nop 1
	v_cndmask_b32_e32 v91, v203, v91, vcc
	v_lshlrev_b32_e32 v91, 2, v91
	s_nop 1
	s_waitcnt lgkmcnt(0)
	v_add_f32_dpp v3, v3, v3 row_half_mirror row_mask:0xf bank_mask:0xf
	v_xor_b32_e32 v91, 8, v203
	v_cmp_lt_i32_e32 vcc, v91, v5
	s_nop 1
	v_cndmask_b32_e32 v91, v203, v91, vcc
	v_lshlrev_b32_e32 v91, 2, v91
	s_nop 1
	s_waitcnt lgkmcnt(0)
	v_add_f32_dpp v3, v3, v3 row_mirror row_mask:0xf bank_mask:0xf
	v_xor_b32_e32 v91, 16, v203
	v_cmp_lt_i32_e32 vcc, v91, v5
	s_nop 1
	v_cndmask_b32_e32 v91, v203, v91, vcc
	v_lshlrev_b32_e32 v91, 2, v91
	v_mov_b32_e32 v91, v3
	s_nop 1
	v_permlane16_swap_b32_e32 v91, v3
	s_waitcnt lgkmcnt(0)
	v_add_f32_e32 v3, v3, v91
	v_xor_b32_e32 v91, 32, v203
	v_cmp_lt_i32_e32 vcc, v91, v5
	s_nop 1
	v_cndmask_b32_e32 v5, v203, v91, vcc
	v_lshlrev_b32_e32 v5, 2, v5
	v_mov_b32_e32 v5, v3
	s_nop 1
	v_permlane32_swap_b32_e32 v5, v3
	s_waitcnt lgkmcnt(0)
	v_add_f32_e32 v3, v3, v5
	v_fmamk_f32 v3, v3, 0x3a800000, v165
	v_rsq_f32_e32 v110, v3
	s_nop 0
	v_pk_mul_f32 v[112:113], v[74:75], v[110:111] op_sel_hi:[1,0]
	v_pk_mul_f32 v[114:115], v[76:77], v[110:111] op_sel_hi:[1,0]
	v_pk_mul_f32 v[100:101], v[100:101], v[112:113]
	v_pk_mul_f32 v[98:99], v[98:99], v[114:115]
	v_pk_fma_f32 v[100:101], v[108:109], v[100:101], v[104:105]
	v_pk_fma_f32 v[98:99], v[106:107], v[98:99], v[102:103]
	v_add_co_u32_e32 v112, vcc, s0, v30
	v_cvt_pk_bf16_f32 v98, v98, v99
	v_cvt_pk_bf16_f32 v99, v100, v101
	v_addc_co_u32_e32 v113, vcc, 0, v31, vcc
	global_store_dwordx2 v[112:113], v[98:99], off
	v_mov_b64_e32 v[98:99], v[136:137]
	v_mov_b64_e32 v[100:101], v[138:139]
	v_mov_b64_e32 v[102:103], v[140:141]
	v_mov_b64_e32 v[104:105], v[142:143]
	v_mov_b64_e32 v[106:107], v[144:145]
	v_mov_b64_e32 v[108:109], v[146:147]
	s_nop 0
	s_nop 0
	s_nop 0
	v_pk_mul_f32 v[114:115], v[78:79], v[110:111] op_sel_hi:[1,0]
	v_pk_mul_f32 v[116:117], v[80:81], v[110:111] op_sel_hi:[1,0]
	s_mov_b64 s[0:1], 0
	s_nop 0
	v_pk_mul_f32 v[98:99], v[98:99], v[116:117]
	v_pk_mul_f32 v[100:101], v[100:101], v[114:115]
	s_nop 0
	v_pk_add_f32 v[104:105], v[104:105], 1.0 op_sel_hi:[1,0]
	v_pk_add_f32 v[102:103], v[102:103], 1.0 op_sel_hi:[1,0]
	s_nop 0
	v_pk_fma_f32 v[100:101], v[104:105], v[100:101], v[108:109]
	v_pk_fma_f32 v[98:99], v[102:103], v[98:99], v[106:107]
	v_pk_mul_f32 v[114:115], v[82:83], v[110:111] op_sel_hi:[1,0]
	v_cvt_pk_bf16_f32 v98, v98, v99
	v_cvt_pk_bf16_f32 v99, v100, v101
	global_store_dwordx2 v[112:113], v[98:99], off offset:512
	v_mov_b64_e32 v[98:99], v[148:149]
	v_mov_b64_e32 v[100:101], v[150:151]
	v_mov_b64_e32 v[102:103], v[152:153]
	v_mov_b64_e32 v[104:105], v[154:155]
	v_mov_b64_e32 v[106:107], v[156:157]
	v_mov_b64_e32 v[108:109], v[158:159]
	s_nop 0
	s_nop 0
	s_nop 0
	v_pk_mul_f32 v[116:117], v[84:85], v[110:111] op_sel_hi:[1,0]
	s_nop 0
	v_pk_mul_f32 v[100:101], v[114:115], v[100:101]
	v_pk_mul_f32 v[98:99], v[116:117], v[98:99]
	s_nop 0
	v_pk_add_f32 v[104:105], v[104:105], 1.0 op_sel_hi:[1,0]
	v_pk_add_f32 v[102:103], v[102:103], 1.0 op_sel_hi:[1,0]
	s_nop 0
	v_pk_fma_f32 v[100:101], v[100:101], v[104:105], v[108:109]
	v_pk_fma_f32 v[98:99], v[98:99], v[102:103], v[106:107]
	v_pk_mul_f32 v[114:115], v[88:89], v[110:111] op_sel_hi:[1,0]
	v_cvt_pk_bf16_f32 v98, v98, v99
	v_cvt_pk_bf16_f32 v99, v100, v101
	global_store_dwordx2 v[112:113], v[98:99], off offset:1024
	v_mov_b64_e32 v[98:99], v[172:173]
	v_mov_b64_e32 v[100:101], v[174:175]
	v_mov_b64_e32 v[102:103], v[176:177]
	v_mov_b64_e32 v[104:105], v[178:179]
	v_mov_b64_e32 v[106:107], v[180:181]
	v_mov_b64_e32 v[108:109], v[182:183]
	s_nop 0
	s_nop 0
	s_nop 0
	v_pk_mul_f32 v[110:111], v[86:87], v[110:111] op_sel_hi:[1,0]
	s_nop 0
	v_pk_mul_f32 v[100:101], v[114:115], v[100:101]
	v_pk_mul_f32 v[98:99], v[110:111], v[98:99]
	s_nop 0
	v_pk_add_f32 v[104:105], v[104:105], 1.0 op_sel_hi:[1,0]
	v_pk_add_f32 v[102:103], v[102:103], 1.0 op_sel_hi:[1,0]
	s_nop 0
	v_pk_fma_f32 v[100:101], v[100:101], v[104:105], v[108:109]
	v_pk_fma_f32 v[98:99], v[98:99], v[102:103], v[106:107]
	s_nop 0
	v_cvt_pk_bf16_f32 v98, v98, v99
	v_cvt_pk_bf16_f32 v99, v100, v101
	global_store_dwordx2 v[112:113], v[98:99], off offset:1536
.LBB0_1733:
	s_andn2_b64 vcc, exec, s[0:1]
	s_cbranch_vccnz .LBB0_1735
	v_pk_mul_f32 v[98:99], v[74:75], v[74:75]
	v_mov_b32_e32 v100, v96
	v_mov_b32_e32 v101, v99
	v_pk_mov_b32 v[96:97], v[96:97], v[98:99] op_sel:[1,0]
	v_pk_mul_f32 v[98:99], v[78:79], v[78:79]
	v_pk_add_f32 v[96:97], v[96:97], v[100:101]
	v_mov_b32_e32 v100, v94
	v_mov_b32_e32 v101, v99
	v_pk_mov_b32 v[94:95], v[94:95], v[98:99] op_sel:[1,0]
	v_pk_add_f32 v[96:97], v[96:97], v[96:97] op_sel:[0,1] op_sel_hi:[1,0]
	v_pk_add_f32 v[94:95], v[94:95], v[100:101]
	v_mov_b32_e32 v97, v92
	v_pk_add_f32 v[92:93], v[94:95], v[94:95] op_sel:[0,1] op_sel_hi:[1,0]
	s_nop 0
	v_mov_b32_e32 v93, v90
	v_pk_add_f32 v[90:91], v[96:97], v[92:93]
	v_mul_f32_e32 v92, v85, v85
	v_pk_fma_f32 v[92:93], v[84:85], v[84:85], v[92:93] op_sel_hi:[1,1,0]
	s_nop 0
	v_mov_b32_e32 v93, v4
	v_mul_f32_e32 v4, v83, v83
	v_pk_fma_f32 v[4:5], v[82:83], v[82:83], v[4:5] op_sel_hi:[1,1,0]
	s_nop 0
	v_mov_b32_e32 v5, v2
	v_pk_add_f32 v[2:3], v[92:93], v[4:5]
	v_xor_b32_e32 v4, 1, v203
	v_pk_add_f32 v[2:3], v[90:91], v[2:3]
	s_nop 0
	v_add_f32_e32 v2, v2, v3
	v_and_b32_e32 v3, 64, v203
	v_add_u32_e32 v3, 64, v3
	v_cmp_lt_i32_e32 vcc, v4, v3
	s_nop 1
	v_cndmask_b32_e32 v4, v203, v4, vcc
	v_lshlrev_b32_e32 v4, 2, v4
	s_nop 1
	s_waitcnt lgkmcnt(0)
	v_add_f32_dpp v2, v2, v2 quad_perm:[1,0,3,2] row_mask:0xf bank_mask:0xf
	v_xor_b32_e32 v4, 2, v203
	v_cmp_lt_i32_e32 vcc, v4, v3
	s_nop 1
	v_cndmask_b32_e32 v4, v203, v4, vcc
	v_lshlrev_b32_e32 v4, 2, v4
	s_nop 1
	s_waitcnt lgkmcnt(0)
	v_add_f32_dpp v2, v2, v2 quad_perm:[2,3,0,1] row_mask:0xf bank_mask:0xf
	v_xor_b32_e32 v4, 4, v203
	v_cmp_lt_i32_e32 vcc, v4, v3
	s_nop 1
	v_cndmask_b32_e32 v4, v203, v4, vcc
	v_lshlrev_b32_e32 v4, 2, v4
	s_nop 1
	s_waitcnt lgkmcnt(0)
	v_add_f32_dpp v2, v2, v2 row_half_mirror row_mask:0xf bank_mask:0xf
	v_xor_b32_e32 v4, 8, v203
	v_cmp_lt_i32_e32 vcc, v4, v3
	s_nop 1
	v_cndmask_b32_e32 v4, v203, v4, vcc
	v_lshlrev_b32_e32 v4, 2, v4
	s_nop 1
	s_waitcnt lgkmcnt(0)
	v_add_f32_dpp v2, v2, v2 row_mirror row_mask:0xf bank_mask:0xf
	v_xor_b32_e32 v4, 16, v203
	v_cmp_lt_i32_e32 vcc, v4, v3
	s_nop 1
	v_cndmask_b32_e32 v4, v203, v4, vcc
	v_lshlrev_b32_e32 v4, 2, v4
	v_mov_b32_e32 v4, v2
	s_nop 1
	v_permlane16_swap_b32_e32 v4, v2
	s_waitcnt lgkmcnt(0)
	v_add_f32_e32 v2, v2, v4
	v_xor_b32_e32 v4, 32, v203
	v_cmp_lt_i32_e32 vcc, v4, v3
	s_nop 1
	v_cndmask_b32_e32 v3, v203, v4, vcc
	v_lshlrev_b32_e32 v3, 2, v3
	v_mov_b32_e32 v3, v2
	s_nop 1
	v_permlane32_swap_b32_e32 v3, v2
	s_waitcnt lgkmcnt(0)
	v_add_f32_e32 v2, v2, v3
	v_fmamk_f32 v2, v2, 0x3a800000, v165
	v_rsq_f32_e32 v90, v2
	global_load_dwordx4 v[2:5], v[24:25], off
	v_pk_mul_f32 v[76:77], v[76:77], v[90:91] op_sel_hi:[1,0]
	v_pk_mul_f32 v[74:75], v[74:75], v[90:91] op_sel_hi:[1,0]
	s_waitcnt vmcnt(0)
	v_pk_mul_f32 v[2:3], v[2:3], v[76:77]
	v_pk_mul_f32 v[4:5], v[4:5], v[74:75]
	global_store_dwordx4 v[26:27], v[2:5], off offset:-4096
	global_load_dwordx4 v[2:5], v[24:25], off offset:1024
	v_pk_mul_f32 v[74:75], v[78:79], v[90:91] op_sel_hi:[1,0]
	v_pk_mul_f32 v[76:77], v[80:81], v[90:91] op_sel_hi:[1,0]
	s_waitcnt vmcnt(0)
	v_pk_mul_f32 v[4:5], v[4:5], v[74:75]
	v_pk_mul_f32 v[2:3], v[2:3], v[76:77]
	global_store_dwordx4 v[26:27], v[2:5], off offset:-3072
	global_load_dwordx4 v[2:5], v[24:25], off offset:2048
	v_pk_mul_f32 v[74:75], v[82:83], v[90:91] op_sel_hi:[1,0]
	v_pk_mul_f32 v[76:77], v[84:85], v[90:91] op_sel_hi:[1,0]
	s_waitcnt vmcnt(0)
	v_pk_mul_f32 v[4:5], v[4:5], v[74:75]
	v_pk_mul_f32 v[2:3], v[2:3], v[76:77]
	global_store_dwordx4 v[26:27], v[2:5], off offset:-2048
	global_load_dwordx4 v[2:5], v[24:25], off offset:3072
	v_pk_mul_f32 v[74:75], v[88:89], v[90:91] op_sel_hi:[1,0]
	v_pk_mul_f32 v[76:77], v[86:87], v[90:91] op_sel_hi:[1,0]
	s_waitcnt vmcnt(0)
	v_pk_mul_f32 v[4:5], v[4:5], v[74:75]
	v_pk_mul_f32 v[2:3], v[2:3], v[76:77]
	global_store_dwordx4 v[26:27], v[2:5], off offset:-1024
.LBB0_1735:
	s_add_i32 s0, s2, 1
	s_ashr_i32 s1, s0, 31
	s_lshr_b32 s1, s1, 20
	s_add_i32 s1, s0, s1
	s_ashr_i32 s1, s1, 12
	v_lshlrev_b32_e32 v78, 16, v66
	v_and_b32_e32 v79, 0xffff0000, v66
	v_lshlrev_b32_e32 v80, 16, v67
	v_and_b32_e32 v81, 0xffff0000, v67
	v_lshlrev_b32_e32 v74, 16, v68
	v_and_b32_e32 v75, 0xffff0000, v68
	v_lshlrev_b32_e32 v76, 16, v69
	v_and_b32_e32 v77, 0xffff0000, v69
	v_lshlrev_b32_e32 v66, 16, v72
	v_and_b32_e32 v67, 0xffff0000, v72
	v_lshlrev_b32_e32 v68, 16, v73
	v_and_b32_e32 v69, 0xffff0000, v73
	s_cmpk_lt_i32 s0, 0x4000
	v_lshlrev_b32_e32 v2, 16, v58
	v_and_b32_e32 v3, 0xffff0000, v58
	v_lshlrev_b32_e32 v72, 16, v60
	v_and_b32_e32 v73, 0xffff0000, v60
	s_cselect_b32 s0, s1, 4
	v_pk_add_f32 v[2:3], v[2:3], v[72:73]
	v_lshlrev_b32_e32 v72, 16, v62
	v_and_b32_e32 v73, 0xffff0000, v62
	v_lshlrev_b32_e32 v82, 16, v64
	v_and_b32_e32 v83, 0xffff0000, v64
	s_mul_i32 s10, s0, 0x6000
	v_pk_add_f32 v[72:73], v[72:73], v[82:83]
	s_mul_hi_i32 s3, s0, 0x6000
	s_add_u32 s8, s18, s10
	v_pk_add_f32 v[72:73], v[2:3], v[72:73]
	v_lshlrev_b32_e32 v2, 16, v59
	v_and_b32_e32 v3, 0xffff0000, v59
	v_lshlrev_b32_e32 v58, 16, v61
	v_and_b32_e32 v59, 0xffff0000, v61
	s_addc_u32 s9, s19, s3
	v_pk_add_f32 v[2:3], v[2:3], v[58:59]
	v_lshlrev_b32_e32 v58, 16, v63
	v_and_b32_e32 v59, 0xffff0000, v63
	v_lshlrev_b32_e32 v60, 16, v65
	v_and_b32_e32 v61, 0xffff0000, v65
	v_pk_add_f32 v[58:59], v[58:59], v[60:61]
	v_lshl_add_u64 v[60:61], s[8:9], 0, v[34:35]
	s_mov_b64 s[0:1], 0x5000
	v_pk_add_f32 v[58:59], v[2:3], v[58:59]
	v_lshl_add_u64 v[2:3], v[60:61], 0, s[0:1]
	v_add_co_u32_e32 v60, vcc, s28, v60
	v_lshlrev_b32_e32 v64, 16, v52
	s_nop 0
	v_addc_co_u32_e32 v61, vcc, 0, v61, vcc
	global_load_dwordx4 v[60:63], v[60:61], off
	global_load_dwordx4 v[124:127], v[2:3], off offset:1024
	global_load_dwordx4 v[128:131], v[2:3], off offset:2048
	global_load_dwordx4 v[132:135], v[2:3], off offset:3072
	v_and_b32_e32 v65, 0xffff0000, v52
	v_lshlrev_b32_e32 v52, 16, v53
	v_and_b32_e32 v53, 0xffff0000, v53
	v_lshlrev_b32_e32 v4, 16, v70
	v_and_b32_e32 v5, 0xffff0000, v70
	v_lshlrev_b32_e32 v70, 16, v71
	v_and_b32_e32 v71, 0xffff0000, v71
	v_readlane_b32 s8, v255, 48
	v_readlane_b32 s9, v255, 49
	s_mov_b64 s[0:1], -1
	s_and_b64 vcc, exec, s[8:9]
	s_waitcnt vmcnt(0)
	v_pk_fma_f32 v[58:59], v[58:59], v[62:63], v[80:81]
	v_lshlrev_b32_e32 v62, 16, v50
	v_and_b32_e32 v63, 0xffff0000, v50
	v_lshlrev_b32_e32 v50, 16, v51
	v_and_b32_e32 v51, 0xffff0000, v51
	v_pk_add_f32 v[62:63], v[62:63], v[64:65]
	v_lshlrev_b32_e32 v64, 16, v54
	v_and_b32_e32 v65, 0xffff0000, v54
	v_pk_add_f32 v[50:51], v[50:51], v[52:53]
	v_lshlrev_b32_e32 v52, 16, v55
	v_and_b32_e32 v53, 0xffff0000, v55
	v_lshlrev_b32_e32 v54, 16, v57
	v_and_b32_e32 v55, 0xffff0000, v57
	v_pk_add_f32 v[52:53], v[52:53], v[54:55]
	v_pk_fma_f32 v[60:61], v[72:73], v[60:61], v[78:79]
	v_pk_add_f32 v[50:51], v[50:51], v[52:53]
	v_mov_b64_e32 v[52:53], v[124:125]
	v_mov_b64_e32 v[54:55], v[126:127]
	v_lshlrev_b32_e32 v72, 16, v56
	v_and_b32_e32 v73, 0xffff0000, v56
	v_pk_add_f32 v[64:65], v[64:65], v[72:73]
	v_lshlrev_b32_e32 v56, 16, v46
	v_pk_add_f32 v[62:63], v[62:63], v[64:65]
	v_and_b32_e32 v57, 0xffff0000, v46
	v_lshlrev_b32_e32 v46, 16, v47
	v_and_b32_e32 v47, 0xffff0000, v47
	s_nop 0
	v_pk_fma_f32 v[50:51], v[50:51], v[54:55], v[76:77]
	v_lshlrev_b32_e32 v54, 16, v48
	v_and_b32_e32 v55, 0xffff0000, v48
	v_pk_fma_f32 v[52:53], v[62:63], v[52:53], v[74:75]
	v_pk_add_f32 v[54:55], v[54:55], v[56:57]
	v_lshlrev_b32_e32 v56, 16, v44
	v_and_b32_e32 v57, 0xffff0000, v44
	v_lshlrev_b32_e32 v62, 16, v42
	v_and_b32_e32 v63, 0xffff0000, v42
	v_lshlrev_b32_e32 v48, 16, v49
	v_and_b32_e32 v49, 0xffff0000, v49
	v_lshlrev_b32_e32 v44, 16, v45
	v_and_b32_e32 v45, 0xffff0000, v45
	v_lshlrev_b32_e32 v42, 16, v43
	v_and_b32_e32 v43, 0xffff0000, v43
	v_pk_add_f32 v[46:47], v[48:49], v[46:47]
	v_pk_add_f32 v[42:43], v[44:45], v[42:43]
	v_pk_add_f32 v[56:57], v[56:57], v[62:63]
	v_pk_add_f32 v[42:43], v[46:47], v[42:43]
	v_mov_b64_e32 v[44:45], v[128:129]
	v_mov_b64_e32 v[46:47], v[130:131]
	v_pk_add_f32 v[54:55], v[54:55], v[56:57]
	v_lshlrev_b32_e32 v48, 16, v32
	v_and_b32_e32 v49, 0xffff0000, v32
	v_lshlrev_b32_e32 v32, 16, v33
	v_and_b32_e32 v33, 0xffff0000, v33
	s_nop 0
	v_pk_fma_f32 v[42:43], v[42:43], v[46:47], v[70:71]
	v_pk_fma_f32 v[44:45], v[54:55], v[44:45], v[4:5]
	v_lshlrev_b32_e32 v4, 16, v40
	v_and_b32_e32 v5, 0xffff0000, v40
	v_lshlrev_b32_e32 v46, 16, v38
	v_and_b32_e32 v47, 0xffff0000, v38
	v_pk_add_f32 v[4:5], v[4:5], v[46:47]
	v_lshlrev_b32_e32 v46, 16, v36
	v_and_b32_e32 v47, 0xffff0000, v36
	v_pk_add_f32 v[46:47], v[46:47], v[48:49]
	v_lshlrev_b32_e32 v38, 16, v39
	v_pk_add_f32 v[46:47], v[4:5], v[46:47]
	v_lshlrev_b32_e32 v4, 16, v41
	v_and_b32_e32 v5, 0xffff0000, v41
	v_and_b32_e32 v39, 0xffff0000, v39
	v_lshlrev_b32_e32 v36, 16, v37
	v_and_b32_e32 v37, 0xffff0000, v37
	v_pk_add_f32 v[4:5], v[4:5], v[38:39]
	v_pk_add_f32 v[32:33], v[36:37], v[32:33]
	v_pk_mul_f32 v[48:49], v[60:61], v[60:61]
	v_pk_add_f32 v[32:33], v[4:5], v[32:33]
	v_mov_b64_e32 v[2:3], v[132:133]
	v_mov_b64_e32 v[4:5], v[134:135]
	s_nop 0
	v_pk_fma_f32 v[32:33], v[32:33], v[4:5], v[68:69]
	v_pk_fma_f32 v[36:37], v[46:47], v[2:3], v[66:67]
	v_mul_f32_e32 v4, v32, v32
	v_mul_f32_e32 v40, v36, v36
	v_mul_f32_e32 v38, v37, v37
	v_mul_f32_e32 v2, v33, v33
	v_pk_mul_f32 v[46:47], v[52:53], v[52:53]
	s_cbranch_vccz .LBB0_1737
	s_mov_b64 s[0:1], 0x178800
	v_lshl_add_u64 v[54:55], v[30:31], 0, s[0:1]
	s_mov_b64 s[0:1], 0x178a00
	v_cvt_pk_bf16_f32 v66, v60, v61
	v_cvt_pk_bf16_f32 v67, v58, v59
	v_lshl_add_u64 v[56:57], v[30:31], 0, s[0:1]
	s_mov_b64 s[0:1], 0x178c00
	global_store_dwordx2 v[54:55], v[66:67], off
	v_cvt_pk_bf16_f32 v54, v52, v53
	v_cvt_pk_bf16_f32 v55, v50, v51
	v_lshl_add_u64 v[62:63], v[30:31], 0, s[0:1]
	s_mov_b64 s[0:1], 0x178e00
	global_store_dwordx2 v[56:57], v[54:55], off
	v_cvt_pk_bf16_f32 v54, v44, v45
	v_cvt_pk_bf16_f32 v55, v42, v43
	v_lshl_add_u64 v[64:65], v[30:31], 0, s[0:1]
	global_store_dwordx2 v[62:63], v[54:55], off
	v_cvt_pk_bf16_f32 v54, v36, v37
	v_cvt_pk_bf16_f32 v55, v32, v33
	global_store_dwordx2 v[64:65], v[54:55], off
	v_pk_mul_f32 v[54:55], v[58:59], v[58:59]
	v_mov_b32_e32 v56, v48
	v_mov_b32_e32 v57, v55
	v_pk_mov_b32 v[54:55], v[48:49], v[54:55] op_sel:[1,0]
	s_add_u32 s8, s22, s10
	v_pk_add_f32 v[54:55], v[54:55], v[56:57]
	v_mov_b32_e32 v56, v46
	v_pk_add_f32 v[70:71], v[54:55], v[54:55] op_sel_hi:[0,1]
	v_pk_mul_f32 v[54:55], v[50:51], v[50:51]
	s_addc_u32 s9, s23, s3
	v_mov_b32_e32 v57, v55
	v_pk_mov_b32 v[54:55], v[46:47], v[54:55] op_sel:[1,0]
	s_add_u32 s10, s8, 0x1000
	v_pk_add_f32 v[54:55], v[54:55], v[56:57]
	s_addc_u32 s11, s9, 0
	v_pk_add_f32 v[72:73], v[54:55], v[54:55] op_sel_hi:[0,1]
	v_mul_f32_e32 v54, v44, v44
	v_pk_fma_f32 v[74:75], v[44:45], v[44:45], v[54:55] op_sel_hi:[1,1,0]
	v_mul_f32_e32 v54, v42, v42
	v_pk_fma_f32 v[76:77], v[42:43], v[42:43], v[54:55] op_sel_hi:[1,1,0]
	global_load_dwordx4 v[54:57], v[16:17], off
	global_load_dwordx4 v[62:65], v34, s[8:9]
	global_load_dwordx4 v[66:69], v34, s[10:11]
	global_load_dwordx4 v[136:139], v[18:19], off
	global_load_dwordx4 v[140:143], v15, s[10:11]
	global_load_dwordx4 v[144:147], v34, s[8:9] offset:1024
	global_load_dwordx4 v[148:151], v[20:21], off
	global_load_dwordx4 v[152:155], v13, s[10:11]
	global_load_dwordx4 v[156:159], v34, s[8:9] offset:2048
	global_load_dwordx4 v[172:175], v[22:23], off
	global_load_dwordx4 v[176:179], v11, s[10:11]
	global_load_dwordx4 v[180:183], v34, s[8:9] offset:3072
	v_mov_b32_e32 v5, v71
	v_mov_b32_e32 v3, v73
	v_mov_b32_e32 v41, v75
	v_mov_b32_e32 v39, v77
	v_pk_add_f32 v[70:71], v[4:5], v[2:3]
	v_and_b32_e32 v5, 64, v203
	v_pk_add_f32 v[74:75], v[40:41], v[38:39]
	v_add_u32_e32 v5, 64, v5
	v_xor_b32_e32 v39, 1, v203
	v_cmp_lt_i32_e32 vcc, v39, v5
	v_pk_add_f32 v[70:71], v[74:75], v[70:71]
	s_mov_b32 s0, 0x4578000
	v_cndmask_b32_e32 v39, v203, v39, vcc
	v_add_f32_e32 v3, v70, v71
	v_lshlrev_b32_e32 v39, 2, v39
	s_nop 1
	s_waitcnt lgkmcnt(0)
	v_add_f32_dpp v3, v3, v3 quad_perm:[1,0,3,2] row_mask:0xf bank_mask:0xf
	v_xor_b32_e32 v39, 2, v203
	v_cmp_lt_i32_e32 vcc, v39, v5
	s_waitcnt vmcnt(0)
	v_pk_add_f32 v[68:69], v[68:69], 1.0 op_sel_hi:[1,0]
	v_cndmask_b32_e32 v39, v203, v39, vcc
	v_lshlrev_b32_e32 v39, 2, v39
	s_nop 1
	v_pk_add_f32 v[66:67], v[66:67], 1.0 op_sel_hi:[1,0]
	s_waitcnt lgkmcnt(0)
	v_add_f32_dpp v3, v3, v3 quad_perm:[2,3,0,1] row_mask:0xf bank_mask:0xf
	v_xor_b32_e32 v39, 4, v203
	v_cmp_lt_i32_e32 vcc, v39, v5
	s_nop 1
	v_cndmask_b32_e32 v39, v203, v39, vcc
	v_lshlrev_b32_e32 v39, 2, v39
	s_nop 1
	s_waitcnt lgkmcnt(0)
	v_add_f32_dpp v3, v3, v3 row_half_mirror row_mask:0xf bank_mask:0xf
	v_xor_b32_e32 v39, 8, v203
	v_cmp_lt_i32_e32 vcc, v39, v5
	s_nop 1
	v_cndmask_b32_e32 v39, v203, v39, vcc
	v_lshlrev_b32_e32 v39, 2, v39
	s_nop 1
	s_waitcnt lgkmcnt(0)
	v_add_f32_dpp v3, v3, v3 row_mirror row_mask:0xf bank_mask:0xf
	v_xor_b32_e32 v39, 16, v203
	v_cmp_lt_i32_e32 vcc, v39, v5
	s_nop 1
	v_cndmask_b32_e32 v39, v203, v39, vcc
	v_lshlrev_b32_e32 v39, 2, v39
	v_mov_b32_e32 v39, v3
	s_nop 1
	v_permlane16_swap_b32_e32 v39, v3
	s_waitcnt lgkmcnt(0)
	v_add_f32_e32 v3, v3, v39
	v_xor_b32_e32 v39, 32, v203
	v_cmp_lt_i32_e32 vcc, v39, v5
	s_nop 1
	v_cndmask_b32_e32 v5, v203, v39, vcc
	v_lshlrev_b32_e32 v5, 2, v5
	v_mov_b32_e32 v5, v3
	s_nop 1
	v_permlane32_swap_b32_e32 v5, v3
	v_add_co_u32_e32 v30, vcc, s0, v30
	s_mov_b64 s[0:1], 0
	s_nop 0
	v_addc_co_u32_e32 v31, vcc, 0, v31, vcc
	s_waitcnt lgkmcnt(0)
	v_add_f32_e32 v3, v3, v5
	v_fmamk_f32 v3, v3, 0x3a800000, v165
	v_rsq_f32_e32 v70, v3
	s_nop 0
	v_pk_mul_f32 v[72:73], v[58:59], v[70:71] op_sel_hi:[1,0]
	v_pk_mul_f32 v[74:75], v[60:61], v[70:71] op_sel_hi:[1,0]
	v_pk_mul_f32 v[56:57], v[56:57], v[72:73]
	v_pk_mul_f32 v[54:55], v[54:55], v[74:75]
	v_pk_fma_f32 v[56:57], v[68:69], v[56:57], v[64:65]
	v_pk_fma_f32 v[54:55], v[66:67], v[54:55], v[62:63]
	v_pk_mul_f32 v[72:73], v[50:51], v[70:71] op_sel_hi:[1,0]
	v_cvt_pk_bf16_f32 v54, v54, v55
	v_cvt_pk_bf16_f32 v55, v56, v57
	global_store_dwordx2 v[30:31], v[54:55], off offset:2048
	v_mov_b64_e32 v[54:55], v[136:137]
	v_mov_b64_e32 v[56:57], v[138:139]
	v_mov_b64_e32 v[62:63], v[140:141]
	v_mov_b64_e32 v[64:65], v[142:143]
	v_mov_b64_e32 v[66:67], v[144:145]
	v_mov_b64_e32 v[68:69], v[146:147]
	s_nop 0
	s_nop 0
	s_nop 0
	v_pk_mul_f32 v[74:75], v[52:53], v[70:71] op_sel_hi:[1,0]
	s_nop 0
	v_pk_mul_f32 v[56:57], v[56:57], v[72:73]
	v_pk_mul_f32 v[54:55], v[54:55], v[74:75]
	s_nop 0
	v_pk_add_f32 v[64:65], v[64:65], 1.0 op_sel_hi:[1,0]
	v_pk_add_f32 v[62:63], v[62:63], 1.0 op_sel_hi:[1,0]
	s_nop 0
	v_pk_fma_f32 v[56:57], v[64:65], v[56:57], v[68:69]
	v_pk_fma_f32 v[54:55], v[62:63], v[54:55], v[66:67]
	v_pk_mul_f32 v[72:73], v[42:43], v[70:71] op_sel_hi:[1,0]
	v_cvt_pk_bf16_f32 v54, v54, v55
	v_cvt_pk_bf16_f32 v55, v56, v57
	global_store_dwordx2 v[30:31], v[54:55], off offset:2560
	v_mov_b64_e32 v[54:55], v[148:149]
	v_mov_b64_e32 v[56:57], v[150:151]
	v_mov_b64_e32 v[62:63], v[152:153]
	v_mov_b64_e32 v[64:65], v[154:155]
	v_mov_b64_e32 v[66:67], v[156:157]
	v_mov_b64_e32 v[68:69], v[158:159]
	s_nop 0
	s_nop 0
	s_nop 0
	v_pk_mul_f32 v[74:75], v[44:45], v[70:71] op_sel_hi:[1,0]
	s_nop 0
	v_pk_mul_f32 v[56:57], v[72:73], v[56:57]
	v_pk_mul_f32 v[54:55], v[74:75], v[54:55]
	s_nop 0
	v_pk_add_f32 v[64:65], v[64:65], 1.0 op_sel_hi:[1,0]
	v_pk_add_f32 v[62:63], v[62:63], 1.0 op_sel_hi:[1,0]
	s_nop 0
	v_pk_fma_f32 v[56:57], v[56:57], v[64:65], v[68:69]
	v_pk_fma_f32 v[54:55], v[54:55], v[62:63], v[66:67]
	v_pk_mul_f32 v[72:73], v[32:33], v[70:71] op_sel_hi:[1,0]
	v_cvt_pk_bf16_f32 v54, v54, v55
	v_cvt_pk_bf16_f32 v55, v56, v57
	global_store_dwordx2 v[30:31], v[54:55], off offset:3072
	v_mov_b64_e32 v[54:55], v[172:173]
	v_mov_b64_e32 v[56:57], v[174:175]
	v_mov_b64_e32 v[62:63], v[176:177]
	v_mov_b64_e32 v[64:65], v[178:179]
	v_mov_b64_e32 v[66:67], v[180:181]
	v_mov_b64_e32 v[68:69], v[182:183]
	s_nop 0
	s_nop 0
	s_nop 0
	v_pk_mul_f32 v[70:71], v[36:37], v[70:71] op_sel_hi:[1,0]
	s_nop 0
	v_pk_mul_f32 v[56:57], v[72:73], v[56:57]
	v_pk_mul_f32 v[54:55], v[70:71], v[54:55]
	s_nop 0
	v_pk_add_f32 v[64:65], v[64:65], 1.0 op_sel_hi:[1,0]
	v_pk_add_f32 v[62:63], v[62:63], 1.0 op_sel_hi:[1,0]
	s_nop 0
	v_pk_fma_f32 v[56:57], v[56:57], v[64:65], v[68:69]
	v_pk_fma_f32 v[54:55], v[54:55], v[62:63], v[66:67]
	s_nop 0
	v_cvt_pk_bf16_f32 v54, v54, v55
	v_cvt_pk_bf16_f32 v55, v56, v57
	global_store_dwordx2 v[30:31], v[54:55], off offset:3584
.LBB0_1737:
	s_andn2_b64 vcc, exec, s[0:1]
	s_cbranch_vccnz .LBB0_1730
	v_pk_mul_f32 v[30:31], v[58:59], v[58:59]
	v_mov_b32_e32 v54, v48
	v_mov_b32_e32 v55, v31
	v_pk_mov_b32 v[30:31], v[48:49], v[30:31] op_sel:[1,0]
	v_pk_mul_f32 v[48:49], v[50:51], v[50:51]
	v_pk_add_f32 v[30:31], v[30:31], v[54:55]
	v_mov_b32_e32 v54, v46
	v_mov_b32_e32 v55, v49
	v_pk_mov_b32 v[46:47], v[46:47], v[48:49] op_sel:[1,0]
	v_pk_add_f32 v[30:31], v[30:31], v[30:31] op_sel:[0,1] op_sel_hi:[1,0]
	v_pk_add_f32 v[46:47], v[46:47], v[54:55]
	v_mov_b32_e32 v31, v40
	v_pk_add_f32 v[40:41], v[46:47], v[46:47] op_sel:[0,1] op_sel_hi:[1,0]
	v_mul_f32_e32 v34, v45, v45
	v_mov_b32_e32 v41, v38
	v_pk_fma_f32 v[38:39], v[44:45], v[44:45], v[34:35] op_sel_hi:[1,1,0]
	v_pk_add_f32 v[30:31], v[30:31], v[40:41]
	v_mov_b32_e32 v39, v4
	v_mul_f32_e32 v4, v43, v43
	v_pk_fma_f32 v[4:5], v[42:43], v[42:43], v[4:5] op_sel_hi:[1,1,0]
	s_nop 0
	v_mov_b32_e32 v5, v2
	v_pk_add_f32 v[2:3], v[38:39], v[4:5]
	v_xor_b32_e32 v4, 1, v203
	v_pk_add_f32 v[2:3], v[30:31], v[2:3]
	s_nop 0
	v_add_f32_e32 v2, v2, v3
	v_and_b32_e32 v3, 64, v203
	v_add_u32_e32 v3, 64, v3
	v_cmp_lt_i32_e32 vcc, v4, v3
	s_nop 1
	v_cndmask_b32_e32 v4, v203, v4, vcc
	v_lshlrev_b32_e32 v4, 2, v4
	s_nop 1
	s_waitcnt lgkmcnt(0)
	v_add_f32_dpp v2, v2, v2 quad_perm:[1,0,3,2] row_mask:0xf bank_mask:0xf
	v_xor_b32_e32 v4, 2, v203
	v_cmp_lt_i32_e32 vcc, v4, v3
	s_nop 1
	v_cndmask_b32_e32 v4, v203, v4, vcc
	v_lshlrev_b32_e32 v4, 2, v4
	s_nop 1
	s_waitcnt lgkmcnt(0)
	v_add_f32_dpp v2, v2, v2 quad_perm:[2,3,0,1] row_mask:0xf bank_mask:0xf
	v_xor_b32_e32 v4, 4, v203
	v_cmp_lt_i32_e32 vcc, v4, v3
	s_nop 1
	v_cndmask_b32_e32 v4, v203, v4, vcc
	v_lshlrev_b32_e32 v4, 2, v4
	s_nop 1
	s_waitcnt lgkmcnt(0)
	v_add_f32_dpp v2, v2, v2 row_half_mirror row_mask:0xf bank_mask:0xf
	v_xor_b32_e32 v4, 8, v203
	v_cmp_lt_i32_e32 vcc, v4, v3
	s_nop 1
	v_cndmask_b32_e32 v4, v203, v4, vcc
	v_lshlrev_b32_e32 v4, 2, v4
	s_nop 1
	s_waitcnt lgkmcnt(0)
	v_add_f32_dpp v2, v2, v2 row_mirror row_mask:0xf bank_mask:0xf
	v_xor_b32_e32 v4, 16, v203
	v_cmp_lt_i32_e32 vcc, v4, v3
	s_nop 1
	v_cndmask_b32_e32 v4, v203, v4, vcc
	v_lshlrev_b32_e32 v4, 2, v4
	v_mov_b32_e32 v4, v2
	s_nop 1
	v_permlane16_swap_b32_e32 v4, v2
	s_waitcnt lgkmcnt(0)
	v_add_f32_e32 v2, v2, v4
	v_xor_b32_e32 v4, 32, v203
	v_cmp_lt_i32_e32 vcc, v4, v3
	s_nop 1
	v_cndmask_b32_e32 v3, v203, v4, vcc
	v_lshlrev_b32_e32 v3, 2, v3
	v_mov_b32_e32 v3, v2
	s_nop 1
	v_permlane32_swap_b32_e32 v3, v2
	s_waitcnt lgkmcnt(0)
	v_add_f32_e32 v2, v2, v3
	v_fmamk_f32 v2, v2, 0x3a800000, v165
	v_rsq_f32_e32 v30, v2
	global_load_dwordx4 v[2:5], v[24:25], off
	v_pk_mul_f32 v[38:39], v[60:61], v[30:31] op_sel_hi:[1,0]
	v_pk_mul_f32 v[40:41], v[58:59], v[30:31] op_sel_hi:[1,0]
	v_pk_mul_f32 v[32:33], v[32:33], v[30:31] op_sel_hi:[1,0]
	s_waitcnt vmcnt(0)
	v_pk_mul_f32 v[4:5], v[4:5], v[40:41]
	v_pk_mul_f32 v[2:3], v[2:3], v[38:39]
	global_store_dwordx4 v[26:27], v[2:5], off
	global_load_dwordx4 v[2:5], v[24:25], off offset:1024
	v_pk_mul_f32 v[38:39], v[50:51], v[30:31] op_sel_hi:[1,0]
	v_pk_mul_f32 v[40:41], v[52:53], v[30:31] op_sel_hi:[1,0]
	s_waitcnt vmcnt(0)
	v_pk_mul_f32 v[4:5], v[4:5], v[38:39]
	v_pk_mul_f32 v[2:3], v[2:3], v[40:41]
	global_store_dwordx4 v[26:27], v[2:5], off offset:1024
	global_load_dwordx4 v[2:5], v[24:25], off offset:2048
	v_pk_mul_f32 v[38:39], v[42:43], v[30:31] op_sel_hi:[1,0]
	v_pk_mul_f32 v[40:41], v[44:45], v[30:31] op_sel_hi:[1,0]
	v_pk_mul_f32 v[30:31], v[36:37], v[30:31] op_sel_hi:[1,0]
	s_waitcnt vmcnt(0)
	v_pk_mul_f32 v[2:3], v[2:3], v[40:41]
	v_pk_mul_f32 v[4:5], v[4:5], v[38:39]
	global_store_dwordx4 v[26:27], v[2:5], off offset:2048
	global_load_dwordx4 v[2:5], v[24:25], off offset:3072
	s_waitcnt vmcnt(0)
	v_pk_mul_f32 v[2:3], v[2:3], v[30:31]
	v_pk_mul_f32 v[4:5], v[4:5], v[32:33]
	global_store_dwordx4 v[26:27], v[2:5], off offset:3072
	s_branch .LBB0_1730
